# scan unit loops: dropped loop-header waits on next-unit prefetch loads, gla_w2 pack deferred to loop bottom
# baseline (speedup 1.0000x reference)
; DEVI int opaque_tid() { int t = threadIdx.x; asm volatile("" : "+v"(t)); return t; }
; DEVI int chunk_row0(int b, int c) { return (c < 4) ? (NLAT + b * CL + c * 64) : (b * SEQ + (c - 4) * 64); }
; DEVI void gla_load(const Params& p, int l, int b, int h, int c, bool need_qg, GlaIn& in) {
;     const bf16_t* P = (const bf16_t*)(p.ws + WS_P);
;     const int tid = opaque_tid(), wid = tid >> 6, lane = tid & 63, fr = lane & 15, fq = lane >> 4, d = wid >> 2, kf = wid & 3, kk = kf * 16 + fr;
;     const int row0 = chunk_row0(b, c), tk = tid >> 3, c8 = (tid & 7) * 8;
;     in.k = *(const bf16x8*)(P + (size_t)(row0 + tk) * INC + C_GK + h * 64 + c8);
;     in.v0 = *(const bf16x8*)(P + (size_t)(row0 + tk) * INC + C_GV + h * 128 + c8);
;     in.v1 = *(const bf16x8*)(P + (size_t)(row0 + tk) * INC + C_GV + h * 128 + 64 + c8);
;     if (need_qg) {
;         in.q = *(const bf16x8*)(P + (size_t)(row0 + tk) * INC + C_GQ + h * 64 + c8);
;         in.g0 = *(const bf16x8*)(P + (size_t)(row0 + tk) * INC + C_GOG + h * 128 + (tid & 7) * 16);
;         in.g1 = *(const bf16x8*)(P + (size_t)(row0 + tk) * INC + C_GOG + h * 128 + (tid & 7) * 16 + 8);
;     }
;     const bf16x8 zero = {0, 0, 0, 0, 0, 0, 0, 0};
;     in.z0 = zero; in.z1 = zero; in.z2 = zero; in.z3 = zero; in.bw = zero;
;     if (fq < 2) {
;         const bf16_t* zp = P + (size_t)(row0 + fr) * INC + C_GZ + d * 16 + fq * 8;
;         in.z0 = *(const bf16x8*)(zp); in.z1 = *(const bf16x8*)(zp + (size_t)16 * INC); in.z2 = *(const bf16x8*)(zp + (size_t)32 * INC); in.z3 = *(const bf16x8*)(zp + (size_t)48 * INC);
;         float wv[8];
; #pragma unroll
;         for (int j = 0; j < 8; ++j) wv[j] = p.gla_w2[((size_t)(l * 2 + d) * 16 + fq * 8 + j) * 256 + h * 64 + kk];
;         in.bw = pack8(wv);
;     }
;     in.bias = p.gla_b[(size_t)(l * 2 + d) * 256 + h * 64 + kk];
; DEVI void phase_l2(const Params& p, int l, char* smem) {
;     ...
;         {   GlaIn cur; bool have = u < nG;
;             if (have) gla_load(p, l, (u / NCH) >> 2, (u / NCH) & 3, u % NCH, false, cur);
;             while (have) { const int un = u + G; const bool hn = un < nG; GlaIn nxt;
;                 if (hn) gla_load(p, l, (un / NCH) >> 2, (un / NCH) & 3, un % NCH, false, nxt);
.LBB0_494:
	s_or_b64 exec, exec, s[16:17]
	s_load_dwordx4 s[16:19], s[0:1], 0x58
	v_lshlrev_b64 v[4:5], 10, v[8:9]
	v_lshlrev_b32_e32 v2, 2, v6
	s_lshl_b32 s52, s4, 2
	v_readlane_b32 s4, v254, 49
	s_waitcnt lgkmcnt(0)
	v_lshl_add_u64 v[4:5], s[18:19], 0, v[4:5]
	v_lshl_add_u64 v[4:5], v[4:5], 0, v[2:3]
	v_lshl_add_u64 v[4:5], v[4:5], 0, s[52:53]
	global_load_dword v98, v[4:5], off
	v_readlane_b32 s5, v254, 50
	s_and_b64 s[4:5], s[4:5], exec
	s_movk_i32 s4, 0x2700
	s_cselect_b32 s15, s4, 0x2780
	v_readlane_b32 s4, v254, 61
	s_lshl_b32 s18, s4, 4
	s_add_i32 s4, s63, s14
	s_sub_i32 s19, 0, s14
	s_lshl_b32 s23, s4, 6
	s_lshl_b32 s24, s63, 6
	s_mov_b32 s6, s14
	v_readlane_b32 s5, v254, 62
	s_waitcnt vmcnt(0)
.LBB0_495:
	s_add_i32 s14, s6, s63
	s_cmpk_gt_i32 s14, 0x23f
	s_cselect_b64 s[40:41], -1, 0
	s_and_b64 vcc, exec, s[40:41]
	s_cbranch_vccnz .LBB0_501
	s_mul_hi_i32 s4, s14, 0x38e38e39
	s_lshr_b32 s5, s4, 31
	s_ashr_i32 s4, s4, 3
	s_add_i32 s7, s4, s5
	s_mul_i32 s16, s7, 0xffffffdc
	s_ashr_i32 s5, s7, 2
	s_and_b32 s4, s7, 3
	s_add_i32 s16, s14, s16
	s_cmp_lt_i32 s16, 4
	s_cselect_b32 s16, 8, 11
	s_movk_i32 s17, 0xff00
	v_mov_b32_e32 v18, v0
	s_cselect_b32 s17, 0x2000, s17
	s_lshl_b32 s5, s5, s16
	s_add_i32 s5, s5, s17
	v_ashrrev_i32_e32 v2, 3, v18
	v_add_u32_e32 v2, s5, v2
	s_mulk_i32 s7, 0x900
	v_subrev_u32_e32 v2, s7, v2
	v_add_u32_e32 v2, s23, v2
	v_mov_b64_e32 v[4:5], s[86:87]
	v_mad_i64_i32 v[4:5], s[16:17], v2, s93, v[4:5]
	s_lshl_b32 s52, s4, 7
	v_lshlrev_b32_e32 v2, 4, v18
	v_lshl_add_u64 v[6:7], v[4:5], 0, s[52:53]
	v_and_b32_e32 v2, 0x70, v2
	s_lshl_b32 s52, s4, 8
	v_lshl_add_u64 v[6:7], v[6:7], 0, v[2:3]
	v_lshl_add_u64 v[4:5], v[4:5], 0, s[52:53]
	v_lshl_add_u64 v[4:5], v[4:5], 0, v[2:3]
	global_load_dwordx4 v[6:9], v[6:7], off offset:2176
	s_nop 0
	global_load_dwordx4 v[10:13], v[4:5], off offset:2688
	global_load_dwordx4 v[14:17], v[4:5], off offset:2816
	v_and_b32_e32 v43, 15, v18
	v_bfe_u32 v39, v18, 4, 2
	v_lshrrev_b32_e32 v2, 2, v18
	v_ashrrev_i32_e32 v42, 8, v18
	v_and_or_b32 v38, v2, 48, v43
	v_cmp_lt_u32_e32 vcc, 1, v39
	s_and_saveexec_b64 s[16:17], vcc
	s_xor_b64 s[16:17], exec, s[16:17]
	v_add_u32_e32 v40, v42, v1
	v_ashrrev_i32_e32 v41, 31, v40
	s_or_saveexec_b64 s[16:17], s[16:17]
	v_mov_b32_e32 v4, v3
	v_mov_b32_e32 v5, v3
	v_mov_b32_e32 v20, v3
	v_mov_b32_e32 v21, v3
	v_mov_b32_e32 v2, v3
	v_mov_b32_e32 v18, v3
	v_mov_b32_e32 v19, v3
	v_mov_b64_e32 v[24:25], v[20:21]
	v_mov_b64_e32 v[28:29], v[20:21]
	v_mov_b64_e32 v[32:33], v[20:21]
	v_mov_b64_e32 v[36:37], v[4:5]
	s_lshl_b32 s4, s4, 6
	v_mov_b64_e32 v[22:23], v[18:19]
	v_mov_b64_e32 v[26:27], v[18:19]
	v_mov_b64_e32 v[30:31], v[18:19]
	v_mov_b64_e32 v[34:35], v[2:3]
	s_xor_b64 exec, exec, s[16:17]
	s_cbranch_execz .LBB0_500
	v_add_u32_e32 v2, s5, v43
	v_subrev_u32_e32 v2, s7, v2
	v_add_u32_e32 v2, s23, v2
	v_mov_b64_e32 v[4:5], s[86:87]
	v_lshlrev_b32_e32 v18, 4, v42
	v_mad_i64_i32 v[4:5], s[28:29], v2, s93, v[4:5]
	v_ashrrev_i32_e32 v19, 31, v18
	v_lshl_add_u64 v[4:5], v[18:19], 1, v[4:5]
	v_lshlrev_b32_e32 v2, 4, v39
	v_lshl_add_u64 v[4:5], v[4:5], 0, v[2:3]
	v_add_co_u32_e32 v18, vcc, 0x23000, v4
	v_add_u32_e32 v40, v42, v1
	s_nop 0
	v_addc_co_u32_e32 v19, vcc, 0, v5, vcc
	global_load_dwordx4 v[22:25], v[4:5], off offset:3712
	s_nop 0
	global_load_dwordx4 v[18:21], v[18:19], off offset:2688
	s_load_dwordx4 s[44:47], s[0:1], 0x58
	v_lshlrev_b32_e32 v2, 2, v38
	v_add_co_u32_e32 v26, vcc, 0x46000, v4
	v_ashrrev_i32_e32 v41, 31, v40
	s_waitcnt lgkmcnt(0)
	v_lshl_add_u64 v[28:29], s[44:45], 0, v[2:3]
	s_lshl_b32 s52, s4, 2
	v_addc_co_u32_e32 v27, vcc, 0, v5, vcc
	v_lshl_add_u64 v[28:29], v[28:29], 0, s[52:53]
	v_lshlrev_b64 v[30:31], 14, v[40:41]
	v_add_co_u32_e32 v4, vcc, 0x69000, v4
	v_lshlrev_b32_e32 v2, 13, v39
	v_lshl_add_u64 v[28:29], v[28:29], 0, v[30:31]
	v_addc_co_u32_e32 v5, vcc, 0, v5, vcc
	v_lshl_add_u64 v[28:29], v[28:29], 0, v[2:3]
	s_movk_i32 s5, 0x1000
	v_add_co_u32_e32 v30, vcc, s5, v28
	s_nop 1
	v_addc_co_u32_e32 v31, vcc, 0, v29, vcc
	global_load_dword v156, v[28:29], off
	global_load_dword v157, v[28:29], off offset:1024
	global_load_dword v158, v[28:29], off offset:2048
	global_load_dword v159, v[28:29], off offset:3072
	global_load_dword v160, v[30:31], off
	global_load_dword v161, v[30:31], off offset:1024
	global_load_dword v162, v[30:31], off offset:2048
	global_load_dword v163, v[30:31], off offset:3072
	s_nop 0
	global_load_dwordx4 v[26:29], v[26:27], off offset:1664
	s_nop 0
	global_load_dwordx4 v[30:33], v[4:5], off offset:640

; DEVI int opaque_tid() { int t = threadIdx.x; asm volatile("" : "+v"(t)); return t; }
; DEVI float log_sigmoid_f(float x) { return fminf(x, 0.f) - __logf(1.f + __expf(-fabsf(x))); }
; DEVI void cvt8_load(const Params& p, int L, int t, CvtIn& in) {
;     const int which = t / 4096, r = t % 4096, le = L * 16 + r / 256, kt = (r % 256) / 16, nt = r % 16;
;     const float* src = (which == 2 ? p.w_down : (which == 0 ? p.w_gate : p.w_up)) + (size_t)le * 2048 * 2048;
;     const int tid = opaque_tid(), nq = tid & 31, kq0 = tid >> 5;
; #pragma unroll
;     for (int it = 0; it < 2; ++it)
; #pragma unroll
;         for (int kk = 0; kk < 4; ++kk) in.v[it * 4 + kk] = __builtin_nontemporal_load((const f32x4*)(src + (size_t)(kt * 128 + (kq0 + it * 16) * 4 + kk) * 2048 + nt * 128 + nq * 4));
; }
; DEVI void gla_cum(const GlaIn& in, float* cum) {
;     const int tid = opaque_tid(), wid = tid >> 6, lane = tid & 63, fr = lane & 15, fq = lane >> 4, d = wid >> 2, kf = wid & 3;
;     const int kk = kf * 16 + fr;
;     float la[4][4];
; #pragma unroll
;     for (int f = 0; f < 4; ++f) {
;         const bf16x8 az = (f == 0) ? in.z0 : (f == 1) ? in.z1 : (f == 2) ? in.z2 : in.z3;
;         f32x4 acc = {0.f, 0.f, 0.f, 0.f};
;         acc = __builtin_amdgcn_mfma_f32_16x16x32_bf16(az, in.bw, acc, 0, 0, 0);
; #pragma unroll
;         for (int r = 0; r < 4; ++r) la[f][r] = log_sigmoid_f(acc[r] + in.bias) * (1.f / 16.f);
;     }
.LBB0_501:
	s_add_i32 s7, s15, s6
	s_and_b32 s4, s7, 0xfffff000
	s_add_i32 s5, s7, 0xfff
	s_cmpk_lt_u32 s5, 0x1fff
	s_cselect_b32 s16, s64, 0x80
	s_cmpk_lg_i32 s4, 0x2000
	s_cselect_b64 s[44:45], -1, 0
	s_and_b64 s[4:5], s[44:45], exec
	s_cselect_b32 s4, s16, 0x88
	s_add_u32 s4, s0, s4
	s_addc_u32 s5, s1, 0
	s_ashr_i32 s16, s7, 31
	s_lshr_b32 s16, s16, 20
	s_add_i32 s34, s7, s16
	s_and_b32 s16, s34, 0xf000
	s_sub_i32 s7, s7, s16
	s_sext_i32_i16 s16, s7
	s_lshr_b32 s16, s16, 15
	s_bfe_u32 s17, s16, 0x4000c
	s_add_i32 s17, s7, s17
	s_and_b32 s17, s17, 0xfff0
	s_bfe_u32 s16, s16, 0x80008
	s_sub_i32 s17, s7, s17
	s_add_i32 s16, s7, s16
	s_sext_i32_i16 s33, s17
	s_sext_i32_i16 s17, s16
	s_and_b32 s16, s16, 0xff00
	s_sub_i32 s7, s7, s16
	s_sext_i32_i16 s16, s7
	s_bfe_u32 s16, s16, 0x4001b
	s_load_dwordx2 s[4:5], s[4:5], 0x0
	s_add_i32 s7, s7, s16
	s_ashr_i32 s16, s17, 8
	s_add_i32 s42, s18, s16
	s_ashr_i32 s43, s42, 31
	s_lshl_b64 s[16:17], s[42:43], 24
	s_sext_i32_i16 s7, s7
	s_waitcnt lgkmcnt(0)
	s_add_u32 s16, s4, s16
	s_addc_u32 s17, s5, s17
	s_lshl_b32 s4, s7, 3
	v_mov_b32_e32 v2, v0
	s_and_b32 s25, s4, 0xffffff80
	s_lshl_b32 s4, s33, 7
	s_ashr_i32 s5, s4, 31
	v_ashrrev_i32_e32 v4, 3, v2
	v_and_b32_e32 v4, -4, v4
	s_lshl_b64 s[4:5], s[4:5], 2
	v_add_u32_e32 v4, s25, v4
	s_add_u32 s4, s16, s4
	v_lshlrev_b32_e32 v2, 4, v2
	s_addc_u32 s5, s17, s5
	v_and_b32_e32 v2, 0x1f0, v2
	v_ashrrev_i32_e32 v5, 31, v4
	v_lshl_add_u64 v[38:39], s[4:5], 0, v[2:3]
	v_lshlrev_b64 v[40:41], 13, v[4:5]
	v_lshl_add_u64 v[58:59], v[38:39], 0, v[40:41]
	v_or_b32_e32 v40, 1, v4
	v_ashrrev_i32_e32 v41, 31, v40
	v_lshlrev_b64 v[40:41], 13, v[40:41]
	v_lshl_add_u64 v[40:41], v[38:39], 0, v[40:41]
	global_load_dwordx4 v[46:49], v[58:59], off nt
	global_load_dwordx4 v[50:53], v[40:41], off nt
	v_or_b32_e32 v40, 2, v4
	v_or_b32_e32 v4, 3, v4
	v_ashrrev_i32_e32 v41, 31, v40
	v_ashrrev_i32_e32 v5, 31, v4
	v_mfma_f32_16x16x32_bf16 v[100:103], v[54:57], v[86:89], 0
	v_lshlrev_b64 v[40:41], 13, v[40:41]
	v_lshlrev_b64 v[4:5], 13, v[4:5]
	v_lshl_add_u64 v[40:41], v[38:39], 0, v[40:41]
	v_lshl_add_u64 v[4:5], v[38:39], 0, v[4:5]
	global_load_dwordx4 v[62:65], v[40:41], off nt
	global_load_dwordx4 v[66:69], v[4:5], off nt
	v_add_co_u32_e32 v4, vcc, s94, v58
	s_mov_b32 s4, 0x82000
	s_nop 0
	v_addc_co_u32_e32 v5, vcc, 0, v59, vcc
	v_add_f32_e32 v99, v98, v100
	v_add_co_u32_e32 v42, vcc, s4, v58
	v_mul_f32_e64 v2, |v99|, s48
	s_nop 0
	v_addc_co_u32_e32 v43, vcc, 0, v59, vcc
	s_mov_b32 s4, 0x84000
	v_exp_f32_e32 v2, v2
	global_load_dwordx4 v[38:41], v[4:5], off nt
	s_nop 0
	global_load_dwordx4 v[42:45], v[42:43], off nt
	v_add_co_u32_e32 v4, vcc, s4, v58
	s_mov_b32 s4, 0x86000
	s_nop 0
	v_addc_co_u32_e32 v5, vcc, 0, v59, vcc
	v_add_co_u32_e32 v58, vcc, s4, v58
	v_add_f32_e32 v2, 1.0, v2
	s_nop 0
	v_addc_co_u32_e32 v59, vcc, 0, v59, vcc
	v_cmp_gt_f32_e32 vcc, s97, v2
	global_load_dwordx4 v[54:57], v[4:5], off nt
	s_nop 0
	global_load_dwordx4 v[58:61], v[58:59], off nt
	v_cndmask_b32_e64 v4, 0, 32, vcc
	v_ldexp_f32 v2, v2, v4
	v_log_f32_e32 v4, v2
	v_add_f32_e32 v100, v98, v101
	v_min_f32_e32 v5, 0, v99
	v_mul_f32_e64 v101, |v100|, s48
	v_mul_f32_e32 v99, 0x3f317217, v4
	v_fma_f32 v99, v4, s49, -v99
	v_exp_f32_e32 v101, v101
	v_fmac_f32_e32 v99, 0x3377d1cf, v4
	v_fmac_f32_e32 v99, 0x3f317217, v4
	v_cmp_lt_f32_e64 s[38:39], |v4|, s22
	v_mfma_f32_16x16x32_bf16 v[90:93], v[90:93], v[86:89], 0
	v_mov_b32_e32 v117, v0
	v_cndmask_b32_e64 v4, v4, v99, s[38:39]
	v_cndmask_b32_e32 v99, 0, v230, vcc
	v_sub_f32_e32 v4, v4, v99
	v_add_f32_e32 v99, 1.0, v101
	v_cmp_gt_f32_e32 vcc, s97, v99
	v_sub_f32_e32 v4, v5, v4
	v_mul_f32_e32 v5, 0x3d800000, v4
	v_cndmask_b32_e64 v101, 0, 32, vcc
	v_ldexp_f32 v99, v99, v101
	v_log_f32_e32 v99, v99
	v_add_f32_e32 v101, v98, v102
	v_min_f32_e32 v4, 0, v100
	v_mul_f32_e64 v102, |v101|, s48
	v_mul_f32_e32 v100, 0x3f317217, v99
	v_fma_f32 v100, v99, s49, -v100
	v_exp_f32_e32 v102, v102
	v_fmac_f32_e32 v100, 0x3377d1cf, v99
	v_fmac_f32_e32 v100, 0x3f317217, v99
	v_cmp_lt_f32_e64 s[38:39], |v99|, s22
	v_add_f32_e32 v93, v98, v93
	v_mov_b32_e32 v2, v0
	v_cndmask_b32_e64 v99, v99, v100, s[38:39]
	v_cndmask_b32_e32 v100, 0, v230, vcc
	v_sub_f32_e32 v99, v99, v100
	v_add_f32_e32 v100, 1.0, v102
	v_cmp_gt_f32_e32 vcc, s97, v100
	v_sub_f32_e32 v4, v4, v99
	v_mul_f32_e32 v99, 0x3d800000, v4
	v_cndmask_b32_e64 v102, 0, 32, vcc
	v_ldexp_f32 v100, v100, v102
	v_log_f32_e32 v100, v100
	v_add_f32_e32 v102, v98, v103
	v_min_f32_e32 v4, 0, v101
	v_mul_f32_e64 v103, |v102|, s48
	v_mul_f32_e32 v101, 0x3f317217, v100
	v_fma_f32 v101, v100, s49, -v101
	v_exp_f32_e32 v103, v103
	v_fmac_f32_e32 v101, 0x3377d1cf, v100
	v_fmac_f32_e32 v101, 0x3f317217, v100
	v_cmp_lt_f32_e64 s[38:39], |v100|, s22
	s_movk_i32 s4, 0xff
	s_nop 0
	v_cndmask_b32_e64 v100, v100, v101, s[38:39]
	v_cndmask_b32_e32 v101, 0, v230, vcc
	v_sub_f32_e32 v100, v100, v101
	v_add_f32_e32 v101, 1.0, v103
	v_cmp_gt_f32_e32 vcc, s97, v101
	v_sub_f32_e32 v4, v4, v100
	v_and_b32_e32 v119, 15, v2
	v_cndmask_b32_e64 v103, 0, 32, vcc
	v_ldexp_f32 v101, v101, v103
	v_log_f32_e32 v106, v101
	v_mul_f32_e32 v101, 0x3d800000, v4
	v_min_f32_e32 v4, 0, v102
	v_mfma_f32_16x16x32_bf16 v[102:105], v[94:97], v[86:89], 0
	v_mul_f32_e32 v100, 0x3f317217, v106
	v_fma_f32 v100, v106, s49, -v100
	v_fmac_f32_e32 v100, 0x3377d1cf, v106
	v_fmac_f32_e32 v100, 0x3f317217, v106
	v_cmp_lt_f32_e64 s[38:39], |v106|, s22
	s_nop 2
	v_add_f32_e32 v94, v98, v102
	v_mul_f32_e64 v95, |v94|, s48
	v_exp_f32_e32 v95, v95
	v_cndmask_b32_e64 v96, v106, v100, s[38:39]
	v_cndmask_b32_e32 v97, 0, v230, vcc
	v_sub_f32_e32 v96, v96, v97
	v_add_f32_e32 v95, 1.0, v95
; DEVI float log_sigmoid_f(float x) { return fminf(x, 0.f) - __logf(1.f + __expf(-fabsf(x))); }
; DEVI void gla_cum(const GlaIn& in, float* cum) {
;     ...
;     for (int f = 0; f < 4; ++f) {
;         const bf16x8 az = (f == 0) ? in.z0 : (f == 1) ? in.z1 : (f == 2) ? in.z2 : in.z3;
;         f32x4 acc = {0.f, 0.f, 0.f, 0.f};
;         acc = __builtin_amdgcn_mfma_f32_16x16x32_bf16(az, in.bw, acc, 0, 0, 0);
; #pragma unroll
;         for (int r = 0; r < 4; ++r) la[f][r] = log_sigmoid_f(acc[r] + in.bias) * (1.f / 16.f);
;     }
	v_cmp_gt_f32_e32 vcc, s97, v95
	v_sub_f32_e32 v4, v4, v96
	v_add_f32_e32 v96, v98, v103
	v_cndmask_b32_e64 v97, 0, 32, vcc
	v_ldexp_f32 v95, v95, v97
	v_log_f32_e32 v97, v95
	v_mul_f32_e32 v95, 0x3d800000, v4
	v_min_f32_e32 v4, 0, v94
	v_mul_f32_e64 v100, |v96|, s48
	v_mul_f32_e32 v94, 0x3f317217, v97
	v_fma_f32 v94, v97, s49, -v94
	v_exp_f32_e32 v100, v100
	v_fmac_f32_e32 v94, 0x3377d1cf, v97
	v_fmac_f32_e32 v94, 0x3f317217, v97
	v_cmp_lt_f32_e64 s[38:39], |v97|, s22
	v_mfma_f32_16x16x32_bf16 v[84:87], v[82:85], v[86:89], 0
	v_bfe_u32 v118, v2, 4, 2
	v_cndmask_b32_e64 v94, v97, v94, s[38:39]
	v_cndmask_b32_e32 v97, 0, v230, vcc
	v_sub_f32_e32 v94, v94, v97
	v_add_f32_e32 v97, 1.0, v100
	v_cmp_gt_f32_e32 vcc, s97, v97
	v_sub_f32_e32 v4, v4, v94
	s_nop 0
	v_add_f32_e32 v83, v98, v84
	v_cndmask_b32_e64 v100, 0, 32, vcc
	v_ldexp_f32 v97, v97, v100
	v_log_f32_e32 v100, v97
	v_mul_f32_e32 v97, 0x3d800000, v4
	v_min_f32_e32 v4, 0, v96
	v_add_f32_e32 v96, v98, v104
	v_mul_f32_e32 v94, 0x3f317217, v100
	v_mul_f32_e64 v102, |v96|, s48
	v_fma_f32 v94, v100, s49, -v94
	v_exp_f32_e32 v102, v102
	v_fmac_f32_e32 v94, 0x3377d1cf, v100
	v_fmac_f32_e32 v94, 0x3f317217, v100
	v_cmp_lt_f32_e64 s[38:39], |v100|, s22
	v_mul_f32_e64 v82, |v83|, s48
	v_exp_f32_e32 v82, v82
	v_cndmask_b32_e64 v94, v100, v94, s[38:39]
	v_cndmask_b32_e32 v100, 0, v230, vcc
	v_sub_f32_e32 v94, v94, v100
	v_add_f32_e32 v100, 1.0, v102
	v_cmp_gt_f32_e32 vcc, s97, v100
	v_sub_f32_e32 v4, v4, v94
	v_mul_f32_e32 v94, 0x3d800000, v4
	v_cndmask_b32_e64 v102, 0, 32, vcc
	v_ldexp_f32 v100, v100, v102
	v_log_f32_e32 v100, v100
	v_add_f32_e32 v102, v98, v105
	v_min_f32_e32 v4, 0, v96
	v_mul_f32_e64 v103, |v102|, s48
	v_mul_f32_e32 v96, 0x3f317217, v100
	v_fma_f32 v96, v100, s49, -v96
	v_exp_f32_e32 v103, v103
	v_fmac_f32_e32 v96, 0x3377d1cf, v100
	v_fmac_f32_e32 v96, 0x3f317217, v100
	v_cmp_lt_f32_e64 s[38:39], |v100|, s22
	v_add_f32_e32 v82, 1.0, v82
	v_add_f32_e32 v87, v98, v87
	v_cndmask_b32_e64 v96, v100, v96, s[38:39]
	v_cndmask_b32_e32 v100, 0, v230, vcc
	v_sub_f32_e32 v96, v96, v100
	v_add_f32_e32 v100, 1.0, v103
	v_cmp_gt_f32_e32 vcc, s97, v100
	v_sub_f32_e32 v4, v4, v96
	s_nop 0
	v_cndmask_b32_e64 v103, 0, 32, vcc
	v_ldexp_f32 v100, v100, v103
	v_log_f32_e32 v103, v100
	v_mul_f32_e32 v100, 0x3d800000, v4
	v_min_f32_e32 v4, 0, v102
	v_add_f32_e32 v102, v98, v90
	v_mul_f32_e64 v90, |v102|, s48
	v_exp_f32_e32 v90, v90
	v_mul_f32_e32 v96, 0x3f317217, v103
	v_fma_f32 v96, v103, s49, -v96
	v_fmac_f32_e32 v96, 0x3377d1cf, v103
	v_fmac_f32_e32 v96, 0x3f317217, v103
	v_cmp_lt_f32_e64 s[38:39], |v103|, s22
	v_add_f32_e32 v90, 1.0, v90
	s_nop 0
	v_cndmask_b32_e64 v96, v103, v96, s[38:39]
	v_cndmask_b32_e32 v103, 0, v230, vcc
	v_cmp_gt_f32_e32 vcc, s97, v90
	v_sub_f32_e32 v96, v96, v103
	v_sub_f32_e32 v4, v4, v96
	v_cndmask_b32_e64 v103, 0, 32, vcc
	v_ldexp_f32 v90, v90, v103
	v_log_f32_e32 v103, v90
	v_mul_f32_e32 v90, 0x3d800000, v4
	v_min_f32_e32 v4, 0, v102
	v_add_f32_e32 v102, v98, v91
	v_mul_f32_e64 v91, |v102|, s48
	v_exp_f32_e32 v91, v91
	v_mul_f32_e32 v96, 0x3f317217, v103
	v_fma_f32 v96, v103, s49, -v96
	v_fmac_f32_e32 v96, 0x3377d1cf, v103
	v_fmac_f32_e32 v96, 0x3f317217, v103
	v_cmp_lt_f32_e64 s[38:39], |v103|, s22
	v_add_f32_e32 v91, 1.0, v91
	s_nop 0
	v_cndmask_b32_e64 v96, v103, v96, s[38:39]
	v_cndmask_b32_e32 v103, 0, v230, vcc
	v_cmp_gt_f32_e32 vcc, s97, v91
	v_sub_f32_e32 v96, v96, v103
	v_sub_f32_e32 v4, v4, v96
	v_cndmask_b32_e64 v103, 0, 32, vcc
	v_ldexp_f32 v91, v91, v103
	v_log_f32_e32 v103, v91
	v_mul_f32_e32 v91, 0x3d800000, v4
	v_min_f32_e32 v4, 0, v102
	v_add_f32_e32 v102, v98, v92
	v_mul_f32_e64 v92, |v102|, s48
	v_exp_f32_e32 v92, v92
	v_mul_f32_e32 v96, 0x3f317217, v103
	v_fma_f32 v96, v103, s49, -v96
	v_fmac_f32_e32 v96, 0x3377d1cf, v103
	v_fmac_f32_e32 v96, 0x3f317217, v103
	v_cmp_lt_f32_e64 s[38:39], |v103|, s22
	v_add_f32_e32 v92, 1.0, v92
	s_nop 0
	v_cndmask_b32_e64 v96, v103, v96, s[38:39]
	v_cndmask_b32_e32 v103, 0, v230, vcc
	v_cmp_gt_f32_e32 vcc, s97, v92
	v_sub_f32_e32 v96, v96, v103
	v_sub_f32_e32 v4, v4, v96
	v_cndmask_b32_e64 v103, 0, 32, vcc
	v_ldexp_f32 v92, v92, v103
	v_log_f32_e32 v103, v92
	v_mul_f32_e32 v92, 0x3d800000, v4
	v_min_f32_e32 v4, 0, v102
	v_mul_f32_e64 v102, |v93|, s48
	v_exp_f32_e32 v102, v102
	v_mul_f32_e32 v96, 0x3f317217, v103
	v_fma_f32 v96, v103, s49, -v96
	v_fmac_f32_e32 v96, 0x3377d1cf, v103
	v_fmac_f32_e32 v96, 0x3f317217, v103
	v_cmp_lt_f32_e64 s[38:39], |v103|, s22
	v_add_f32_e32 v102, 1.0, v102
	s_nop 0
	v_cndmask_b32_e64 v96, v103, v96, s[38:39]
	v_cndmask_b32_e32 v103, 0, v230, vcc
	v_cmp_gt_f32_e32 vcc, s97, v102
	v_sub_f32_e32 v96, v96, v103
	v_sub_f32_e32 v4, v4, v96
	v_cndmask_b32_e64 v103, 0, 32, vcc
	v_ldexp_f32 v102, v102, v103
	v_log_f32_e32 v102, v102
	v_mul_f32_e32 v120, 0x3d800000, v4
	v_min_f32_e32 v4, 0, v93
	v_cndmask_b32_e32 v88, 0, v230, vcc
	v_mul_f32_e32 v93, 0x3f317217, v102
	v_fma_f32 v93, v102, s49, -v93
	v_fmac_f32_e32 v93, 0x3377d1cf, v102
	v_fmac_f32_e32 v93, 0x3f317217, v102
	v_cmp_lt_f32_e64 s[38:39], |v102|, s22
	v_cmp_gt_f32_e32 vcc, s97, v82
	s_nop 0
	v_cndmask_b32_e64 v84, v102, v93, s[38:39]
; DEVI void gla_cum(const GlaIn& in, float* cum) {
;     ...
;     if (d == 0) {
;         float carry = 0.f;
; #pragma unroll
;         for (int f = 0; f < 4; ++f) {
;             la[f][1] += la[f][0]; la[f][2] += la[f][1]; la[f][3] += la[f][2];
;             float x = la[f][3]; const float own = x;
;             float y = __shfl_up(x, 16); if (fq >= 1) x += y;
;             y = __shfl_up(x, 32); if (fq >= 2) x += y;
;             const float excl = x - own + carry;
;             carry += __shfl(x, 48 + fr);
; #pragma unroll
;             for (int r = 0; r < 4; ++r) la[f][r] += excl;
;         }
;     } else {
;         float carry = 0.f;
; #pragma unroll
;         for (int f = 3; f >= 0; --f) {
;             la[f][2] += la[f][3]; la[f][1] += la[f][2]; la[f][0] += la[f][1];
;             float x = la[f][0]; const float own = x;
;             float y = __shfl_down(x, 16); if (fq <= 2) x += y;
;             y = __shfl_down(x, 32); if (fq <= 1) x += y;
;             const float excl = x - own + carry;
;             carry += __shfl(x, fr);
; #pragma unroll
;             for (int r = 0; r < 4; ++r) la[f][r] += excl;
;         }
;     }
	v_sub_f32_e32 v84, v84, v88
	v_cndmask_b32_e64 v88, 0, 32, vcc
	v_ldexp_f32 v82, v82, v88
	v_log_f32_e32 v88, v82
	v_sub_f32_e32 v4, v4, v84
	v_add_f32_e32 v84, v98, v85
	v_mul_f32_e64 v85, |v84|, s48
	v_exp_f32_e32 v85, v85
	v_mul_f32_e32 v82, 0x3d800000, v4
	v_min_f32_e32 v4, 0, v83
	v_mul_f32_e32 v83, 0x3f317217, v88
	v_fma_f32 v83, v88, s49, -v83
	v_fmac_f32_e32 v83, 0x3377d1cf, v88
	v_fmac_f32_e32 v83, 0x3f317217, v88
	v_cmp_lt_f32_e64 s[38:39], |v88|, s22
	v_add_f32_e32 v85, 1.0, v85
	s_nop 0
	v_cndmask_b32_e64 v83, v88, v83, s[38:39]
	v_cndmask_b32_e32 v88, 0, v230, vcc
	v_cmp_gt_f32_e32 vcc, s97, v85
	v_sub_f32_e32 v83, v83, v88
	v_sub_f32_e32 v4, v4, v83
	v_cndmask_b32_e64 v88, 0, 32, vcc
	v_ldexp_f32 v85, v85, v88
	v_log_f32_e32 v88, v85
	v_mul_f32_e32 v85, 0x3d800000, v4
	v_min_f32_e32 v4, 0, v84
	v_add_f32_e32 v84, v98, v86
	v_mul_f32_e64 v86, |v84|, s48
	v_exp_f32_e32 v86, v86
	v_mul_f32_e32 v83, 0x3f317217, v88
	v_fma_f32 v83, v88, s49, -v83
	v_fmac_f32_e32 v83, 0x3377d1cf, v88
	v_fmac_f32_e32 v83, 0x3f317217, v88
	v_cmp_lt_f32_e64 s[38:39], |v88|, s22
	v_add_f32_e32 v86, 1.0, v86
	s_nop 0
	v_cndmask_b32_e64 v83, v88, v83, s[38:39]
	v_cndmask_b32_e32 v88, 0, v230, vcc
	v_cmp_gt_f32_e32 vcc, s97, v86
	v_sub_f32_e32 v83, v83, v88
	v_sub_f32_e32 v4, v4, v83
	v_cndmask_b32_e64 v88, 0, 32, vcc
	v_ldexp_f32 v86, v86, v88
	v_log_f32_e32 v86, v86
	v_mul_f32_e32 v83, 0x3d800000, v4
	v_min_f32_e32 v4, 0, v84
	v_mul_f32_e64 v88, |v87|, s48
	v_mul_f32_e32 v84, 0x3f317217, v86
	v_fma_f32 v84, v86, s49, -v84
	v_exp_f32_e32 v88, v88
	v_fmac_f32_e32 v84, 0x3377d1cf, v86
	v_fmac_f32_e32 v84, 0x3f317217, v86
	v_cmp_lt_f32_e64 s[38:39], |v86|, s22
	s_nop 1
	v_cndmask_b32_e64 v84, v86, v84, s[38:39]
	v_cndmask_b32_e32 v86, 0, v230, vcc
	v_sub_f32_e32 v84, v84, v86
	v_add_f32_e32 v86, 1.0, v88
	v_cmp_gt_f32_e32 vcc, s97, v86
	v_sub_f32_e32 v4, v4, v84
	v_mul_f32_e32 v93, 0x3d800000, v4
	v_cndmask_b32_e64 v88, 0, 32, vcc
	v_ldexp_f32 v86, v86, v88
	v_log_f32_e32 v86, v86
	v_min_f32_e32 v4, 0, v87
	v_mul_f32_e32 v84, 0x3f317217, v86
	v_fma_f32 v84, v86, s49, -v84
	v_fmac_f32_e32 v84, 0x3377d1cf, v86
	v_fmac_f32_e32 v84, 0x3f317217, v86
	v_cmp_lt_f32_e64 s[38:39], |v86|, s22
	s_nop 1
	v_cndmask_b32_e64 v84, v86, v84, s[38:39]
	v_cndmask_b32_e32 v86, 0, v230, vcc
	v_sub_f32_e32 v84, v84, v86
	v_sub_f32_e32 v4, v4, v84
	v_mul_f32_e32 v86, 0x3d800000, v4
	v_cmp_lt_u32_e32 vcc, s4, v2
	s_and_saveexec_b64 s[4:5], vcc
	s_xor_b64 s[16:17], exec, s[4:5]
	s_cbranch_execz .LBB0_503
	v_and_b32_e32 v4, 48, v227
	v_cmp_eq_u32_e32 vcc, 48, v4
	v_add_f32_e32 v87, v86, v93
	v_add_f32_e32 v84, v83, v87
	v_cndmask_b32_e64 v4, 16, 0, vcc
	v_add_lshl_u32 v89, v4, v227, 2
	v_add_f32_e32 v85, v85, v84
	ds_bpermute_b32 v4, v89, v85
	v_mov_b32_e32 v83, 0x80
	v_cmp_eq_u32_e32 vcc, 3, v118
	v_lshl_or_b32 v104, v227, 2, v83
	v_cmp_gt_u32_e64 s[38:39], 2, v118
	s_waitcnt lgkmcnt(0)
	v_add_f32_e32 v4, v85, v4
	v_cndmask_b32_e32 v4, v4, v85, vcc
	ds_bpermute_b32 v83, v104, v4
	v_and_or_b32 v88, v227, 64, v119
	v_lshlrev_b32_e32 v105, 2, v88
	s_waitcnt lgkmcnt(0)
	v_add_f32_e32 v83, v4, v83
	v_cndmask_b32_e64 v4, v4, v83, s[38:39]
	v_sub_f32_e32 v83, v4, v85
	v_add_f32_e32 v88, 0, v83
	v_add_f32_e32 v83, v82, v120
	v_add_f32_e32 v92, v92, v83
	v_add_f32_e32 v93, v91, v92
	v_add_f32_e32 v91, v90, v100
	v_add_f32_e32 v96, v94, v91
	ds_bpermute_b32 v98, v89, v93
	v_add_f32_e32 v97, v97, v96
	ds_bpermute_b32 v100, v89, v97
	ds_bpermute_b32 v94, v105, v4
	v_pk_add_f32 v[102:103], v[84:85], v[88:89] op_sel_hi:[1,0]
	s_waitcnt lgkmcnt(2)
	v_add_f32_e32 v4, v93, v98
	v_cndmask_b32_e32 v4, v4, v93, vcc
	s_waitcnt lgkmcnt(1)
	v_add_f32_e32 v100, v97, v100
	ds_bpermute_b32 v98, v104, v4
	v_cndmask_b32_e32 v100, v100, v97, vcc
	ds_bpermute_b32 v106, v104, v100
	s_waitcnt lgkmcnt(1)
	v_add_f32_e32 v84, v4, v98
	v_cndmask_b32_e64 v108, v4, v84, s[38:39]
	s_waitcnt lgkmcnt(0)
	v_add_f32_e32 v4, v100, v106
	ds_bpermute_b32 v98, v105, v108
	v_cndmask_b32_e64 v109, v100, v4, s[38:39]
	ds_bpermute_b32 v4, v105, v109
	v_mov_b32_e32 v100, v3
	v_pk_add_f32 v[84:85], v[94:95], v[100:101]
	v_pk_add_f32 v[106:107], v[86:87], v[88:89] op_sel_hi:[1,0]
	s_waitcnt lgkmcnt(1)
	v_pk_add_f32 v[86:87], v[84:85], v[98:99]
	v_sub_f32_e32 v94, v109, v97
	s_waitcnt lgkmcnt(0)
	v_pk_add_f32 v[4:5], v[86:87], v[4:5]
	ds_bpermute_b32 v88, v89, v5
	v_sub_f32_e32 v89, v108, v93
	v_add_f32_e32 v84, v84, v89
	v_pk_add_f32 v[112:113], v[82:83], v[84:85] op_sel_hi:[1,0]
	v_add_f32_e32 v82, v86, v94
	s_waitcnt lgkmcnt(0)
	v_add_f32_e32 v88, v5, v88
	v_cndmask_b32_e32 v88, v88, v5, vcc
	ds_bpermute_b32 v89, v104, v88
	v_pk_add_f32 v[110:111], v[96:97], v[82:83] op_sel_hi:[1,0]
	v_pk_add_f32 v[114:115], v[90:91], v[82:83] op_sel_hi:[1,0]
	v_pk_add_f32 v[108:109], v[92:93], v[84:85] op_sel_hi:[1,0]
	v_mov_b32_e32 v84, v95
	s_waitcnt lgkmcnt(0)
	v_add_f32_e32 v82, v88, v89
	v_cndmask_b32_e64 v82, v88, v82, s[38:39]
	v_sub_f32_e32 v82, v82, v5
	v_add_f32_e32 v82, v4, v82
	v_mov_b32_e32 v4, v87
	v_pk_add_f32 v[88:89], v[4:5], v[82:83] op_sel_hi:[1,0]
	v_pk_add_f32 v[104:105], v[84:85], v[82:83] op_sel_hi:[1,0]

; DEVI int opaque_tid() { int t = threadIdx.x; asm volatile("" : "+v"(t)); return t; }
; DEVI unsigned cvt4_fp8(float a, float b, float c, float d) { int w = 0; w = __builtin_amdgcn_cvt_pk_fp8_f32(a, b, w, false); w = __builtin_amdgcn_cvt_pk_fp8_f32(c, d, w, true); return (unsigned)w; }
; DEVI void cvt8_finish(const Params& p, int L, int t, const CvtIn& in, char* smem) {
;     const int which = t / 4096, r = t % 4096, le = L * 16 + r / 256, kt = (r % 256) / 16, nt = r % 16;
;     unsigned char* dst = (which == 2) ? (unsigned char*)(p.ws + WS_WDN) + (size_t)le * 2048 * 2048 + (size_t)(nt * 128) * 2048
;                                       : (unsigned char*)(p.ws + WS_WGU) + (size_t)le * 4096 * 2048 + (size_t)(nt * 256 + which * 128) * 2048;
;     unsigned char* T = (unsigned char*)smem;
;     const int tid = opaque_tid(), nq = tid & 31, kq0 = tid >> 5;
; #pragma unroll
;     for (int it = 0; it < 2; ++it) { const int kq = kq0 + it * 16;
; #pragma unroll
;         for (int j = 0; j < 4; ++j) *(unsigned*)(T + (nq * 4 + j) * 144 + kq * 4) =
;             cvt4_fp8(in.v[it * 4][j] * W8_SCALE, in.v[it * 4 + 1][j] * W8_SCALE, in.v[it * 4 + 2][j] * W8_SCALE, in.v[it * 4 + 3][j] * W8_SCALE); }
;     __syncthreads();
; #pragma unroll
;     for (int i = 0; i < 2; ++i) { const int nl = (tid >> 3) + 64 * i, kc = (tid & 7) * 16;
;         *(u32x4*)(dst + (size_t)nl * 2048 + kt * 128 + kc) = *(const u32x4*)(T + nl * 144 + kc); }
;     __syncthreads();
; }
; DEVI void gla_load(const Params& p, int l, int b, int h, int c, bool need_qg, GlaIn& in) {
;     ...
;         float wv[8];
; #pragma unroll
;         for (int j = 0; j < 8; ++j) wv[j] = p.gla_w2[((size_t)(l * 2 + d) * 16 + fq * 8 + j) * 256 + h * 64 + kk];
;         in.bw = pack8(wv);
.LBB0_513:
	s_waitcnt vmcnt(15)
	v_mul_f32_e32 v46, 0x42800000, v46
	s_waitcnt vmcnt(14)
	v_mul_f32_e32 v50, 0x42800000, v50
	v_mov_b32_e32 v70, v3
	v_cvt_pk_fp8_f32 v70, v46, v50
	s_waitcnt vmcnt(13)
	v_mul_f32_e32 v50, 0x42800000, v62
	s_waitcnt vmcnt(12)
	v_mul_f32_e32 v62, 0x42800000, v66
	v_mov_b32_e32 v2, v0
	v_cvt_pk_fp8_f32 v70, v50, v62 op_sel:[0,0,1]
	v_mul_f32_e32 v47, 0x42800000, v47
	v_mul_f32_e32 v50, 0x42800000, v51
	v_mov_b32_e32 v51, v3
	v_cvt_pk_fp8_f32 v51, v47, v50
	v_lshlrev_b32_e32 v4, 2, v2
	v_and_b32_e32 v5, 0x7c, v4
	v_ashrrev_i32_e32 v4, 3, v2
	v_and_b32_e32 v46, -4, v4
	v_mul_u32_u24_e32 v5, 0x90, v5
	v_add3_u32 v5, 0, v46, v5
	v_mul_f32_e32 v46, 0x42800000, v63
	v_mul_f32_e32 v47, 0x42800000, v67
	v_cvt_pk_fp8_f32 v51, v46, v47 op_sel:[0,0,1]
	v_mul_f32_e32 v46, 0x42800000, v48
	v_mul_f32_e32 v47, 0x42800000, v52
	v_mov_b32_e32 v52, v3
	v_cvt_pk_fp8_f32 v52, v46, v47
	v_mul_f32_e32 v48, 0x42800000, v64
	v_mul_f32_e32 v50, 0x42800000, v68
	s_waitcnt vmcnt(11)
	v_mul_f32_e32 v38, 0x42800000, v38
	v_cvt_pk_fp8_f32 v52, v48, v50 op_sel:[0,0,1]
	s_waitcnt vmcnt(10)
	v_mul_f32_e32 v42, 0x42800000, v42
	v_mov_b32_e32 v48, v3
	v_cvt_pk_fp8_f32 v48, v38, v42
	v_mul_f32_e32 v38, 0x42800000, v39
	v_mul_f32_e32 v39, 0x42800000, v43
	v_mov_b32_e32 v42, v3
	v_cvt_pk_fp8_f32 v42, v38, v39
	v_mul_f32_e32 v46, 0x42800000, v49
	v_mul_f32_e32 v47, 0x42800000, v53
	v_mov_b32_e32 v49, v3
	v_cvt_pk_fp8_f32 v49, v46, v47
	s_waitcnt vmcnt(9)
	v_mul_f32_e32 v38, 0x42800000, v55
	s_waitcnt vmcnt(8)
	v_mul_f32_e32 v39, 0x42800000, v59
	v_cvt_pk_fp8_f32 v42, v38, v39 op_sel:[0,0,1]
	v_mul_f32_e32 v38, 0x42800000, v40
	v_mul_f32_e32 v39, 0x42800000, v44
	v_mov_b32_e32 v44, v3
	v_mul_f32_e32 v46, 0x42800000, v65
	v_mul_f32_e32 v47, 0x42800000, v69
	v_cvt_pk_fp8_f32 v44, v38, v39
	v_mul_f32_e32 v38, 0x42800000, v41
	v_mul_f32_e32 v39, 0x42800000, v45
	v_mov_b32_e32 v41, v3
	v_cvt_pk_fp8_f32 v49, v46, v47 op_sel:[0,0,1]
	v_mul_f32_e32 v46, 0x42800000, v54
	v_mul_f32_e32 v47, 0x42800000, v58
	v_cvt_pk_fp8_f32 v41, v38, v39
	v_cvt_pk_fp8_f32 v48, v46, v47 op_sel:[0,0,1]
	v_mul_f32_e32 v40, 0x42800000, v56
	v_mul_f32_e32 v43, 0x42800000, v60
	v_cvt_pk_fp8_f32 v44, v40, v43 op_sel:[0,0,1]
	v_mul_f32_e32 v38, 0x42800000, v57
	v_mul_f32_e32 v39, 0x42800000, v61
	s_ashr_i32 s5, s25, 31
	v_cvt_pk_fp8_f32 v41, v38, v39 op_sel:[0,0,1]
	v_lshlrev_b32_e32 v2, 4, v2
	s_add_u32 s4, s16, s25
	ds_write2_b32 v5, v70, v48 offset1:16
	ds_write2_b32 v5, v51, v42 offset0:36 offset1:52
	ds_write2_b32 v5, v52, v44 offset0:72 offset1:88
	ds_write2_b32 v5, v49, v41 offset0:108 offset1:124
	v_and_b32_e32 v2, 0x70, v2
	s_addc_u32 s5, s17, s5
	v_mul_lo_u32 v5, v4, s91
	v_lshl_add_u64 v[42:43], s[4:5], 0, v[2:3]
	v_add3_u32 v2, 0, v2, v5
	s_waitcnt lgkmcnt(0)
	s_barrier
	ds_read_b128 v[38:41], v2
	v_ashrrev_i32_e32 v5, 31, v4
	v_lshlrev_b64 v[4:5], 11, v[4:5]
	v_lshl_add_u64 v[4:5], v[42:43], 0, v[4:5]
	ds_read_b128 v[42:45], v2 offset:9216
	s_waitcnt lgkmcnt(1)
	global_store_dwordx4 v[4:5], v[38:41], off
	v_add_co_u32_e32 v4, vcc, 0x20000, v4
	s_sub_i32 s19, s19, s63
	s_nop 0
	v_addc_co_u32_e32 v5, vcc, 0, v5, vcc
	s_andn2_b64 vcc, exec, s[40:41]
	s_add_i32 s23, s23, s24
	s_waitcnt lgkmcnt(0)
	global_store_dwordx4 v[4:5], v[42:45], off
	s_barrier
	s_cbranch_vccz .LBB0_515
	v_bfe_u32 v164, v0, 4, 2
	v_cmp_gt_u32_e32 vcc, 2, v164
	v_cvt_pk_bf16_f32 v165, v156, v157
	v_cvt_pk_bf16_f32 v166, v158, v159
	v_cvt_pk_bf16_f32 v167, v160, v161
	v_cvt_pk_bf16_f32 v168, v162, v163
	v_cndmask_b32_e32 v34, v34, v165, vcc
	v_cndmask_b32_e32 v35, v35, v166, vcc
	v_cndmask_b32_e32 v36, v36, v167, vcc
	v_cndmask_b32_e32 v37, v37, v168, vcc
	v_mov_b64_e32 v[88:89], v[36:37]
	v_mov_b64_e32 v[84:85], v[32:33]
	v_mov_b64_e32 v[92:93], v[28:29]
	v_mov_b64_e32 v[96:97], v[20:21]
	v_mov_b64_e32 v[56:57], v[24:25]
	v_mov_b64_e32 v[72:73], v[16:17]
	v_mov_b64_e32 v[76:77], v[12:13]
	v_mov_b64_e32 v[80:81], v[8:9]
	s_mov_b32 s6, s14
	v_mov_b32_e32 v98, v116
	v_mov_b64_e32 v[86:87], v[34:35]
	v_mov_b64_e32 v[82:83], v[30:31]
	v_mov_b64_e32 v[90:91], v[26:27]
	v_mov_b64_e32 v[94:95], v[18:19]
	v_mov_b64_e32 v[54:55], v[22:23]
	v_mov_b64_e32 v[70:71], v[14:15]
	v_mov_b64_e32 v[74:75], v[10:11]
	v_mov_b64_e32 v[78:79], v[6:7]
	s_branch .LBB0_495

; DEVI void phase_l2(const Params& p, int l, char* smem) {
;     ...
;         {   RetIn cur; bool have = u < nsc;
;             if (have) { const int r = u - nG; ret_load(p, (r / NCH) >> 2, (r / NCH) & 3, r % NCH, false, cur); }
;             while (have) { const int un = u + G; const bool hn = un < nsc; RetIn nxt; const int r = u - nG, rn = un - nG;
;                 if (hn) ret_load(p, (rn / NCH) >> 2, (rn / NCH) & 3, rn % NCH, false, nxt);
;                 CvtIn ci; cvt8_load(p, l, (l == 0 ? TS0A : TS1A) + u, ci);
.LBB0_523:
	v_readlane_b32 s4, v254, 49
	v_readlane_b32 s5, v254, 50
	s_and_b64 s[4:5], s[4:5], exec
	s_movk_i32 s4, 0x2700
	s_cselect_b32 s15, s4, 0x2780
	v_readlane_b32 s4, v254, 61
	s_lshl_b32 s18, s4, 4
	s_add_i32 s4, s14, 0xfffffdc0
	v_readlane_b32 s5, v254, 62
	s_waitcnt vmcnt(0)
	s_branch .LBB0_525

; DEVI int opaque_tid() { int t = threadIdx.x; asm volatile("" : "+v"(t)); return t; }
; DEVI void ret_decays(int h, float& ldf, float& ldb) { ldf = log1pf(-exp2f(-(5.f + 2.f * h))); ldb = log1pf(-exp2f(-(6.f + 2.f * h))); }
; DEVI void cvt8_load(const Params& p, int L, int t, CvtIn& in) {
;     const int which = t / 4096, r = t % 4096, le = L * 16 + r / 256, kt = (r % 256) / 16, nt = r % 16;
;     const float* src = (which == 2 ? p.w_down : (which == 0 ? p.w_gate : p.w_up)) + (size_t)le * 2048 * 2048;
;     const int tid = opaque_tid(), nq = tid & 31, kq0 = tid >> 5;
; #pragma unroll
;     for (int it = 0; it < 2; ++it)
; #pragma unroll
;         for (int kk = 0; kk < 4; ++kk) in.v[it * 4 + kk] = __builtin_nontemporal_load((const f32x4*)(src + (size_t)(kt * 128 + (kq0 + it * 16) * 4 + kk) * 2048 + nt * 128 + nq * 4));
; }
; DEVI void ret_rot(const bf16x8 r0, const bf16x8 r1, const RetIn& in, bool lat, float scale, float (&o)[16]) {
;     float a[8], c[8]; unpack8(r0, a); unpack8(r1, c);
; #pragma unroll
;     for (int i = 0; i < 8; ++i) { o[i] = a[i]; o[8 + i] = c[i]; }
;     if (lat) {
; #pragma unroll
;         for (int q = 0; q < 4; ++q) { const f32x4 cs = (q == 0) ? in.cs0 : (q == 1) ? in.cs1 : (q == 2) ? in.cs2 : in.cs3;
;             const float x1 = o[4 * q], x2 = o[4 * q + 1], y1 = o[4 * q + 2], y2 = o[4 * q + 3];
;             o[4 * q] = x1 * cs[0] - x2 * cs[1]; o[4 * q + 1] = x1 * cs[1] + x2 * cs[0];
;             o[4 * q + 2] = y1 * cs[2] - y2 * cs[3]; o[4 * q + 3] = y1 * cs[3] + y2 * cs[2]; }
;     }
; #pragma unroll
;     for (int i = 0; i < 16; ++i) o[i] *= scale;
; }
; DEVI void scan_a_ret(const Params& p, int l, int b, int h, int c, const RetIn& in, char* smem) {
;     bf16_t* kTf = (bf16_t*)smem; bf16_t* kTb = kTf + 128 * 72; bf16_t* vT = kTb + 128 * 72;
;     const int tid = opaque_tid(), wid = tid >> 6, lane = tid & 63, fr = lane & 15, fq = lane >> 4;
;     const bool lat = c >= 4;
;     const int tk = tid >> 3, kk16 = (tid & 7) * 16;
;     float ldf, ldb; ret_decays(h, ldf, ldb);
;     float kf[16];
;     ret_rot(in.k0, in.k1, in, lat, 0.08838834764831845f, kf);
;     const float ef = __expf(ldf * (float)(63 - tk)), eb = __expf(ldb * (float)tk);
.LBB0_528:
	s_add_i32 s5, s15, s4
	s_add_i32 s16, s5, 0x240
	s_and_b32 s6, s16, 0xfffff000
	s_addk_i32 s5, 0x123f
	s_cmpk_lt_u32 s5, 0x1fff
	s_cselect_b32 s5, s64, 0x80
	s_cmpk_lg_i32 s6, 0x2000
	s_cselect_b64 s[44:45], -1, 0
	s_and_b64 s[6:7], s[44:45], exec
	s_cselect_b32 s5, s5, 0x88
	s_add_u32 s6, s0, s5
	s_addc_u32 s7, s1, 0
	s_ashr_i32 s5, s16, 31
	s_lshr_b32 s5, s5, 20
	s_add_i32 s24, s16, s5
	s_and_b32 s5, s24, 0xf000
	s_sub_i32 s5, s16, s5
	s_sext_i32_i16 s16, s5
	s_lshr_b32 s16, s16, 15
	s_bfe_u32 s17, s16, 0x4000c
	s_add_i32 s17, s5, s17
	s_and_b32 s17, s17, 0xfff0
	s_bfe_u32 s16, s16, 0x80008
	s_sub_i32 s17, s5, s17
	s_add_i32 s16, s5, s16
	s_sext_i32_i16 s23, s17
	s_sext_i32_i16 s17, s16
	s_and_b32 s16, s16, 0xff00
	s_sub_i32 s5, s5, s16
	s_sext_i32_i16 s16, s5
	s_bfe_u32 s16, s16, 0x4001b
	s_load_dwordx2 s[6:7], s[6:7], 0x0
	s_add_i32 s5, s5, s16
	s_ashr_i32 s16, s17, 8
	s_add_i32 s42, s18, s16
	s_ashr_i32 s43, s42, 31
	s_lshl_b64 s[16:17], s[42:43], 24
	s_waitcnt lgkmcnt(0)
	s_add_u32 s16, s6, s16
	s_sext_i32_i16 s5, s5
	s_addc_u32 s17, s7, s17
	v_mov_b32_e32 v1, v0
	s_lshl_b32 s6, s23, 7
	s_lshl_b32 s5, s5, 3
	v_ashrrev_i32_e32 v2, 3, v1
	s_ashr_i32 s7, s6, 31
	s_and_b32 s19, s5, 0xffffff80
	v_and_b32_e32 v2, -4, v2
	s_lshl_b64 s[6:7], s[6:7], 2
	v_add_u32_e32 v36, s19, v2
	s_add_u32 s6, s16, s6
	v_lshlrev_b32_e32 v1, 4, v1
	s_addc_u32 s7, s17, s7
	v_and_b32_e32 v2, 0x1f0, v1
	v_ashrrev_i32_e32 v37, 31, v36
	v_lshl_add_u64 v[38:39], s[6:7], 0, v[2:3]
	v_lshlrev_b64 v[40:41], 13, v[36:37]
	v_lshl_add_u64 v[44:45], v[38:39], 0, v[40:41]
	v_or_b32_e32 v40, 1, v36
	v_ashrrev_i32_e32 v41, 31, v40
	v_lshlrev_b64 v[40:41], 13, v[40:41]
	v_lshl_add_u64 v[40:41], v[38:39], 0, v[40:41]
	global_load_dwordx4 v[52:55], v[44:45], off nt
	global_load_dwordx4 v[56:59], v[40:41], off nt
	v_or_b32_e32 v40, 2, v36
	v_or_b32_e32 v36, 3, v36
	v_ashrrev_i32_e32 v41, 31, v40
	v_ashrrev_i32_e32 v37, 31, v36
	v_lshlrev_b64 v[40:41], 13, v[40:41]
	v_lshlrev_b64 v[36:37], 13, v[36:37]
	v_lshl_add_u64 v[40:41], v[38:39], 0, v[40:41]
	v_lshl_add_u64 v[36:37], v[38:39], 0, v[36:37]
	global_load_dwordx4 v[60:63], v[40:41], off nt
	global_load_dwordx4 v[64:67], v[36:37], off nt
	v_add_co_u32_e32 v36, vcc, s94, v44
	s_mov_b32 s5, 0x82000
	s_nop 0
	v_addc_co_u32_e32 v37, vcc, 0, v45, vcc
	v_add_co_u32_e32 v40, vcc, s5, v44
	s_mov_b32 s5, 0x84000
	s_nop 0
	v_addc_co_u32_e32 v41, vcc, 0, v45, vcc
	v_add_co_u32_e32 v46, vcc, s5, v44
	s_mov_b32 s5, 0x86000
	s_nop 0
	v_addc_co_u32_e32 v47, vcc, 0, v45, vcc
	v_add_co_u32_e32 v48, vcc, s5, v44
	global_load_dwordx4 v[36:39], v[36:37], off nt
	s_nop 0
	global_load_dwordx4 v[40:43], v[40:41], off nt
	v_addc_co_u32_e32 v49, vcc, 0, v45, vcc
	global_load_dwordx4 v[44:47], v[46:47], off nt
	s_nop 0
	global_load_dwordx4 v[48:51], v[48:49], off nt
	s_mul_hi_i32 s6, s4, 0x38e38e39
	s_lshr_b32 s7, s6, 31
	s_ashr_i32 s6, s6, 3
	s_add_i32 s6, s6, s7
	s_mul_i32 s7, s6, 36
	s_sub_i32 s4, s4, s7
	v_lshlrev_b32_e32 v123, 16, v85
	v_lshlrev_b32_e32 v120, 16, v84
	v_lshlrev_b32_e32 v119, 16, v87
	v_lshlrev_b32_e32 v116, 16, v86
	v_lshlrev_b32_e32 v115, 16, v89
	v_lshlrev_b32_e32 v112, 16, v88
	v_lshlrev_b32_e32 v111, 16, v91
	v_lshlrev_b32_e32 v108, 16, v90
	s_mov_b32 s5, 3
	v_mov_b32_e32 v124, v0
	s_cmp_lt_i32 s4, 4
	v_pk_mov_b32 v[100:101], v[110:111], v[108:109] op_sel:[1,0]
	v_pk_mov_b32 v[102:103], v[114:115], v[112:113] op_sel:[1,0]
	v_pk_mov_b32 v[104:105], v[118:119], v[116:117] op_sel:[1,0]
	v_pk_mov_b32 v[106:107], v[122:123], v[120:121] op_sel:[1,0]
	s_cbranch_scc1 .LBB0_530
	v_and_b32_e32 v133, 0xffff0000, v85
	v_and_b32_e32 v132, 16, v84
	v_and_b32_e32 v85, 16, v85
	v_and_b32_e32 v84, 0xffff0000, v84
	v_mov_b32_e32 v122, v84
	v_mov_b32_e32 v136, v99
	v_mov_b32_e32 v137, v97
	v_pk_mov_b32 v[84:85], v[132:133], v[84:85] op_sel:[1,0]
	v_mov_b32_e32 v134, v98
	v_mov_b32_e32 v135, v96
	v_pk_mul_f32 v[84:85], v[136:137], v[84:85]
	v_and_b32_e32 v129, 0xffff0000, v87
	v_and_b32_e32 v128, 16, v86
	v_and_b32_e32 v87, 16, v87
	v_and_b32_e32 v86, 0xffff0000, v86
	v_pk_fma_f32 v[106:107], v[134:135], v[106:107], v[84:85] neg_lo:[0,0,1] neg_hi:[0,0,1]
	v_mov_b32_e32 v84, v96
	v_mov_b32_e32 v85, v99
	v_mov_b32_e32 v118, v86
	v_mov_b32_e32 v121, v133
	v_pk_mul_f32 v[84:85], v[84:85], v[122:123]
	v_mov_b32_e32 v96, v97
	v_mov_b32_e32 v97, v98
	v_mov_b32_e32 v98, v95
	v_mov_b32_e32 v99, v93
	v_pk_mov_b32 v[86:87], v[128:129], v[86:87] op_sel:[1,0]
	v_pk_fma_f32 v[84:85], v[96:97], v[120:121], v[84:85]
	v_mov_b32_e32 v96, v94
	v_mov_b32_e32 v97, v92
	v_pk_mul_f32 v[86:87], v[98:99], v[86:87]
	v_and_b32_e32 v131, 0xffff0000, v89
	v_and_b32_e32 v130, 16, v88
	v_and_b32_e32 v89, 16, v89
	v_and_b32_e32 v88, 0xffff0000, v88
	v_pk_fma_f32 v[104:105], v[96:97], v[104:105], v[86:87] neg_lo:[0,0,1] neg_hi:[0,0,1]
	v_mov_b32_e32 v86, v92
	v_mov_b32_e32 v87, v95
	v_mov_b32_e32 v117, v129
	v_mov_b32_e32 v114, v88
	v_pk_mul_f32 v[86:87], v[86:87], v[118:119]
	v_mov_b32_e32 v92, v93
	v_mov_b32_e32 v93, v94
	v_mov_b32_e32 v94, v83
	v_mov_b32_e32 v95, v81
	v_pk_mov_b32 v[88:89], v[130:131], v[88:89] op_sel:[1,0]
	v_pk_fma_f32 v[86:87], v[92:93], v[116:117], v[86:87]
	v_mov_b32_e32 v92, v82
	v_mov_b32_e32 v93, v80
	v_pk_mul_f32 v[88:89], v[94:95], v[88:89]
	v_and_b32_e32 v127, 0xffff0000, v91
	v_pk_fma_f32 v[102:103], v[92:93], v[102:103], v[88:89] neg_lo:[0,0,1] neg_hi:[0,0,1]
	v_mov_b32_e32 v88, v80
	v_mov_b32_e32 v89, v83
	v_and_b32_e32 v126, 16, v90
	v_and_b32_e32 v91, 16, v91
	v_and_b32_e32 v90, 0xffff0000, v90
	v_mov_b32_e32 v113, v131
	v_pk_mul_f32 v[88:89], v[88:89], v[114:115]
	v_mov_b32_e32 v80, v81
	v_mov_b32_e32 v81, v82
	v_mov_b32_e32 v110, v90
	v_pk_fma_f32 v[80:81], v[80:81], v[112:113], v[88:89]
	v_mov_b32_e32 v88, v79
	v_mov_b32_e32 v89, v77
	v_pk_mov_b32 v[90:91], v[126:127], v[90:91] op_sel:[1,0]
	v_mov_b32_e32 v82, v78
	v_mov_b32_e32 v83, v76
	v_pk_mul_f32 v[88:89], v[88:89], v[90:91]
	v_mov_b32_e32 v109, v127
	v_pk_fma_f32 v[100:101], v[82:83], v[100:101], v[88:89] neg_lo:[0,0,1] neg_hi:[0,0,1]
	v_mov_b32_e32 v82, v76
	v_mov_b32_e32 v83, v79
	v_pk_mul_f32 v[82:83], v[82:83], v[110:111]
	v_mov_b32_e32 v76, v77
	v_mov_b32_e32 v77, v78
	v_pk_fma_f32 v[76:77], v[76:77], v[108:109], v[82:83]
	s_mov_b32 s5, 39
	s_branch .LBB0_531

; DEVI void ret_decays(int h, float& ldf, float& ldb) { ldf = log1pf(-exp2f(-(5.f + 2.f * h))); ldb = log1pf(-exp2f(-(6.f + 2.f * h))); }
; DEVI void ret_rot(const bf16x8 r0, const bf16x8 r1, const RetIn& in, bool lat, float scale, float (&o)[16]) {
;     float a[8], c[8]; unpack8(r0, a); unpack8(r1, c);
; #pragma unroll
;     for (int i = 0; i < 8; ++i) { o[i] = a[i]; o[8 + i] = c[i]; }
;     if (lat) {
; #pragma unroll
;         for (int q = 0; q < 4; ++q) { const f32x4 cs = (q == 0) ? in.cs0 : (q == 1) ? in.cs1 : (q == 2) ? in.cs2 : in.cs3;
;             const float x1 = o[4 * q], x2 = o[4 * q + 1], y1 = o[4 * q + 2], y2 = o[4 * q + 3];
;             o[4 * q] = x1 * cs[0] - x2 * cs[1]; o[4 * q + 1] = x1 * cs[1] + x2 * cs[0];
;             o[4 * q + 2] = y1 * cs[2] - y2 * cs[3]; o[4 * q + 3] = y1 * cs[3] + y2 * cs[2]; }
;     }
; #pragma unroll
;     for (int i = 0; i < 16; ++i) o[i] *= scale;
; }
.LBB0_531:
	s_lshl_b32 s6, s6, 1
	s_and_b32 s7, s6, 6
	s_add_i32 s16, s7, 6
	v_cvt_f32_ubyte0_e32 v1, s16
	s_mov_b32 s25, 0x42fc0000
	v_cmp_lt_f32_e32 vcc, s25, v1
	s_and_b64 s[16:17], vcc, exec
	s_cselect_b32 s16, 0xffffffc0, 0
	v_cndmask_b32_e32 v2, 0, v226, vcc
	v_sub_f32_e32 v1, v2, v1
	v_exp_f32_e32 v1, v1
	s_mov_b32 s29, 0x3f2aaaab
	s_mov_b32 s33, 0x3f317218
	s_mov_b32 s28, 0x33800000
	v_ldexp_f32 v1, v1, s16
	v_sub_f32_e32 v2, 1.0, v1
	v_cvt_f64_f32_e32 v[78:79], v2
	v_frexp_exp_i32_f64_e32 v78, v[78:79]
	v_frexp_mant_f32_e32 v79, v2
	v_cmp_gt_f32_e64 s[38:39], s29, v79
	v_add_f32_e32 v90, -1.0, v2
	v_sub_f32_e64 v91, -v1, v90
	v_subbrev_co_u32_e64 v78, s[38:39], 0, v78, s[38:39]
	v_cvt_f32_i32_e32 v79, v78
	v_sub_u32_e32 v78, 0, v78
	v_ldexp_f32 v88, v2, v78
	v_sub_f32_e32 v2, v90, v2
	v_add_f32_e32 v2, 1.0, v2
	v_add_f32_e32 v89, -1.0, v88
	v_add_f32_e32 v2, v91, v2
	v_add_f32_e32 v91, 1.0, v88
	v_ldexp_f32 v2, v2, v78
	v_add_f32_e32 v78, 1.0, v89
	v_add_f32_e32 v92, -1.0, v91
	v_sub_f32_e32 v78, v88, v78
	v_sub_f32_e32 v88, v88, v92
	v_add_f32_e32 v78, v2, v78
	v_add_f32_e32 v2, v2, v88
	v_add_f32_e32 v88, v91, v2
	v_rcp_f32_e32 v92, v88
	v_add_f32_e32 v90, v89, v78
	v_sub_f32_e32 v91, v88, v91
	v_sub_f32_e32 v2, v2, v91
	v_mul_f32_e32 v93, v90, v92
	v_mul_f32_e32 v94, v88, v93
	v_fma_f32 v91, v93, v88, -v94
	v_fmac_f32_e32 v91, v93, v2
	v_add_f32_e32 v95, v94, v91
	v_sub_f32_e32 v96, v90, v95
	v_sub_f32_e32 v89, v90, v89
	v_sub_f32_e32 v78, v78, v89
	v_sub_f32_e32 v89, v90, v96
	v_sub_f32_e32 v94, v95, v94
	v_sub_f32_e32 v89, v89, v95
	v_sub_f32_e32 v91, v94, v91
	v_add_f32_e32 v78, v78, v89
	v_add_f32_e32 v78, v91, v78
	v_add_f32_e32 v89, v96, v78
	v_mul_f32_e32 v90, v92, v89
	v_mul_f32_e32 v94, v88, v90
	v_fma_f32 v88, v90, v88, -v94
	v_add_f32_e32 v91, v93, v90
	v_fmac_f32_e32 v88, v90, v2
	v_sub_f32_e32 v93, v91, v93
	v_add_f32_e32 v2, v94, v88
	v_sub_f32_e32 v93, v90, v93
	v_sub_f32_e32 v90, v89, v2
	v_sub_f32_e32 v94, v2, v94
	v_sub_f32_e32 v88, v94, v88
	v_sub_f32_e32 v94, v96, v89
	v_sub_f32_e32 v89, v89, v90
	v_add_f32_e32 v78, v78, v94
	v_sub_f32_e32 v2, v89, v2
	v_add_f32_e32 v2, v78, v2
	v_add_f32_e32 v2, v88, v2
	v_add_f32_e32 v2, v90, v2
	v_mul_f32_e32 v2, v92, v2
	v_add_f32_e32 v2, v93, v2
	v_add_f32_e32 v78, v91, v2
	v_mul_f32_e32 v89, v78, v78
	v_fmamk_f32 v92, v89, 0x3e9b6dac, v224
	v_mul_f32_e32 v90, v78, v89
	v_fmaak_f32 v89, v89, v92, 0x3f2aaada
	v_ldexp_f32 v88, v78, 1
	v_mul_f32_e32 v89, v90, v89
	v_add_f32_e32 v90, v88, v89
	v_sub_f32_e32 v78, v78, v91
	v_mul_f32_e32 v82, 0x3f317218, v79
	v_sub_f32_e32 v2, v2, v78
	v_sub_f32_e32 v78, v90, v88
	v_fma_f32 v83, v79, s33, -v82
	v_ldexp_f32 v2, v2, 1
	v_sub_f32_e32 v78, v89, v78
	v_fmac_f32_e32 v83, 0xb102e308, v79
	v_add_f32_e32 v2, v2, v78
	v_add_f32_e32 v79, v82, v83
	v_add_f32_e32 v78, v90, v2
	v_add_f32_e32 v88, v79, v78
	v_sub_f32_e32 v82, v79, v82
	v_sub_f32_e32 v82, v83, v82
	v_sub_f32_e32 v83, v78, v90
	v_sub_f32_e32 v89, v88, v79
	v_sub_f32_e32 v2, v2, v83
	v_sub_f32_e32 v78, v78, v89
	v_sub_f32_e32 v89, v88, v89
	v_add_f32_e32 v83, v82, v2
	v_sub_f32_e32 v79, v79, v89
	v_add_f32_e32 v78, v78, v79
	v_sub_f32_e32 v89, v83, v82
	v_add_f32_e32 v78, v83, v78
	v_sub_f32_e32 v83, v83, v89
	v_add_f32_e32 v79, v88, v78
	v_sub_f32_e32 v2, v2, v89
	v_sub_f32_e32 v82, v82, v83
	v_add_f32_e32 v2, v2, v82
	v_sub_f32_e32 v82, v79, v88
	v_sub_f32_e32 v78, v78, v82
	v_add_f32_e32 v2, v2, v78
	v_add_f32_e32 v2, v79, v2
	v_cmp_nlt_f32_e64 s[38:39], 1.0, v1
	v_cmp_gt_f32_e32 vcc, s28, v1
	s_add_i32 s7, s7, 5
	v_cndmask_b32_e64 v2, v231, v2, s[38:39]
	v_cmp_neq_f32_e64 s[38:39], 1.0, v1
	v_mul_f32_e32 v84, 0x3db504f3, v84
	v_mul_f32_e32 v85, 0x3db504f3, v85
	v_cndmask_b32_e64 v2, v234, v2, s[38:39]
	v_cndmask_b32_e64 v1, v2, -v1, vcc
	v_cvt_f32_ubyte0_e32 v2, s7
	v_cmp_lt_f32_e32 vcc, s25, v2
	s_and_b64 s[16:17], vcc, exec
	s_cselect_b32 s7, 0xffffffc0, 0
	v_cndmask_b32_e32 v78, 0, v226, vcc
	v_sub_f32_e32 v2, v78, v2
	v_exp_f32_e32 v2, v2
	v_mul_f32_e32 v86, 0x3db504f3, v86
	v_mul_f32_e32 v87, 0x3db504f3, v87
	v_mul_f32_e32 v80, 0x3db504f3, v80
	v_ldexp_f32 v2, v2, s7
	v_sub_f32_e32 v82, 1.0, v2
	v_cvt_f64_f32_e32 v[78:79], v82
	v_frexp_exp_i32_f64_e32 v78, v[78:79]
	v_frexp_mant_f32_e32 v79, v82
	v_cmp_gt_f32_e64 s[38:39], s29, v79
	v_add_f32_e32 v91, -1.0, v82
	v_sub_f32_e64 v92, -v2, v91
	v_subbrev_co_u32_e64 v78, s[38:39], 0, v78, s[38:39]
	v_cvt_f32_i32_e32 v79, v78
	v_sub_u32_e32 v78, 0, v78
	v_ldexp_f32 v89, v82, v78
	v_sub_f32_e32 v82, v91, v82
	v_add_f32_e32 v82, 1.0, v82
	v_add_f32_e32 v90, -1.0, v89
	v_add_f32_e32 v82, v92, v82
	v_add_f32_e32 v92, 1.0, v89
	v_ldexp_f32 v78, v82, v78
	v_add_f32_e32 v82, 1.0, v90
	v_add_f32_e32 v93, -1.0, v92
	v_sub_f32_e32 v82, v89, v82
	v_sub_f32_e32 v89, v89, v93
	v_add_f32_e32 v82, v78, v82
	v_add_f32_e32 v78, v78, v89
	v_add_f32_e32 v89, v92, v78
	v_rcp_f32_e32 v93, v89
	v_add_f32_e32 v91, v90, v82
	v_sub_f32_e32 v92, v89, v92
	v_sub_f32_e32 v78, v78, v92
	v_mul_f32_e32 v94, v91, v93
	v_mul_f32_e32 v95, v89, v94
	v_fma_f32 v92, v94, v89, -v95
	v_fmac_f32_e32 v92, v94, v78
	v_add_f32_e32 v96, v95, v92
	v_sub_f32_e32 v97, v91, v96
	v_sub_f32_e32 v90, v91, v90
	v_sub_f32_e32 v82, v82, v90
	v_sub_f32_e32 v90, v91, v97
	v_sub_f32_e32 v95, v96, v95
	v_sub_f32_e32 v90, v90, v96
	v_sub_f32_e32 v92, v95, v92
	v_add_f32_e32 v82, v82, v90
	v_add_f32_e32 v82, v92, v82
	v_add_f32_e32 v90, v97, v82
	v_mul_f32_e32 v91, v93, v90
	v_mul_f32_e32 v95, v89, v91
	v_fma_f32 v89, v91, v89, -v95
	v_add_f32_e32 v92, v94, v91
	v_fmac_f32_e32 v89, v91, v78
	v_sub_f32_e32 v94, v92, v94
	v_add_f32_e32 v78, v95, v89
	v_sub_f32_e32 v94, v91, v94
; DEVI bf16_t f2bf(float x) { return (bf16_t)(cvt_pk(x, 0.f) & 0xffffu); }
; DEVI int opaque_tid() { int t = threadIdx.x; asm volatile("" : "+v"(t)); return t; }
; DEVI void ret_decays(int h, float& ldf, float& ldb) { ldf = log1pf(-exp2f(-(5.f + 2.f * h))); ldb = log1pf(-exp2f(-(6.f + 2.f * h))); }
; DEVI void scan_a_ret(const Params& p, int l, int b, int h, int c, const RetIn& in, char* smem) {
;     bf16_t* kTf = (bf16_t*)smem; bf16_t* kTb = kTf + 128 * 72; bf16_t* vT = kTb + 128 * 72;
;     const int tid = opaque_tid(), wid = tid >> 6, lane = tid & 63, fr = lane & 15, fq = lane >> 4;
;     const bool lat = c >= 4;
;     const int tk = tid >> 3, kk16 = (tid & 7) * 16;
;     float ldf, ldb; ret_decays(h, ldf, ldb);
;     float kf[16];
;     ret_rot(in.k0, in.k1, in, lat, 0.08838834764831845f, kf);
;     const float ef = __expf(ldf * (float)(63 - tk)), eb = __expf(ldb * (float)tk);
; #pragma unroll
;     for (int e = 0; e < 16; ++e) { kTf[(kk16 + e) * 72 + tk] = f2bf(kf[e] * ef); kTb[(kk16 + e) * 72 + tk] = f2bf(kf[e] * eb); }
	v_sub_f32_e32 v91, v90, v78
	v_sub_f32_e32 v95, v78, v95
	v_sub_f32_e32 v89, v95, v89
	v_sub_f32_e32 v95, v97, v90
	v_sub_f32_e32 v90, v90, v91
	v_add_f32_e32 v82, v82, v95
	v_sub_f32_e32 v78, v90, v78
	v_add_f32_e32 v78, v82, v78
	v_add_f32_e32 v78, v89, v78
	v_add_f32_e32 v78, v91, v78
	v_mul_f32_e32 v78, v93, v78
	v_add_f32_e32 v78, v94, v78
	v_add_f32_e32 v82, v92, v78
	v_mul_f32_e32 v90, v82, v82
	v_fmamk_f32 v93, v90, 0x3e9b6dac, v224
	v_mul_f32_e32 v91, v82, v90
	v_fmaak_f32 v90, v90, v93, 0x3f2aaada
	v_ldexp_f32 v89, v82, 1
	v_mul_f32_e32 v90, v91, v90
	v_add_f32_e32 v91, v89, v90
	v_sub_f32_e32 v82, v82, v92
	v_mul_f32_e32 v83, 0x3f317218, v79
	v_sub_f32_e32 v78, v78, v82
	v_sub_f32_e32 v82, v91, v89
	v_fma_f32 v88, v79, s33, -v83
	v_ldexp_f32 v78, v78, 1
	v_sub_f32_e32 v82, v90, v82
	v_fmac_f32_e32 v88, 0xb102e308, v79
	v_add_f32_e32 v78, v78, v82
	v_add_f32_e32 v79, v83, v88
	v_add_f32_e32 v82, v91, v78
	v_add_f32_e32 v89, v79, v82
	v_sub_f32_e32 v83, v79, v83
	v_sub_f32_e32 v83, v88, v83
	v_sub_f32_e32 v88, v82, v91
	v_sub_f32_e32 v90, v89, v79
	v_sub_f32_e32 v78, v78, v88
	v_sub_f32_e32 v82, v82, v90
	v_sub_f32_e32 v90, v89, v90
	v_add_f32_e32 v88, v83, v78
	v_sub_f32_e32 v79, v79, v90
	v_add_f32_e32 v79, v82, v79
	v_sub_f32_e32 v90, v88, v83
	v_add_f32_e32 v79, v88, v79
	v_sub_f32_e32 v88, v88, v90
	v_add_f32_e32 v82, v89, v79
	v_sub_f32_e32 v78, v78, v90
	v_sub_f32_e32 v83, v83, v88
	v_add_f32_e32 v78, v78, v83
	v_sub_f32_e32 v83, v82, v89
	v_sub_f32_e32 v79, v79, v83
	v_add_f32_e32 v78, v78, v79
	v_ashrrev_i32_e32 v79, 3, v124
	v_sub_u32_e32 v96, 63, v79
	v_add_f32_e32 v78, v82, v78
	v_cmp_nlt_f32_e64 s[38:39], 1.0, v2
	v_cvt_f32_i32_e32 v96, v96
	v_cmp_gt_f32_e32 vcc, s28, v2
	v_cndmask_b32_e64 v78, v231, v78, s[38:39]
	v_cmp_neq_f32_e64 s[38:39], 1.0, v2
	v_mul_f32_e32 v83, 0x3db504f3, v107
	s_movk_i32 s7, 0x48
	v_cndmask_b32_e64 v78, v234, v78, s[38:39]
	v_cndmask_b32_e64 v2, v78, -v2, vcc
	v_mul_f32_e32 v2, v2, v96
	v_cvt_f32_i32_e32 v96, v79
	v_mul_f32_e32 v2, 0x3fb8aa3b, v2
	v_exp_f32_e32 v2, v2
	v_lshlrev_b32_e32 v78, 4, v124
	v_mul_f32_e32 v1, v1, v96
	v_mul_f32_e32 v1, 0x3fb8aa3b, v1
	v_exp_f32_e32 v1, v1
	v_and_b32_e32 v78, 0x70, v78
	v_mul_f32_e32 v96, v2, v83
	v_mul_u32_u24_e32 v97, 0x48, v78
	v_mad_u32_u24 v78, v78, s7, v79
	v_mul_f32_e32 v83, v1, v83
	v_lshl_add_u32 v78, v78, 1, 0
	v_cvt_pk_bf16_f32 v83, v83, s0
	ds_write_b16 v78, v83 offset:18432
	v_mul_f32_e32 v83, v2, v84
	v_cvt_pk_bf16_f32 v83, v83, s0
	ds_write_b16 v78, v83 offset:144
	v_mul_f32_e32 v83, v1, v84
	v_mul_f32_e32 v89, 0x3db504f3, v106
	v_cvt_pk_bf16_f32 v83, v83, s0
	ds_write_b16 v78, v83 offset:18576
	v_mul_f32_e32 v83, v2, v89
	v_cvt_pk_bf16_f32 v83, v83, s0
	ds_write_b16 v78, v83 offset:288
	v_mul_f32_e32 v83, v1, v89
	v_cvt_pk_bf16_f32 v83, v83, s0
	ds_write_b16 v78, v83 offset:18720
	v_mul_f32_e32 v83, v2, v85
	v_cvt_pk_bf16_f32 v83, v83, s0
	ds_write_b16 v78, v83 offset:432
	v_mul_f32_e32 v83, v1, v85
	v_mul_f32_e32 v90, 0x3db504f3, v105
	v_cvt_pk_bf16_f32 v83, v83, s0
	ds_write_b16 v78, v83 offset:18864
	v_mul_f32_e32 v83, v2, v90
	v_cvt_pk_bf16_f32 v83, v83, s0
	ds_write_b16 v78, v83 offset:576
	v_mul_f32_e32 v83, v1, v90
	v_cvt_pk_bf16_f32 v83, v83, s0
	ds_write_b16 v78, v83 offset:19008
	v_mul_f32_e32 v83, v2, v86
	v_cvt_pk_bf16_f32 v83, v83, s0
	ds_write_b16 v78, v83 offset:720
	v_mul_f32_e32 v83, v1, v86
	v_mul_f32_e32 v91, 0x3db504f3, v104
	v_cvt_pk_bf16_f32 v83, v83, s0
	ds_write_b16 v78, v83 offset:19152
	v_mul_f32_e32 v83, v2, v91
	v_cvt_pk_bf16_f32 v83, v83, s0
	ds_write_b16 v78, v83 offset:864
	v_mul_f32_e32 v83, v1, v91
	v_cvt_pk_bf16_f32 v83, v83, s0
	ds_write_b16 v78, v83 offset:19296
	v_mul_f32_e32 v83, v2, v87
	v_cvt_pk_bf16_f32 v83, v83, s0
	ds_write_b16 v78, v83 offset:1008
	v_mul_f32_e32 v83, v1, v87
	v_mul_f32_e32 v92, 0x3db504f3, v103
	v_cvt_pk_bf16_f32 v83, v83, s0
	ds_write_b16 v78, v83 offset:19440
	v_mul_f32_e32 v83, v2, v92
	v_cvt_pk_bf16_f32 v83, v83, s0
	ds_write_b16 v78, v83 offset:1152
	v_mul_f32_e32 v83, v1, v92
	v_cvt_pk_bf16_f32 v83, v83, s0
	ds_write_b16 v78, v83 offset:19584
	v_mul_f32_e32 v83, v2, v80
	v_mul_f32_e32 v80, v1, v80
	v_mul_f32_e32 v93, 0x3db504f3, v102
	v_cvt_pk_bf16_f32 v80, v80, s0
	ds_write_b16 v78, v80 offset:19728
	v_mul_f32_e32 v80, v2, v93
	v_cvt_pk_bf16_f32 v80, v80, s0
	ds_write_b16 v78, v80 offset:1440
	v_mul_f32_e32 v80, v1, v93
	v_mul_f32_e32 v81, 0x3db504f3, v81
	v_cvt_pk_bf16_f32 v80, v80, s0
	ds_write_b16 v78, v80 offset:19872
	v_mul_f32_e32 v80, v2, v81
	v_cvt_pk_bf16_f32 v80, v80, s0
	ds_write_b16 v78, v80 offset:1584
	v_mul_f32_e32 v80, v1, v81
	v_mul_f32_e32 v94, 0x3db504f3, v101
	v_cvt_pk_bf16_f32 v80, v80, s0
	ds_write_b16 v78, v80 offset:20016
	v_mul_f32_e32 v80, v2, v94
	v_cvt_pk_bf16_f32 v80, v80, s0
	ds_write_b16 v78, v80 offset:1728
	v_mul_f32_e32 v80, v1, v94
	v_mul_f32_e32 v76, 0x3db504f3, v76
	v_cvt_pk_bf16_f32 v80, v80, s0
	ds_write_b16 v78, v80 offset:20160
	v_mul_f32_e32 v80, v2, v76
	v_mul_f32_e32 v76, v1, v76
	v_mul_f32_e32 v95, 0x3db504f3, v100
	v_cvt_pk_bf16_f32 v76, v76, s0
	ds_write_b16 v78, v76 offset:20304
	v_mul_f32_e32 v76, v2, v95
	v_mul_f32_e32 v77, 0x3db504f3, v77
	v_cvt_pk_bf16_f32 v76, v76, s0
	ds_write_b16 v78, v76 offset:2016
	v_mul_f32_e32 v76, v1, v95
	v_mul_f32_e32 v2, v2, v77
	v_mul_f32_e32 v1, v1, v77
	v_cvt_pk_bf16_f32 v2, v2, s0
	v_cvt_pk_bf16_f32 v1, v1, s0
	v_cvt_pk_bf16_f32 v76, v76, s0
	ds_write_b16 v78, v2 offset:2160
	ds_write_b16 v78, v1 offset:20592
	v_lshlrev_b32_e32 v1, 1, v79
	v_lshlrev_b32_e32 v2, 1, v97
	v_readlane_b32 s7, v254, 45
	v_cvt_pk_bf16_f32 v96, v96, s0
	v_cvt_pk_bf16_f32 v83, v83, s0
	v_cvt_pk_bf16_f32 v80, v80, s0
; DEVI unsigned cvt_pk(float lo, float hi) { f32x2 v = {lo, hi}; bf16x2_t b = __builtin_convertvector(v, bf16x2_t); return __builtin_bit_cast(unsigned, b); }
; DEVI void scan_a_ret(const Params& p, int l, int b, int h, int c, const RetIn& in, char* smem) {
;     ...
;     {   const bf16x8 v0 = in.v0, v1 = in.v1;
; #pragma unroll
;         for (int e = 0; e < 8; ++e) { vT[(kk16 + e) * 72 + tk] = (bf16_t)v0[e]; vT[(kk16 + 8 + e) * 72 + tk] = (bf16_t)v1[e]; } }
;     __syncthreads();
;     {   const int dir = wid >> 2;
;         const bf16_t* kT = dir ? kTb : kTf;
;         bf16_t* UT = (bf16_t*)(p.ws + WS_UTR) + ((size_t)((b * 4 + h) * 2 + dir) * NCH + order_idx(dir, c)) * (128 * 128);
; #pragma unroll
;         for (int q = 0; q < 2; ++q) { const int kkf = (wid & 3) * 2 + q;
;             const bf16x8 a0 = ldfrag(kT, 72, kkf * 16, 0, fr, fq), a1 = ldfrag(kT, 72, kkf * 16, 32, fr, fq);
; #pragma unroll
;             for (int vf = 0; vf < 8; ++vf) {
;                 f32x4 acc = {0.f, 0.f, 0.f, 0.f};
;                 acc = __builtin_amdgcn_mfma_f32_16x16x32_bf16(a0, ldfrag(vT, 72, vf * 16, 0, fr, fq), acc, 0, 0, 0);
;                 acc = __builtin_amdgcn_mfma_f32_16x16x32_bf16(a1, ldfrag(vT, 72, vf * 16, 32, fr, fq), acc, 0, 0, 0);
;                 *(u32x2*)(UT + (vf * 16 + fr) * 128 + kkf * 16 + fq * 4) = (u32x2){cvt_pk(acc[0], acc[1]), cvt_pk(acc[2], acc[3])};
;             } }
	ds_write_b16 v78, v76 offset:20448
	v_add3_u32 v76, 0, v1, v2
	v_add3_u32 v1, 0, v2, v1
	v_cmp_gt_u32_e32 vcc, s92, v124
	v_mov_b32_e32 v2, s7
	s_sub_i32 s5, s5, s4
	ds_write_b16 v78, v96
	ds_write_b16 v78, v83 offset:1296
	ds_write_b16 v78, v80 offset:1872
	ds_write_b16 v76, v68 offset:36864
	ds_write_b16 v1, v72 offset:38016
	ds_write_b16_d16_hi v76, v68 offset:37008
	ds_write_b16_d16_hi v1, v72 offset:38160
	ds_write_b16 v76, v69 offset:37152
	ds_write_b16 v1, v73 offset:38304
	ds_write_b16_d16_hi v76, v69 offset:37296
	ds_write_b16_d16_hi v1, v73 offset:38448
	ds_write_b16 v76, v70 offset:37440
	ds_write_b16 v1, v74 offset:38592
	ds_write_b16_d16_hi v76, v70 offset:37584
	ds_write_b16_d16_hi v1, v74 offset:38736
	ds_write_b16 v76, v71 offset:37728
	ds_write_b16 v1, v75 offset:38880
	ds_write_b16_d16_hi v76, v71 offset:37872
	ds_write_b16_d16_hi v1, v75 offset:39024
	v_cndmask_b32_e64 v98, v2, 0, vcc
	v_mov_b32_e32 v2, s5
	v_mov_b32_e32 v68, s4
	v_ashrrev_i32_e32 v1, 8, v124
	v_cndmask_b32_e32 v68, v2, v68, vcc
	v_add_u32_e32 v1, s6, v1
	v_ashrrev_i32_e32 v69, 31, v68
	v_mad_i64_i32 v[68:69], s[4:5], v1, 36, v[68:69]
	v_readlane_b32 s4, v254, 6
	v_bfe_u32 v82, v124, 4, 2
	v_lshlrev_b64 v[68:69], 15, v[68:69]
	v_readlane_b32 s5, v254, 7
	v_lshlrev_b32_e32 v2, 3, v82
	v_and_b32_e32 v88, 15, v124
	v_lshl_add_u64 v[68:69], s[4:5], 0, v[68:69]
	v_lshl_add_u64 v[76:77], v[68:69], 0, v[2:3]
	v_lshrrev_b32_e32 v2, 1, v124
	v_and_b32_e32 v2, 0x60, v2
	v_or_b32_e32 v100, v2, v88
	v_mul_u32_u24_e32 v1, 0x90, v88
	v_lshlrev_b32_e32 v99, 4, v82
	v_mul_u32_u24_e32 v68, 0x90, v100
	v_add3_u32 v1, 0, v1, v99
	v_add3_u32 v72, v98, v68, v99
	v_lshlrev_b32_e32 v2, 1, v2
	s_waitcnt lgkmcnt(0)
	s_barrier
	ds_read_b128 v[68:71], v72
	ds_read_b128 v[72:75], v72 offset:64
	v_lshl_add_u64 v[96:97], v[76:77], 0, v[2:3]
	ds_read_b128 v[76:79], v1 offset:36864
	ds_read_b128 v[80:83], v1 offset:36928
	s_waitcnt lgkmcnt(1)
	v_mfma_f32_16x16x32_bf16 v[76:79], v[68:71], v[76:79], 0
	v_lshlrev_b32_e32 v2, 8, v88
	v_lshl_add_u64 v[90:91], v[96:97], 0, v[2:3]
	ds_read_b128 v[92:95], v1 offset:48448
	s_waitcnt lgkmcnt(1)
	v_mfma_f32_16x16x32_bf16 v[76:79], v[72:75], v[80:83], v[76:79]
	ds_read_b128 v[80:83], v1 offset:39232
	s_mov_b64 s[28:29], -1
	s_and_b64 vcc, s[44:45], exec
	s_nop 4
	v_cvt_pk_bf16_f32 v76, v76, v77
	v_cvt_pk_bf16_f32 v77, v78, v79
	global_store_dwordx2 v[90:91], v[76:77], off
	ds_read_b128 v[76:79], v1 offset:39168
	s_waitcnt lgkmcnt(0)
	v_mfma_f32_16x16x32_bf16 v[76:79], v[68:71], v[76:79], 0
	v_mfma_f32_16x16x32_bf16 v[76:79], v[72:75], v[80:83], v[76:79]
	ds_read_b128 v[80:83], v1 offset:41536
	s_nop 6
	v_cvt_pk_bf16_f32 v76, v76, v77
	v_cvt_pk_bf16_f32 v77, v78, v79
	v_or_b32_e32 v78, 0x1000, v2
	v_mov_b32_e32 v79, v3
	v_lshl_add_u64 v[88:89], v[96:97], 0, v[78:79]
	global_store_dwordx2 v[88:89], v[76:77], off
	ds_read_b128 v[76:79], v1 offset:41472
	s_waitcnt lgkmcnt(0)
	v_mfma_f32_16x16x32_bf16 v[76:79], v[68:71], v[76:79], 0
	v_mfma_f32_16x16x32_bf16 v[76:79], v[72:75], v[80:83], v[76:79]
	ds_read_b128 v[80:83], v1 offset:43840
	s_nop 6
	v_cvt_pk_bf16_f32 v76, v76, v77
	v_cvt_pk_bf16_f32 v77, v78, v79
	v_or_b32_e32 v78, 0x2000, v2
	v_mov_b32_e32 v79, v3
	v_lshl_add_u64 v[86:87], v[96:97], 0, v[78:79]
	global_store_dwordx2 v[86:87], v[76:77], off
	ds_read_b128 v[76:79], v1 offset:43776
	s_waitcnt lgkmcnt(0)
	v_mfma_f32_16x16x32_bf16 v[76:79], v[68:71], v[76:79], 0
	v_mfma_f32_16x16x32_bf16 v[76:79], v[72:75], v[80:83], v[76:79]
	ds_read_b128 v[80:83], v1 offset:46144
	s_nop 6
	v_cvt_pk_bf16_f32 v76, v76, v77
	v_cvt_pk_bf16_f32 v77, v78, v79
	v_or_b32_e32 v78, 0x3000, v2
	v_mov_b32_e32 v79, v3
	v_lshl_add_u64 v[84:85], v[96:97], 0, v[78:79]
	global_store_dwordx2 v[84:85], v[76:77], off
	ds_read_b128 v[76:79], v1 offset:46080
	s_waitcnt lgkmcnt(0)
	v_mfma_f32_16x16x32_bf16 v[76:79], v[68:71], v[76:79], 0
	v_mfma_f32_16x16x32_bf16 v[76:79], v[72:75], v[80:83], v[76:79]
	s_nop 7
	v_cvt_pk_bf16_f32 v76, v76, v77
	v_cvt_pk_bf16_f32 v77, v78, v79
	v_or_b32_e32 v78, 0x4000, v2
	v_mov_b32_e32 v79, v3
	v_lshl_add_u64 v[82:83], v[96:97], 0, v[78:79]
	global_store_dwordx2 v[82:83], v[76:77], off
	ds_read_b128 v[76:79], v1 offset:48384
	s_waitcnt lgkmcnt(0)
	v_mfma_f32_16x16x32_bf16 v[76:79], v[68:71], v[76:79], 0
	v_mfma_f32_16x16x32_bf16 v[76:79], v[72:75], v[92:95], v[76:79]
	ds_read_b128 v[92:95], v1 offset:50752
	s_nop 6
	v_cvt_pk_bf16_f32 v76, v76, v77
	v_cvt_pk_bf16_f32 v77, v78, v79
	v_or_b32_e32 v78, 0x5000, v2
	v_mov_b32_e32 v79, v3
	v_lshl_add_u64 v[80:81], v[96:97], 0, v[78:79]
	global_store_dwordx2 v[80:81], v[76:77], off
	ds_read_b128 v[76:79], v1 offset:50688
	s_waitcnt lgkmcnt(0)
; DEVI unsigned cvt_pk(float lo, float hi) { f32x2 v = {lo, hi}; bf16x2_t b = __builtin_convertvector(v, bf16x2_t); return __builtin_bit_cast(unsigned, b); }
; DEVI void cvt8_finish(const Params& p, int L, int t, const CvtIn& in, char* smem) {
;     const int which = t / 4096, r = t % 4096, le = L * 16 + r / 256, kt = (r % 256) / 16, nt = r % 16;
;     unsigned char* dst = (which == 2) ? (unsigned char*)(p.ws + WS_WDN) + (size_t)le * 2048 * 2048 + (size_t)(nt * 128) * 2048
;                                       : (unsigned char*)(p.ws + WS_WGU) + (size_t)le * 4096 * 2048 + (size_t)(nt * 256 + which * 128) * 2048;
; DEVI void scan_a_ret(const Params& p, int l, int b, int h, int c, const RetIn& in, char* smem) {
;     ...
;         for (int q = 0; q < 2; ++q) { const int kkf = (wid & 3) * 2 + q;
;             const bf16x8 a0 = ldfrag(kT, 72, kkf * 16, 0, fr, fq), a1 = ldfrag(kT, 72, kkf * 16, 32, fr, fq);
; #pragma unroll
;             for (int vf = 0; vf < 8; ++vf) {
;                 f32x4 acc = {0.f, 0.f, 0.f, 0.f};
;                 acc = __builtin_amdgcn_mfma_f32_16x16x32_bf16(a0, ldfrag(vT, 72, vf * 16, 0, fr, fq), acc, 0, 0, 0);
;                 acc = __builtin_amdgcn_mfma_f32_16x16x32_bf16(a1, ldfrag(vT, 72, vf * 16, 32, fr, fq), acc, 0, 0, 0);
;                 *(u32x2*)(UT + (vf * 16 + fr) * 128 + kkf * 16 + fq * 4) = (u32x2){cvt_pk(acc[0], acc[1]), cvt_pk(acc[2], acc[3])};
;             } }
;     }
;     __syncthreads();
	v_mfma_f32_16x16x32_bf16 v[76:79], v[68:71], v[76:79], 0
	v_mfma_f32_16x16x32_bf16 v[76:79], v[72:75], v[92:95], v[76:79]
	ds_read_b128 v[92:95], v1 offset:52992
	s_waitcnt lgkmcnt(0)
	v_mfma_f32_16x16x32_bf16 v[68:71], v[68:71], v[92:95], 0
	ds_read_b128 v[92:95], v1 offset:53056
	s_nop 3
	v_cvt_pk_bf16_f32 v76, v76, v77
	v_cvt_pk_bf16_f32 v77, v78, v79
	s_waitcnt lgkmcnt(0)
	v_mfma_f32_16x16x32_bf16 v[68:71], v[72:75], v[92:95], v[68:71]
	v_or_b32_e32 v78, 0x6000, v2
	v_mov_b32_e32 v79, v3
	v_lshl_add_u64 v[78:79], v[96:97], 0, v[78:79]
	v_or_b32_e32 v2, 0x7000, v2
	global_store_dwordx2 v[78:79], v[76:77], off
	v_lshl_add_u64 v[76:77], v[96:97], 0, v[2:3]
	v_or_b32_e32 v2, 16, v100
	s_nop 0
	v_cvt_pk_bf16_f32 v68, v68, v69
	v_cvt_pk_bf16_f32 v69, v70, v71
	v_mul_u32_u24_e32 v2, 0x90, v2
	global_store_dwordx2 v[76:77], v[68:69], off
	v_add3_u32 v2, v98, v2, v99
	ds_read_b128 v[72:75], v2
	ds_read_b128 v[68:71], v2 offset:64
	ds_read_b128 v[92:95], v1 offset:36864
	ds_read_b128 v[96:99], v1 offset:36928
	s_waitcnt lgkmcnt(1)
	v_mfma_f32_16x16x32_bf16 v[92:95], v[72:75], v[92:95], 0
	s_waitcnt lgkmcnt(0)
	v_mfma_f32_16x16x32_bf16 v[92:95], v[68:71], v[96:99], v[92:95]
	s_nop 7
	v_cvt_pk_bf16_f32 v92, v92, v93
	v_cvt_pk_bf16_f32 v93, v94, v95
	global_store_dwordx2 v[90:91], v[92:93], off offset:32
	ds_read_b128 v[90:93], v1 offset:39168
	ds_read_b128 v[94:97], v1 offset:39232
	s_waitcnt lgkmcnt(1)
	v_mfma_f32_16x16x32_bf16 v[90:93], v[72:75], v[90:93], 0
	s_waitcnt lgkmcnt(0)
	v_mfma_f32_16x16x32_bf16 v[90:93], v[68:71], v[94:97], v[90:93]
	s_nop 7
	v_cvt_pk_bf16_f32 v90, v90, v91
	v_cvt_pk_bf16_f32 v91, v92, v93
	global_store_dwordx2 v[88:89], v[90:91], off offset:32
	ds_read_b128 v[88:91], v1 offset:41472
	ds_read_b128 v[92:95], v1 offset:41536
	s_waitcnt lgkmcnt(1)
	v_mfma_f32_16x16x32_bf16 v[88:91], v[72:75], v[88:91], 0
	s_waitcnt lgkmcnt(0)
	v_mfma_f32_16x16x32_bf16 v[88:91], v[68:71], v[92:95], v[88:91]
	s_nop 7
	v_cvt_pk_bf16_f32 v88, v88, v89
	v_cvt_pk_bf16_f32 v89, v90, v91
	global_store_dwordx2 v[86:87], v[88:89], off offset:32
	ds_read_b128 v[86:89], v1 offset:43776
	ds_read_b128 v[90:93], v1 offset:43840
	s_waitcnt lgkmcnt(1)
	v_mfma_f32_16x16x32_bf16 v[86:89], v[72:75], v[86:89], 0
	s_waitcnt lgkmcnt(0)
	v_mfma_f32_16x16x32_bf16 v[86:89], v[68:71], v[90:93], v[86:89]
	s_nop 7
	v_cvt_pk_bf16_f32 v86, v86, v87
	v_cvt_pk_bf16_f32 v87, v88, v89
	global_store_dwordx2 v[84:85], v[86:87], off offset:32
	ds_read_b128 v[84:87], v1 offset:46080
	ds_read_b128 v[88:91], v1 offset:46144
	s_waitcnt lgkmcnt(1)
	v_mfma_f32_16x16x32_bf16 v[84:87], v[72:75], v[84:87], 0
	s_waitcnt lgkmcnt(0)
	v_mfma_f32_16x16x32_bf16 v[84:87], v[68:71], v[88:91], v[84:87]
	s_nop 7
	v_cvt_pk_bf16_f32 v84, v84, v85
	v_cvt_pk_bf16_f32 v85, v86, v87
	global_store_dwordx2 v[82:83], v[84:85], off offset:32
	ds_read_b128 v[82:85], v1 offset:48384
	ds_read_b128 v[86:89], v1 offset:48448
	s_waitcnt lgkmcnt(1)
	v_mfma_f32_16x16x32_bf16 v[82:85], v[72:75], v[82:85], 0
	s_waitcnt lgkmcnt(0)
	v_mfma_f32_16x16x32_bf16 v[82:85], v[68:71], v[86:89], v[82:85]
	s_nop 7
	v_cvt_pk_bf16_f32 v82, v82, v83
	v_cvt_pk_bf16_f32 v83, v84, v85
	global_store_dwordx2 v[80:81], v[82:83], off offset:32
	ds_read_b128 v[80:83], v1 offset:50688
	ds_read_b128 v[84:87], v1 offset:50752
	s_waitcnt lgkmcnt(1)
	v_mfma_f32_16x16x32_bf16 v[80:83], v[72:75], v[80:83], 0
	s_waitcnt lgkmcnt(0)
	v_mfma_f32_16x16x32_bf16 v[80:83], v[68:71], v[84:87], v[80:83]
	s_nop 7
	v_cvt_pk_bf16_f32 v80, v80, v81
	v_cvt_pk_bf16_f32 v81, v82, v83
	global_store_dwordx2 v[78:79], v[80:81], off offset:32
	ds_read_b128 v[78:81], v1 offset:52992
	s_waitcnt lgkmcnt(0)
	v_mfma_f32_16x16x32_bf16 v[72:75], v[72:75], v[78:81], 0
	ds_read_b128 v[78:81], v1 offset:53056
	s_waitcnt lgkmcnt(0)
	v_mfma_f32_16x16x32_bf16 v[68:71], v[68:71], v[78:81], v[72:75]
	s_nop 7
	v_cvt_pk_bf16_f32 v68, v68, v69
	v_cvt_pk_bf16_f32 v69, v70, v71
	global_store_dwordx2 v[76:77], v[68:69], off offset:32
	s_barrier
	s_cbranch_vccz .LBB0_533
	s_ashr_i32 s6, s24, 12
	s_lshl_b64 s[4:5], s[42:43], 23
	s_add_u32 s7, s37, s4
	s_addc_u32 s17, s78, s5
	s_lshl_b32 s4, s23, 8
	s_lshl_b32 s5, s6, 7
	s_add_i32 s4, s4, s5
	s_ashr_i32 s5, s4, 31
	s_lshl_b64 s[4:5], s[4:5], 11
	s_add_u32 s16, s7, s4
	s_addc_u32 s17, s17, s5
	s_mov_b64 s[28:29], 0

; DEVI int obid() { int b = blockIdx.x; asm volatile("" : "+s"(b)); return b; }
; DEVI void phase_l4(const Params& p, int l, char* smem) {
;     ...
;     {
;         const int G = spec ? 256 - 2 * L4NC : gridDim.x, nG = 16 * ncs, c0 = NCH - ncs;
;         int u = spec ? obid() : (obid() + G - (nal + nac) % G) % G;
;         {   GlaIn cur; bool have = u < nG;
;             if (have) gla_load(p, l, (u / ncs) >> 2, (u / ncs) & 3, u % ncs + c0, true, cur);
;             while (have) { const int un = u + G; const bool hn = un < nG; GlaIn nxt;
;                 if (hn) gla_load(p, l, (un / ncs) >> 2, (un / ncs) & 3, un % ncs + c0, true, nxt);
;                 CvtIn ci; cvt8_load(p, l, (l == 0 ? TS0C : TS1C) + u, ci);
.LBB0_704:
	v_readlane_b32 s4, v255, 2
	v_readlane_b32 s5, v255, 3
	s_and_b64 s[4:5], exec, s[4:5]
	s_cselect_b32 s47, s15, 0xc0
	s_andn2_b64 vcc, exec, s[16:17]
	s_cbranch_vccnz .LBB0_743
	v_cvt_f32_ubyte0_e32 v1, s34
	v_rcp_iflag_f32_e32 v1, v1
	v_readlane_b32 s4, v254, 61
	v_readlane_b32 s5, v254, 62
	s_mov_b32 s6, s4
	v_mul_f32_e32 v1, 0x4f7ffffe, v1
	s_lshl_b32 s18, s4, 1
	v_readlane_b32 s4, v254, 49
	v_cvt_u32_f32_e32 v1, v1
	v_readlane_b32 s5, v254, 50
	s_and_b64 s[4:5], s[4:5], exec
	s_movk_i32 s4, 0x2b80
	s_cselect_b32 s19, s4, 0x2c00
	s_sub_i32 s4, 0, s34
	v_readfirstlane_b32 s5, v1
	s_mul_i32 s4, s4, s5
	s_mul_hi_u32 s4, s5, s4
	s_add_i32 s25, s5, s4
	s_lshl_b32 s4, s46, 6
	s_lshl_b32 s23, s6, 4
	s_lshl_b32 s24, s34, 6
	s_add_i32 s33, s4, 0x800
	s_lshl_b32 s37, s47, 6
	s_sub_i32 s50, 0xffffffdc, s46
	s_mov_b32 s4, s46
	s_waitcnt vmcnt(0)

; DEVI int opaque_tid() { int t = threadIdx.x; asm volatile("" : "+v"(t)); return t; }
; DEVI int chunk_row0(int b, int c) { return (c < 4) ? (NLAT + b * CL + c * 64) : (b * SEQ + (c - 4) * 64); }
; DEVI void gla_load(const Params& p, int l, int b, int h, int c, bool need_qg, GlaIn& in) {
;     const bf16_t* P = (const bf16_t*)(p.ws + WS_P);
;     const int tid = opaque_tid(), wid = tid >> 6, lane = tid & 63, fr = lane & 15, fq = lane >> 4, d = wid >> 2, kf = wid & 3, kk = kf * 16 + fr;
;     const int row0 = chunk_row0(b, c), tk = tid >> 3, c8 = (tid & 7) * 8;
;     in.k = *(const bf16x8*)(P + (size_t)(row0 + tk) * INC + C_GK + h * 64 + c8);
;     in.v0 = *(const bf16x8*)(P + (size_t)(row0 + tk) * INC + C_GV + h * 128 + c8);
;     in.v1 = *(const bf16x8*)(P + (size_t)(row0 + tk) * INC + C_GV + h * 128 + 64 + c8);
;     if (need_qg) {
;         in.q = *(const bf16x8*)(P + (size_t)(row0 + tk) * INC + C_GQ + h * 64 + c8);
;         in.g0 = *(const bf16x8*)(P + (size_t)(row0 + tk) * INC + C_GOG + h * 128 + (tid & 7) * 16);
;         in.g1 = *(const bf16x8*)(P + (size_t)(row0 + tk) * INC + C_GOG + h * 128 + (tid & 7) * 16 + 8);
;     }
;     const bf16x8 zero = {0, 0, 0, 0, 0, 0, 0, 0};
;     in.z0 = zero; in.z1 = zero; in.z2 = zero; in.z3 = zero; in.bw = zero;
;     if (fq < 2) {
;         const bf16_t* zp = P + (size_t)(row0 + fr) * INC + C_GZ + d * 16 + fq * 8;
;         in.z0 = *(const bf16x8*)(zp); in.z1 = *(const bf16x8*)(zp + (size_t)16 * INC); in.z2 = *(const bf16x8*)(zp + (size_t)32 * INC); in.z3 = *(const bf16x8*)(zp + (size_t)48 * INC);
;         float wv[8];
; #pragma unroll
;         for (int j = 0; j < 8; ++j) wv[j] = p.gla_w2[((size_t)(l * 2 + d) * 16 + fq * 8 + j) * 256 + h * 64 + kk];
;         in.bw = pack8(wv);
;     }
;     in.bias = p.gla_b[(size_t)(l * 2 + d) * 256 + h * 64 + kk];
.LBB0_711:
	v_ashrrev_i32_e32 v2, 3, v1
	s_and_b32 s5, s5, 3
	v_add_u32_e32 v2, s6, v2
	v_mov_b64_e32 v[12:13], s[86:87]
	v_mad_i64_i32 v[12:13], s[16:17], v2, s93, v[12:13]
	s_lshl_b32 s52, s5, 7
	v_and_b32_e32 v30, 7, v1
	v_lshl_add_u64 v[14:15], v[12:13], 0, s[52:53]
	s_lshl_b32 s52, s5, 8
	v_lshlrev_b32_e32 v2, 4, v30
	v_lshl_add_u64 v[28:29], v[12:13], 0, s[52:53]
	v_lshl_add_u64 v[16:17], v[14:15], 0, v[2:3]
	v_lshl_add_u64 v[18:19], v[28:29], 0, v[2:3]
	global_load_dwordx4 v[12:15], v[18:19], off offset:2688
	global_load_dwordx4 v[24:27], v[18:19], off offset:2816
	global_load_dwordx4 v[20:23], v[16:17], off offset:2176
	s_nop 0
	global_load_dwordx4 v[16:19], v[16:17], off offset:1664
	v_lshlrev_b32_e32 v2, 5, v30
	v_lshl_add_u64 v[28:29], v[28:29], 0, v[2:3]
	global_load_dwordx4 v[32:35], v[28:29], off offset:3792
	s_nop 0
	global_load_dwordx4 v[28:31], v[28:29], off offset:3776
	v_ashrrev_i32_e32 v56, 8, v1
	v_and_b32_e32 v2, 15, v1
	v_bfe_u32 v53, v1, 4, 2
	v_lshrrev_b32_e32 v1, 2, v1
	v_add_u32_e32 v54, s18, v56
	v_and_or_b32 v52, v1, 48, v2
	v_cmp_lt_u32_e32 vcc, 1, v53
	v_ashrrev_i32_e32 v55, 31, v54
	s_and_saveexec_b64 s[16:17], vcc
	s_xor_b64 s[16:17], exec, s[16:17]
	s_or_saveexec_b64 s[16:17], s[16:17]
	s_lshl_b32 s5, s5, 6
	v_mov_b32_e32 v1, 0
	v_mov_b32_e32 v40, 0
	v_mov_b32_e32 v41, 0
	v_mov_b32_e32 v42, 0
	v_mov_b32_e32 v43, 0
	v_mov_b32_e32 v36, 0
	v_mov_b32_e32 v37, 0
	v_mov_b32_e32 v38, 0
	v_mov_b32_e32 v39, 0
	v_mov_b32_e32 v44, 0
	v_mov_b32_e32 v45, 0
	v_mov_b32_e32 v46, 0
	v_mov_b32_e32 v47, 0
	v_mov_b32_e32 v48, 0
	v_mov_b32_e32 v49, 0
	v_mov_b32_e32 v50, 0
	v_mov_b32_e32 v51, 0
	v_mov_b32_e32 v152, 0
	v_mov_b32_e32 v153, 0
	v_mov_b32_e32 v154, 0
	s_xor_b64 exec, exec, s[16:17]
	s_cbranch_execz .LBB0_715
	v_add_u32_e32 v1, s6, v2
	v_mov_b64_e32 v[36:37], s[86:87]
	v_lshlrev_b32_e32 v38, 4, v56
	v_mad_i64_i32 v[36:37], s[6:7], v1, s93, v[36:37]
	v_ashrrev_i32_e32 v39, 31, v38
	v_lshl_add_u64 v[36:37], v[38:39], 1, v[36:37]
	v_lshlrev_b32_e32 v2, 4, v53
	v_lshl_add_u64 v[44:45], v[36:37], 0, v[2:3]
	v_add_co_u32_e32 v40, vcc, 0x23000, v44
	v_lshlrev_b32_e32 v2, 2, v52
	s_nop 0
	v_addc_co_u32_e32 v41, vcc, 0, v45, vcc
	global_load_dwordx4 v[36:39], v[44:45], off offset:3712
	s_nop 0
	global_load_dwordx4 v[40:43], v[40:41], off offset:2688
	s_load_dwordx4 s[56:59], s[0:1], 0x58
	v_add_co_u32_e32 v46, vcc, 0x46000, v44
	s_lshl_b32 s52, s5, 2
	s_nop 0
	v_addc_co_u32_e32 v47, vcc, 0, v45, vcc
	v_add_co_u32_e32 v48, vcc, 0x69000, v44
	v_lshlrev_b64 v[50:51], 14, v[54:55]
	s_nop 0
	v_addc_co_u32_e32 v49, vcc, 0, v45, vcc
	s_waitcnt lgkmcnt(0)
	v_lshl_add_u64 v[44:45], s[56:57], 0, v[2:3]
	v_lshl_add_u64 v[44:45], v[44:45], 0, s[52:53]
	v_lshlrev_b32_e32 v2, 13, v53
	v_lshl_add_u64 v[44:45], v[44:45], 0, v[50:51]
	v_lshl_add_u64 v[44:45], v[44:45], 0, v[2:3]
	s_movk_i32 s6, 0x1000
	v_add_co_u32_e32 v50, vcc, s6, v44
	s_nop 1
	v_addc_co_u32_e32 v51, vcc, 0, v45, vcc
	global_load_dword v164, v[44:45], off
	global_load_dword v165, v[44:45], off offset:1024
	global_load_dword v166, v[44:45], off offset:2048
	global_load_dword v167, v[44:45], off offset:3072
	global_load_dword v168, v[50:51], off
	global_load_dword v169, v[50:51], off offset:1024
	global_load_dword v170, v[50:51], off offset:2048
	global_load_dword v171, v[50:51], off offset:3072
	s_nop 0
	global_load_dwordx4 v[44:47], v[46:47], off offset:1664
	s_nop 0
	global_load_dwordx4 v[48:51], v[48:49], off offset:640

; DEVI int opaque_tid() { int t = threadIdx.x; asm volatile("" : "+v"(t)); return t; }
; DEVI float log_sigmoid_f(float x) { return fminf(x, 0.f) - __logf(1.f + __expf(-fabsf(x))); }
; DEVI void gla_cum(const GlaIn& in, float* cum) {
;     const int tid = opaque_tid(), wid = tid >> 6, lane = tid & 63, fr = lane & 15, fq = lane >> 4, d = wid >> 2, kf = wid & 3;
;     const int kk = kf * 16 + fr;
;     float la[4][4];
; #pragma unroll
;     for (int f = 0; f < 4; ++f) {
;         const bf16x8 az = (f == 0) ? in.z0 : (f == 1) ? in.z1 : (f == 2) ? in.z2 : in.z3;
;         f32x4 acc = {0.f, 0.f, 0.f, 0.f};
;         acc = __builtin_amdgcn_mfma_f32_16x16x32_bf16(az, in.bw, acc, 0, 0, 0);
; #pragma unroll
;         for (int r = 0; r < 4; ++r) la[f][r] = log_sigmoid_f(acc[r] + in.bias) * (1.f / 16.f);
; DEVI void scan_c_gla(const Params& p, int l, int b, int h, int c, const GlaIn& in, char* smem) {
;     ...
;     const bf16_t* SF = (const bf16_t*)(p.ws + WS_STG) + ((size_t)((b * 4 + h) * 2 + 0) * NCH + order_idx(0, c)) * 8192;
;     const bf16_t* SB = (const bf16_t*)(p.ws + WS_STG) + ((size_t)((b * 4 + h) * 2 + 1) * NCH + order_idx(1, c)) * 8192;
;     const bf16x8 sf0 = *(const bf16x8*)(SF + (wid * 16 + fr) * 64 + fq * 8), sf1 = *(const bf16x8*)(SF + (wid * 16 + fr) * 64 + 32 + fq * 8);
;     const bf16x8 sb0 = *(const bf16x8*)(SB + (wid * 16 + fr) * 64 + fq * 8), sb1 = *(const bf16x8*)(SB + (wid * 16 + fr) * 64 + 32 + fq * 8);
.LBB0_720:
	v_mfma_f32_16x16x32_bf16 v[134:137], v[108:111], v[116:119], 0
	s_and_b32 s29, s29, 3
	s_lshl_b32 s4, s7, 3
	s_lshl_b32 s7, s29, 1
	s_or_b32 s4, s7, s4
	s_cmp_gt_i32 s6, 3
	s_nop 1
	v_add_f32_e32 v133, v132, v134
	v_mul_f32_e64 v108, |v133|, s48
	v_exp_f32_e32 v134, v108
	s_mul_i32 s16, s4, 36
	s_cselect_b32 s17, 39, 3
	s_ashr_i32 s38, s6, 31
	v_add_f32_e32 v134, 1.0, v134
	s_mul_hi_i32 s7, s4, 36
	s_add_u32 s6, s16, s6
	v_cmp_gt_f32_e32 vcc, s97, v134
	s_addc_u32 s7, s7, s38
	s_lshl_b64 s[6:7], s[6:7], 14
	v_cndmask_b32_e64 v138, 0, 32, vcc
	v_readlane_b32 s38, v254, 12
	v_ldexp_f32 v134, v134, v138
	s_add_u32 s6, s38, s6
	v_readlane_b32 s39, v254, 13
	v_log_f32_e32 v134, v134
	s_addc_u32 s7, s39, s7
	s_or_b32 s4, s4, 1
	s_sub_i32 s5, s17, s5
	s_mul_hi_i32 s16, s4, 36
	s_mul_i32 s4, s4, 36
	s_add_i32 s5, s50, s5
	s_add_u32 s4, s4, s5
	v_add_f32_e32 v135, v132, v135
	s_addc_u32 s5, s16, 0
	v_mul_f32_e32 v138, 0x3f317217, v134
	v_mul_f32_e64 v139, |v135|, s48
	s_lshl_b64 s[4:5], s[4:5], 14
	v_fma_f32 v138, v134, s49, -v138
	v_exp_f32_e32 v139, v139
	s_add_u32 s4, s38, s4
	v_fmac_f32_e32 v138, 0x3377d1cf, v134
	s_addc_u32 s5, s39, s5
	v_fmac_f32_e32 v138, 0x3f317217, v134
	v_cmp_lt_f32_e64 s[38:39], |v134|, s22
	v_min_f32_e32 v133, 0, v133
	v_add_f32_e32 v136, v132, v136
	v_cndmask_b32_e64 v134, v134, v138, s[38:39]
	v_cndmask_b32_e32 v138, 0, v230, vcc
	v_sub_f32_e32 v134, v134, v138
	v_add_f32_e32 v138, 1.0, v139
	v_cmp_gt_f32_e32 vcc, s97, v138
	v_sub_f32_e32 v133, v133, v134
	v_min_f32_e32 v134, 0, v135
	v_cndmask_b32_e64 v139, 0, 32, vcc
	v_ldexp_f32 v138, v138, v139
	v_log_f32_e32 v138, v138
	v_mul_f32_e64 v139, |v136|, s48
	v_exp_f32_e32 v139, v139
	v_mfma_f32_16x16x32_bf16 v[124:127], v[124:127], v[116:119], 0
	v_mul_f32_e32 v135, 0x3f317217, v138
	v_fma_f32 v135, v138, s49, -v135
	v_fmac_f32_e32 v135, 0x3377d1cf, v138
	v_fmac_f32_e32 v135, 0x3f317217, v138
	v_cmp_lt_f32_e64 s[38:39], |v138|, s22
	v_ashrrev_i32_e32 v2, 6, v156
	v_and_b32_e32 v157, 15, v156
	v_cndmask_b32_e64 v135, v138, v135, s[38:39]
	v_cndmask_b32_e32 v138, 0, v230, vcc
	v_sub_f32_e32 v135, v135, v138
	v_add_f32_e32 v138, 1.0, v139
	v_cmp_gt_f32_e32 vcc, s97, v138
	v_sub_f32_e32 v134, v134, v135
	v_mul_f32_e32 v135, 0x3d800000, v134
	v_cndmask_b32_e64 v139, 0, 32, vcc
	v_ldexp_f32 v138, v138, v139
	v_log_f32_e32 v138, v138
	v_add_f32_e32 v139, v132, v137
	v_mul_f32_e64 v137, |v139|, s48
	v_exp_f32_e32 v137, v137
	v_min_f32_e32 v134, 0, v136
	v_mul_f32_e32 v136, 0x3f317217, v138
	v_fma_f32 v136, v138, s49, -v136
	v_fmac_f32_e32 v136, 0x3377d1cf, v138
	v_fmac_f32_e32 v136, 0x3f317217, v138
	v_cmp_lt_f32_e64 s[38:39], |v138|, s22
	v_add_f32_e32 v137, 1.0, v137
	v_lshlrev_b32_e32 v158, 4, v2
	v_cndmask_b32_e64 v136, v138, v136, s[38:39]
	v_cndmask_b32_e32 v138, 0, v230, vcc
	v_cmp_gt_f32_e32 vcc, s97, v137
	v_sub_f32_e32 v136, v136, v138
	v_sub_f32_e32 v134, v134, v136
	v_cndmask_b32_e64 v138, 0, 32, vcc
	v_ldexp_f32 v137, v137, v138
	v_log_f32_e32 v142, v137
	v_mul_f32_e32 v137, 0x3d800000, v134
	v_min_f32_e32 v134, 0, v139
	v_mfma_f32_16x16x32_bf16 v[138:141], v[128:131], v[116:119], 0
	v_mul_f32_e32 v136, 0x3f317217, v142
	v_fma_f32 v136, v142, s49, -v136
	v_fmac_f32_e32 v136, 0x3377d1cf, v142
	v_fmac_f32_e32 v136, 0x3f317217, v142
	v_cmp_lt_f32_e64 s[38:39], |v142|, s22
	s_nop 2
	v_add_f32_e32 v128, v132, v138
	v_mul_f32_e64 v129, |v128|, s48
	v_exp_f32_e32 v129, v129
	v_cndmask_b32_e64 v130, v142, v136, s[38:39]
	v_cndmask_b32_e32 v131, 0, v230, vcc
	v_sub_f32_e32 v130, v130, v131
	v_add_f32_e32 v129, 1.0, v129
	v_cmp_gt_f32_e32 vcc, s97, v129
	v_min_f32_e32 v128, 0, v128
	v_or_b32_e32 v159, v158, v157
	v_cndmask_b32_e64 v131, 0, 32, vcc
	v_ldexp_f32 v129, v129, v131
	v_log_f32_e32 v131, v129
	v_sub_f32_e32 v129, v134, v130
	v_add_f32_e32 v134, v132, v139
	v_mul_f32_e64 v136, |v134|, s48
	v_mul_f32_e32 v130, 0x3f317217, v131
	v_fma_f32 v130, v131, s49, -v130
	v_exp_f32_e32 v136, v136
	v_fmac_f32_e32 v130, 0x3377d1cf, v131
	v_fmac_f32_e32 v130, 0x3f317217, v131
	v_cmp_lt_f32_e64 s[38:39], |v131|, s22
	v_lshlrev_b32_e32 v100, 6, v159
	v_ashrrev_i32_e32 v101, 31, v100
	v_cndmask_b32_e64 v130, v131, v130, s[38:39]
	v_cndmask_b32_e32 v131, 0, v230, vcc
	v_sub_f32_e32 v130, v130, v131
	v_add_f32_e32 v131, 1.0, v136
	v_cmp_gt_f32_e32 vcc, s97, v131
	v_sub_f32_e32 v128, v128, v130
	v_bfe_u32 v160, v156, 4, 2
	v_cndmask_b32_e64 v136, 0, 32, vcc
	v_ldexp_f32 v131, v131, v136
	v_log_f32_e32 v136, v131
	v_mul_f32_e32 v131, 0x3d800000, v128
	v_min_f32_e32 v128, 0, v134
	v_add_f32_e32 v134, v132, v140
	v_mul_f32_e32 v130, 0x3f317217, v136
	v_mul_f32_e64 v138, |v134|, s48
	v_fma_f32 v130, v136, s49, -v130
	v_exp_f32_e32 v138, v138
	v_fmac_f32_e32 v130, 0x3377d1cf, v136
	v_fmac_f32_e32 v130, 0x3f317217, v136
	v_cmp_lt_f32_e64 s[38:39], |v136|, s22
	v_lshlrev_b64 v[112:113], 1, v[100:101]
	v_lshl_add_u64 v[100:101], s[6:7], 0, v[112:113]
	v_cndmask_b32_e64 v130, v136, v130, s[38:39]
	v_cndmask_b32_e32 v136, 0, v230, vcc
	v_sub_f32_e32 v130, v130, v136
	v_add_f32_e32 v136, 1.0, v138
	v_cmp_gt_f32_e32 vcc, s97, v136
	v_sub_f32_e32 v128, v128, v130
	v_min_f32_e32 v130, 0, v134
	v_cndmask_b32_e64 v138, 0, 32, vcc
	v_ldexp_f32 v136, v136, v138
	v_log_f32_e32 v136, v136
	v_add_f32_e32 v138, v132, v141
	v_mul_f32_e64 v139, |v138|, s48
	v_exp_f32_e32 v139, v139
	v_mul_f32_e32 v134, 0x3f317217, v136
	v_fma_f32 v134, v136, s49, -v134
	v_fmac_f32_e32 v134, 0x3377d1cf, v136
	v_fmac_f32_e32 v134, 0x3f317217, v136
	v_cmp_lt_f32_e64 s[38:39], |v136|, s22
	v_lshlrev_b32_e32 v2, 4, v160
	v_lshl_add_u64 v[112:113], s[4:5], 0, v[112:113]
	v_cndmask_b32_e64 v134, v136, v134, s[38:39]
; DEVI float log_sigmoid_f(float x) { return fminf(x, 0.f) - __logf(1.f + __expf(-fabsf(x))); }
; DEVI void gla_cum(const GlaIn& in, float* cum) {
;     ...
; #pragma unroll
;     for (int f = 0; f < 4; ++f) {
;         const bf16x8 az = (f == 0) ? in.z0 : (f == 1) ? in.z1 : (f == 2) ? in.z2 : in.z3;
;         f32x4 acc = {0.f, 0.f, 0.f, 0.f};
;         acc = __builtin_amdgcn_mfma_f32_16x16x32_bf16(az, in.bw, acc, 0, 0, 0);
; #pragma unroll
;         for (int r = 0; r < 4; ++r) la[f][r] = log_sigmoid_f(acc[r] + in.bias) * (1.f / 16.f);
;     }
;     if (d == 0) {
; DEVI void scan_c_gla(const Params& p, int l, int b, int h, int c, const GlaIn& in, char* smem) {
;     ...
;     const bf16x8 sf0 = *(const bf16x8*)(SF + (wid * 16 + fr) * 64 + fq * 8), sf1 = *(const bf16x8*)(SF + (wid * 16 + fr) * 64 + 32 + fq * 8);
;     const bf16x8 sb0 = *(const bf16x8*)(SB + (wid * 16 + fr) * 64 + fq * 8), sb1 = *(const bf16x8*)(SB + (wid * 16 + fr) * 64 + 32 + fq * 8);
	v_cndmask_b32_e32 v136, 0, v230, vcc
	v_sub_f32_e32 v134, v134, v136
	v_add_f32_e32 v136, 1.0, v139
	v_cmp_gt_f32_e32 vcc, s97, v136
	v_sub_f32_e32 v130, v130, v134
	v_mul_f32_e32 v134, 0x3d800000, v130
	v_cndmask_b32_e64 v139, 0, 32, vcc
	v_ldexp_f32 v136, v136, v139
	v_log_f32_e32 v136, v136
	v_add_f32_e32 v139, v132, v124
	v_mul_f32_e64 v124, |v139|, s48
	v_exp_f32_e32 v124, v124
	v_min_f32_e32 v130, 0, v138
	v_mul_f32_e32 v138, 0x3f317217, v136
	v_fma_f32 v138, v136, s49, -v138
	v_fmac_f32_e32 v138, 0x3377d1cf, v136
	v_fmac_f32_e32 v138, 0x3f317217, v136
	v_cmp_lt_f32_e64 s[38:39], |v136|, s22
	v_add_f32_e32 v124, 1.0, v124
	v_lshl_add_u64 v[100:101], v[100:101], 0, v[2:3]
	v_cndmask_b32_e64 v136, v136, v138, s[38:39]
	v_cndmask_b32_e32 v138, 0, v230, vcc
	v_cmp_gt_f32_e32 vcc, s97, v124
	v_sub_f32_e32 v136, v136, v138
	v_lshl_add_u64 v[108:109], v[112:113], 0, v[2:3]
	v_cndmask_b32_e64 v138, 0, 32, vcc
	v_ldexp_f32 v124, v124, v138
	v_log_f32_e32 v138, v124
	v_sub_f32_e32 v124, v130, v136
	v_min_f32_e32 v130, 0, v139
	v_add_f32_e32 v139, v132, v125
	v_mul_f32_e64 v125, |v139|, s48
	v_exp_f32_e32 v125, v125
	v_mul_f32_e32 v136, 0x3f317217, v138
	v_fma_f32 v136, v138, s49, -v136
	v_fmac_f32_e32 v136, 0x3377d1cf, v138
	v_fmac_f32_e32 v136, 0x3f317217, v138
	v_cmp_lt_f32_e64 s[38:39], |v138|, s22
	v_add_f32_e32 v125, 1.0, v125
	global_load_dwordx4 v[104:107], v[100:101], off
	s_nop 0
	global_load_dwordx4 v[100:103], v[100:101], off offset:64
	v_cndmask_b32_e64 v136, v138, v136, s[38:39]
	v_cndmask_b32_e32 v138, 0, v230, vcc
	v_cmp_gt_f32_e32 vcc, s97, v125
	v_sub_f32_e32 v136, v136, v138
	global_load_dwordx4 v[112:115], v[108:109], off
	s_nop 0
	global_load_dwordx4 v[108:111], v[108:109], off offset:64
	v_cndmask_b32_e64 v138, 0, 32, vcc
	v_ldexp_f32 v125, v125, v138
	v_log_f32_e32 v138, v125
	v_sub_f32_e32 v125, v130, v136
	v_min_f32_e32 v130, 0, v139
	v_add_f32_e32 v139, v132, v126
	v_mul_f32_e64 v126, |v139|, s48
	v_exp_f32_e32 v126, v126
	v_mul_f32_e32 v136, 0x3f317217, v138
	v_fma_f32 v136, v138, s49, -v136
	v_fmac_f32_e32 v136, 0x3377d1cf, v138
	v_fmac_f32_e32 v136, 0x3f317217, v138
	v_cmp_lt_f32_e64 s[38:39], |v138|, s22
	v_add_f32_e32 v126, 1.0, v126
	v_add_f32_e32 v127, v132, v127
	v_cndmask_b32_e64 v136, v138, v136, s[38:39]
	v_cndmask_b32_e32 v138, 0, v230, vcc
	v_cmp_gt_f32_e32 vcc, s97, v126
	v_sub_f32_e32 v136, v136, v138
	v_mfma_f32_16x16x32_bf16 v[118:121], v[120:123], v[116:119], 0
	v_cndmask_b32_e64 v138, 0, 32, vcc
	v_ldexp_f32 v126, v126, v138
	v_log_f32_e32 v138, v126
	v_sub_f32_e32 v126, v130, v136
	v_min_f32_e32 v130, 0, v139
	v_mul_f32_e64 v139, |v127|, s48
	v_mul_f32_e32 v136, 0x3f317217, v138
	v_fma_f32 v136, v138, s49, -v136
	v_exp_f32_e32 v139, v139
	v_fmac_f32_e32 v136, 0x3377d1cf, v138
	v_fmac_f32_e32 v136, 0x3f317217, v138
	v_cmp_lt_f32_e64 s[38:39], |v138|, s22
	v_add_f32_e32 v117, v132, v118
	v_mul_f32_e64 v116, |v117|, s48
	v_cndmask_b32_e64 v136, v138, v136, s[38:39]
	v_cndmask_b32_e32 v138, 0, v230, vcc
	v_sub_f32_e32 v136, v136, v138
	v_add_f32_e32 v138, 1.0, v139
	v_cmp_gt_f32_e32 vcc, s97, v138
	v_sub_f32_e32 v130, v130, v136
	v_exp_f32_e32 v116, v116
	v_cndmask_b32_e64 v139, 0, 32, vcc
	v_ldexp_f32 v138, v138, v139
	v_log_f32_e32 v138, v138
	v_mul_f32_e32 v136, 0x3d800000, v130
	v_add_f32_e32 v116, 1.0, v116
	v_cndmask_b32_e32 v122, 0, v230, vcc
	v_mul_f32_e32 v130, 0x3f317217, v138
	v_fma_f32 v130, v138, s49, -v130
	v_fmac_f32_e32 v130, 0x3377d1cf, v138
	v_fmac_f32_e32 v130, 0x3f317217, v138
	v_cmp_lt_f32_e64 s[38:39], |v138|, s22
	v_cmp_gt_f32_e32 vcc, s97, v116
	v_add_f32_e32 v123, v132, v119
	v_cndmask_b32_e64 v118, v138, v130, s[38:39]
	v_sub_f32_e32 v118, v118, v122
	v_cndmask_b32_e64 v122, 0, 32, vcc
	v_ldexp_f32 v116, v116, v122
	v_log_f32_e32 v122, v116
	v_mul_f32_e64 v119, |v123|, s48
	v_min_f32_e32 v127, 0, v127
	v_exp_f32_e32 v119, v119
	v_sub_f32_e32 v116, v127, v118
	v_mul_f32_e32 v118, 0x3f317217, v122
	v_fma_f32 v118, v122, s49, -v118
	v_fmac_f32_e32 v118, 0x3377d1cf, v122
	v_fmac_f32_e32 v118, 0x3f317217, v122
	v_cmp_lt_f32_e64 s[38:39], |v122|, s22
	v_add_f32_e32 v119, 1.0, v119
	v_min_f32_e32 v117, 0, v117
	v_cndmask_b32_e64 v118, v122, v118, s[38:39]
	v_cndmask_b32_e32 v122, 0, v230, vcc
	v_cmp_gt_f32_e32 vcc, s97, v119
	v_sub_f32_e32 v118, v118, v122
	v_sub_f32_e32 v117, v117, v118
	v_cndmask_b32_e64 v122, 0, 32, vcc
	v_ldexp_f32 v119, v119, v122
	v_log_f32_e32 v122, v119
	v_add_f32_e32 v120, v132, v120
	v_mul_f32_e32 v119, 0x3d800000, v117
	v_min_f32_e32 v117, 0, v123
	v_mul_f32_e32 v118, 0x3f317217, v122
	v_mul_f32_e64 v123, |v120|, s48
	v_fma_f32 v118, v122, s49, -v118
	v_exp_f32_e32 v123, v123
	v_fmac_f32_e32 v118, 0x3377d1cf, v122
	v_fmac_f32_e32 v118, 0x3f317217, v122
	v_cmp_lt_f32_e64 s[38:39], |v122|, s22
	v_add_f32_e32 v121, v132, v121
	v_mov_b32_e32 v161, v0
	v_cndmask_b32_e64 v118, v122, v118, s[38:39]
	v_cndmask_b32_e32 v122, 0, v230, vcc
	v_sub_f32_e32 v118, v118, v122
	v_add_f32_e32 v122, 1.0, v123
	v_cmp_gt_f32_e32 vcc, s97, v122
	v_sub_f32_e32 v117, v117, v118
	v_min_f32_e32 v118, 0, v120
	v_cndmask_b32_e64 v123, 0, 32, vcc
	v_ldexp_f32 v122, v122, v123
	v_log_f32_e32 v122, v122
	v_mul_f32_e64 v123, |v121|, s48
	v_exp_f32_e32 v123, v123
	s_movk_i32 s4, 0xff
	v_mul_f32_e32 v120, 0x3f317217, v122
	v_fma_f32 v120, v122, s49, -v120
	v_fmac_f32_e32 v120, 0x3377d1cf, v122
	v_fmac_f32_e32 v120, 0x3f317217, v122
	v_cmp_lt_f32_e64 s[38:39], |v122|, s22
	v_mul_f32_e32 v133, 0x3d800000, v133
	v_mul_f32_e32 v129, 0x3d800000, v129
	v_cndmask_b32_e64 v120, v122, v120, s[38:39]
	v_cndmask_b32_e32 v122, 0, v230, vcc
	v_sub_f32_e32 v120, v120, v122
	v_add_f32_e32 v122, 1.0, v123
	v_cmp_gt_f32_e32 vcc, s97, v122
	v_sub_f32_e32 v118, v118, v120
	v_mul_f32_e32 v127, 0x3d800000, v118
	v_cndmask_b32_e64 v123, 0, 32, vcc
	v_ldexp_f32 v122, v122, v123
	v_log_f32_e32 v122, v122
	v_min_f32_e32 v118, 0, v121
	v_cndmask_b32_e32 v121, 0, v230, vcc
	v_mul_f32_e32 v128, 0x3d800000, v128
	v_mul_f32_e32 v120, 0x3f317217, v122
	v_fma_f32 v120, v122, s49, -v120
	v_fmac_f32_e32 v120, 0x3377d1cf, v122
	v_fmac_f32_e32 v120, 0x3f317217, v122
	v_cmp_lt_f32_e64 s[38:39], |v122|, s22
	v_mul_f32_e32 v124, 0x3d800000, v124
	v_mul_f32_e32 v125, 0x3d800000, v125
	v_cndmask_b32_e64 v120, v122, v120, s[38:39]
	v_sub_f32_e32 v120, v120, v121
	v_sub_f32_e32 v118, v118, v120
	v_mul_f32_e32 v126, 0x3d800000, v126
	v_mul_f32_e32 v116, 0x3d800000, v116
	v_mul_f32_e32 v117, 0x3d800000, v117
	v_mul_f32_e32 v120, 0x3d800000, v118
	v_and_b32_e32 v163, 15, v161
	v_bfe_u32 v162, v161, 4, 2
	v_cmp_lt_u32_e32 vcc, s4, v161
	s_and_saveexec_b64 s[4:5], vcc
	s_xor_b64 s[16:17], exec, s[4:5]
	s_cbranch_execz .LBB0_722
; DEVI void gla_cum(const GlaIn& in, float* cum) {
;     ...
;     } else {
;         float carry = 0.f;
; #pragma unroll
;         for (int f = 3; f >= 0; --f) {
;             la[f][2] += la[f][3]; la[f][1] += la[f][2]; la[f][0] += la[f][1];
;             float x = la[f][0]; const float own = x;
;             float y = __shfl_down(x, 16); if (fq <= 2) x += y;
;             y = __shfl_down(x, 32); if (fq <= 1) x += y;
;             const float excl = x - own + carry;
;             carry += __shfl(x, fr);
; #pragma unroll
;             for (int r = 0; r < 4; ++r) la[f][r] += excl;
;         }
	v_and_b32_e32 v118, 48, v227
	v_cmp_eq_u32_e32 vcc, 48, v118
	v_add_f32_e32 v121, v120, v127
	v_mov_b32_e32 v122, 0x80
	v_cndmask_b32_e64 v118, 16, 0, vcc
	v_add_lshl_u32 v140, v118, v227, 2
	v_add_f32_e32 v118, v117, v121
	v_add_f32_e32 v119, v119, v118
	ds_bpermute_b32 v117, v140, v119
	v_cmp_eq_u32_e32 vcc, 3, v162
	v_lshl_or_b32 v141, v227, 2, v122
	v_cmp_gt_u32_e64 s[38:39], 2, v162
	v_and_or_b32 v123, v227, 64, v163
	s_waitcnt lgkmcnt(0)
	v_add_f32_e32 v117, v119, v117
	v_cndmask_b32_e32 v117, v117, v119, vcc
	ds_bpermute_b32 v122, v141, v117
	v_lshlrev_b32_e32 v123, 2, v123
	s_waitcnt lgkmcnt(0)
	v_add_f32_e32 v122, v117, v122
	v_cndmask_b32_e64 v132, v117, v122, s[38:39]
	v_sub_f32_e32 v117, v132, v119
	v_add_f32_e32 v122, 0, v117
	v_add_f32_e32 v117, v116, v136
	v_add_f32_e32 v126, v126, v117
	v_add_f32_e32 v127, v125, v126
	v_add_f32_e32 v125, v124, v134
	v_add_f32_e32 v130, v128, v125
	ds_bpermute_b32 v136, v140, v127
	v_add_f32_e32 v131, v131, v130
	ds_bpermute_b32 v134, v140, v131
	ds_bpermute_b32 v128, v123, v132
	v_pk_add_f32 v[138:139], v[118:119], v[122:123] op_sel_hi:[1,0]
	s_waitcnt lgkmcnt(2)
	v_add_f32_e32 v132, v127, v136
	v_cndmask_b32_e32 v132, v132, v127, vcc
	s_waitcnt lgkmcnt(1)
	v_add_f32_e32 v134, v131, v134
	ds_bpermute_b32 v136, v141, v132
	v_cndmask_b32_e32 v142, v134, v131, vcc
	ds_bpermute_b32 v143, v141, v142
	s_waitcnt lgkmcnt(1)
	v_add_f32_e32 v118, v132, v136
	v_cndmask_b32_e64 v144, v132, v118, s[38:39]
	s_waitcnt lgkmcnt(0)
	v_add_f32_e32 v118, v142, v143
	ds_bpermute_b32 v134, v123, v144
	v_cndmask_b32_e64 v145, v142, v118, s[38:39]
	ds_bpermute_b32 v132, v123, v145
	v_mov_b32_e32 v136, v3
	v_pk_add_f32 v[118:119], v[128:129], v[136:137]
	v_pk_add_f32 v[142:143], v[120:121], v[122:123] op_sel_hi:[1,0]
	s_waitcnt lgkmcnt(1)
	v_pk_add_f32 v[120:121], v[118:119], v[134:135]
	s_waitcnt lgkmcnt(0)
	v_pk_add_f32 v[122:123], v[120:121], v[132:133]
	ds_bpermute_b32 v128, v140, v123
	v_sub_f32_e32 v132, v144, v127
	v_add_f32_e32 v118, v118, v132
	v_sub_f32_e32 v133, v145, v131
	v_pk_add_f32 v[144:145], v[126:127], v[118:119] op_sel_hi:[1,0]
	s_waitcnt lgkmcnt(0)
	v_add_f32_e32 v126, v123, v128
	v_cndmask_b32_e32 v126, v126, v123, vcc
	ds_bpermute_b32 v127, v141, v126
	v_pk_add_f32 v[148:149], v[116:117], v[118:119] op_sel_hi:[1,0]
	v_add_f32_e32 v116, v120, v133
	v_pk_add_f32 v[146:147], v[130:131], v[116:117] op_sel_hi:[1,0]
	v_pk_add_f32 v[150:151], v[124:125], v[116:117] op_sel_hi:[1,0]
	s_waitcnt lgkmcnt(0)
	v_add_f32_e32 v116, v126, v127
	v_cndmask_b32_e64 v116, v126, v116, s[38:39]
	v_sub_f32_e32 v116, v116, v123
	v_add_f32_e32 v116, v122, v116
	v_mov_b32_e32 v122, v121
	v_mov_b32_e32 v118, v129
	v_pk_add_f32 v[122:123], v[122:123], v[116:117] op_sel_hi:[1,0]
	v_pk_add_f32 v[140:141], v[118:119], v[116:117] op_sel_hi:[1,0]

; DEVI int opaque_tid() { int t = threadIdx.x; asm volatile("" : "+v"(t)); return t; }
; DEVI unsigned cvt4_fp8(float a, float b, float c, float d) { int w = 0; w = __builtin_amdgcn_cvt_pk_fp8_f32(a, b, w, false); w = __builtin_amdgcn_cvt_pk_fp8_f32(c, d, w, true); return (unsigned)w; }
; DEVI void cvt8_finish(const Params& p, int L, int t, const CvtIn& in, char* smem) {
;     const int which = t / 4096, r = t % 4096, le = L * 16 + r / 256, kt = (r % 256) / 16, nt = r % 16;
;     unsigned char* dst = (which == 2) ? (unsigned char*)(p.ws + WS_WDN) + (size_t)le * 2048 * 2048 + (size_t)(nt * 128) * 2048
;                                       : (unsigned char*)(p.ws + WS_WGU) + (size_t)le * 4096 * 2048 + (size_t)(nt * 256 + which * 128) * 2048;
;     unsigned char* T = (unsigned char*)smem;
;     const int tid = opaque_tid(), nq = tid & 31, kq0 = tid >> 5;
; #pragma unroll
;     for (int it = 0; it < 2; ++it) { const int kq = kq0 + it * 16;
; #pragma unroll
;         for (int j = 0; j < 4; ++j) *(unsigned*)(T + (nq * 4 + j) * 144 + kq * 4) =
;             cvt4_fp8(in.v[it * 4][j] * W8_SCALE, in.v[it * 4 + 1][j] * W8_SCALE, in.v[it * 4 + 2][j] * W8_SCALE, in.v[it * 4 + 3][j] * W8_SCALE); }
;     __syncthreads();
; #pragma unroll
;     for (int i = 0; i < 2; ++i) { const int nl = (tid >> 3) + 64 * i, kc = (tid & 7) * 16;
;         *(u32x4*)(dst + (size_t)nl * 2048 + kt * 128 + kc) = *(const u32x4*)(T + nl * 144 + kc); }
;     __syncthreads();
; }
; DEVI void gla_load(const Params& p, int l, int b, int h, int c, bool need_qg, GlaIn& in) {
;     ...
;         float wv[8];
; #pragma unroll
;         for (int j = 0; j < 8; ++j) wv[j] = p.gla_w2[((size_t)(l * 2 + d) * 16 + fq * 8 + j) * 256 + h * 64 + kk];
;         in.bw = pack8(wv);
.LBB0_740:
	v_mul_f32_e32 v5, 0x42800000, v68
	v_mul_f32_e32 v6, 0x42800000, v72
	v_mov_b32_e32 v7, v3
	v_cvt_pk_fp8_f32 v7, v5, v6
	v_mul_f32_e32 v6, 0x42800000, v76
	v_mul_f32_e32 v9, 0x42800000, v80
	v_mov_b32_e32 v2, v0
	v_cvt_pk_fp8_f32 v7, v6, v9 op_sel:[0,0,1]
	v_mul_f32_e32 v6, 0x42800000, v69
	v_mul_f32_e32 v9, 0x42800000, v73
	v_mov_b32_e32 v10, v3
	v_cvt_pk_fp8_f32 v10, v6, v9
	v_lshlrev_b32_e32 v4, 2, v2
	v_and_b32_e32 v4, 0x7c, v4
	v_ashrrev_i32_e32 v8, 3, v2
	v_and_b32_e32 v5, -4, v8
	v_mul_u32_u24_e32 v4, 0x90, v4
	v_add3_u32 v4, 0, v5, v4
	v_mul_f32_e32 v5, 0x42800000, v77
	v_mul_f32_e32 v6, 0x42800000, v81
	v_cvt_pk_fp8_f32 v10, v5, v6 op_sel:[0,0,1]
	v_mul_f32_e32 v5, 0x42800000, v70
	v_mul_f32_e32 v6, 0x42800000, v74
	v_mov_b32_e32 v68, v3
	v_cvt_pk_fp8_f32 v68, v5, v6
	v_mul_f32_e32 v5, 0x42800000, v71
	v_mul_f32_e32 v6, 0x42800000, v75
	v_mov_b32_e32 v69, v3
	v_cvt_pk_fp8_f32 v69, v5, v6
	v_mul_f32_e32 v5, 0x42800000, v79
	v_mul_f32_e32 v6, 0x42800000, v83
	v_mul_f32_e32 v9, 0x42800000, v78
	v_cvt_pk_fp8_f32 v69, v5, v6 op_sel:[0,0,1]
	v_mul_f32_e32 v5, 0x42800000, v52
	v_mul_f32_e32 v6, 0x42800000, v56
	v_mov_b32_e32 v52, v3
	v_cvt_pk_fp8_f32 v52, v5, v6
	v_mul_f32_e32 v5, 0x42800000, v53
	v_mul_f32_e32 v6, 0x42800000, v57
	v_mov_b32_e32 v53, v3
	v_cvt_pk_fp8_f32 v53, v5, v6
	v_mul_f32_e32 v5, 0x42800000, v61
	v_mul_f32_e32 v6, 0x42800000, v65
	v_mul_f32_e32 v11, 0x42800000, v82
	v_cvt_pk_fp8_f32 v53, v5, v6 op_sel:[0,0,1]
	v_mul_f32_e32 v5, 0x42800000, v54
	v_mul_f32_e32 v6, 0x42800000, v58
	v_mov_b32_e32 v54, v3
	v_cvt_pk_fp8_f32 v54, v5, v6
	v_mul_f32_e32 v5, 0x42800000, v55
	v_mul_f32_e32 v6, 0x42800000, v59
	v_mov_b32_e32 v55, v3
	v_cvt_pk_fp8_f32 v68, v9, v11 op_sel:[0,0,1]
	v_mul_f32_e32 v9, 0x42800000, v60
	v_mul_f32_e32 v11, 0x42800000, v64
	v_cvt_pk_fp8_f32 v55, v5, v6
	v_cvt_pk_fp8_f32 v52, v9, v11 op_sel:[0,0,1]
	v_mul_f32_e32 v9, 0x42800000, v62
	v_mul_f32_e32 v11, 0x42800000, v66
	v_cvt_pk_fp8_f32 v54, v9, v11 op_sel:[0,0,1]
	v_mul_f32_e32 v5, 0x42800000, v63
	v_mul_f32_e32 v6, 0x42800000, v67
	s_ashr_i32 s5, s51, 31
	v_cvt_pk_fp8_f32 v55, v5, v6 op_sel:[0,0,1]
	v_lshlrev_b32_e32 v2, 4, v2
	s_add_u32 s4, s16, s51
	ds_write2_b32 v4, v7, v52 offset1:16
	ds_write2_b32 v4, v10, v53 offset0:36 offset1:52
	ds_write2_b32 v4, v68, v54 offset0:72 offset1:88
	ds_write2_b32 v4, v69, v55 offset0:108 offset1:124
	v_and_b32_e32 v2, 0x70, v2
	s_addc_u32 s5, s17, s5
	v_mul_lo_u32 v4, v8, s91
	v_lshl_add_u64 v[10:11], s[4:5], 0, v[2:3]
	v_add3_u32 v2, 0, v2, v4
	s_waitcnt lgkmcnt(0)
	s_barrier
	ds_read_b128 v[4:7], v2
	v_ashrrev_i32_e32 v9, 31, v8
	v_lshlrev_b64 v[8:9], 11, v[8:9]
	v_lshl_add_u64 v[52:53], v[10:11], 0, v[8:9]
	ds_read_b128 v[8:11], v2 offset:9216
	s_waitcnt lgkmcnt(1)
	global_store_dwordx4 v[52:53], v[4:7], off
	s_add_i32 s33, s33, s37
	s_sub_i32 s50, s50, s47
	v_add_co_u32_e32 v4, vcc, 0x20000, v52
	s_nop 1
	v_addc_co_u32_e32 v5, vcc, 0, v53, vcc
	s_andn2_b64 vcc, exec, s[40:41]
	s_waitcnt lgkmcnt(0)
	global_store_dwordx4 v[4:5], v[8:11], off
	s_barrier
	s_cbranch_vccz .LBB0_742
	v_bfe_u32 v172, v0, 4, 2
	v_cmp_gt_u32_e32 vcc, 2, v172
	v_cvt_pk_bf16_f32 v173, v164, v165
	v_cvt_pk_bf16_f32 v174, v166, v167
	v_cvt_pk_bf16_f32 v175, v168, v169
	v_cvt_pk_bf16_f32 v176, v170, v171
	v_cndmask_b32_e32 v1, v1, v173, vcc
	v_cndmask_b32_e32 v152, v152, v174, vcc
	v_cndmask_b32_e32 v153, v153, v175, vcc
	v_cndmask_b32_e32 v154, v154, v176, vcc
	v_mov_b64_e32 v[4:5], v[32:33]
	v_mov_b64_e32 v[8:9], v[28:29]
	v_mov_b64_e32 v[86:87], v[26:27]
	v_mov_b64_e32 v[90:91], v[14:15]
	v_mov_b64_e32 v[94:95], v[22:23]
	v_mov_b64_e32 v[98:99], v[18:19]
	s_mov_b32 s4, s46
	v_mov_b32_e32 v132, v155
	v_mov_b64_e32 v[6:7], v[34:35]
	v_mov_b64_e32 v[10:11], v[30:31]
	v_mov_b64_e32 v[84:85], v[24:25]
	v_mov_b64_e32 v[88:89], v[12:13]
	v_mov_b64_e32 v[92:93], v[20:21]
	v_mov_b64_e32 v[96:97], v[16:17]
	v_mov_b32_e32 v116, v1
	v_mov_b32_e32 v117, v152
	v_mov_b32_e32 v118, v153
	v_mov_b32_e32 v119, v154
	v_mov_b32_e32 v120, v48
	v_mov_b32_e32 v121, v49
	v_mov_b32_e32 v122, v50
	v_mov_b32_e32 v123, v51
	v_mov_b32_e32 v124, v44
	v_mov_b32_e32 v125, v45
	v_mov_b32_e32 v126, v46
	v_mov_b32_e32 v127, v47
	v_mov_b32_e32 v128, v40
	v_mov_b32_e32 v129, v41
	v_mov_b32_e32 v130, v42
	v_mov_b32_e32 v131, v43
	v_mov_b32_e32 v108, v36
	v_mov_b32_e32 v109, v37
	v_mov_b32_e32 v110, v38
	v_mov_b32_e32 v111, v39
	s_branch .LBB0_706

; DEVI void phase_l4(const Params& p, int l, char* smem) {
;     ...
;         {   RetIn cur; bool have = u < nsc;
;             if (have) { const int r = u - nG; ret_load(p, (r / ncs) >> 2, (r / ncs) & 3, r % ncs + c0, true, cur); }
;             while (have) { const int un = u + G; const bool hn = un < nsc; RetIn nxt; const int r = u - nG, rn = un - nG;
;                 if (hn) ret_load(p, (rn / ncs) >> 2, (rn / ncs) & 3, rn % ncs + c0, true, nxt);
;                 CvtIn ci; cvt8_load(p, l, (l == 0 ? TS0C : TS1C) + u, ci);
.LBB0_750:
	v_readlane_b32 s4, v254, 49
	v_readlane_b32 s5, v254, 50
	s_and_b64 s[4:5], s[4:5], exec
	s_movk_i32 s4, 0x2b80
	s_cselect_b32 s4, s4, 0x2c00
	v_readlane_b32 s6, v254, 61
	s_lshl_b32 s23, s6, 4
	s_add_i32 s24, s4, s46
	v_readlane_b32 s7, v254, 62
	s_waitcnt vmcnt(0)
	s_branch .LBB0_752

; DEVI void ret_rot(const bf16x8 r0, const bf16x8 r1, const RetIn& in, bool lat, float scale, float (&o)[16]) {
;     float a[8], c[8]; unpack8(r0, a); unpack8(r1, c);
; #pragma unroll
;     for (int i = 0; i < 8; ++i) { o[i] = a[i]; o[8 + i] = c[i]; }
;     if (lat) {
; #pragma unroll
;         for (int q = 0; q < 4; ++q) { const f32x4 cs = (q == 0) ? in.cs0 : (q == 1) ? in.cs1 : (q == 2) ? in.cs2 : in.cs3;
;             const float x1 = o[4 * q], x2 = o[4 * q + 1], y1 = o[4 * q + 2], y2 = o[4 * q + 3];
;             o[4 * q] = x1 * cs[0] - x2 * cs[1]; o[4 * q + 1] = x1 * cs[1] + x2 * cs[0];
;             o[4 * q + 2] = y1 * cs[2] - y2 * cs[3]; o[4 * q + 3] = y1 * cs[3] + y2 * cs[2]; }
; DEVI void scan_c_ret(const Params& p, int l, int b, int h, int c, const RetIn& in, char* smem) {
;     ...
;     const bf16_t* SF = (const bf16_t*)(p.ws + WS_STR) + ((size_t)((b * 4 + h) * 2 + 0) * NCH + order_idx(0, c)) * 16384;
;     const bf16_t* SB = (const bf16_t*)(p.ws + WS_STR) + ((size_t)((b * 4 + h) * 2 + 1) * NCH + order_idx(1, c)) * 16384;
;     bf16x8 sff[4], sbf[4];
; #pragma unroll
;     for (int ksx = 0; ksx < 4; ++ksx) { sff[ksx] = *(const bf16x8*)(SF + (wid * 16 + fr) * 128 + ksx * 32 + fq * 8); sbf[ksx] = *(const bf16x8*)(SB + (wid * 16 + fr) * 128 + ksx * 32 + fq * 8); }
;     {   float qf[16], kf[16];
;         ret_rot(in.q0, in.q1, in, lat, 1.f, qf);
;         ret_rot(in.k0, in.k1, in, lat, 0.08838834764831845f, kf);
.LBB0_763:
	s_and_b32 s29, s4, 3
	s_lshl_b32 s4, s29, 1
	s_lshl_b32 s16, s33, 3
	s_or_b32 s33, s4, s16
	s_cmp_gt_i32 s5, 3
	s_cselect_b64 s[16:17], -1, 0
	s_and_b64 s[38:39], s[16:17], exec
	s_mul_i32 s50, s33, 36
	s_cselect_b32 s51, 39, 3
	s_ashr_i32 s39, s5, 31
	s_mul_hi_i32 s37, s33, 36
	s_add_u32 s38, s50, s5
	s_addc_u32 s39, s37, s39
	s_lshl_b64 s[38:39], s[38:39], 15
	v_readlane_b32 s52, v254, 10
	s_add_u32 s38, s52, s38
	v_readlane_b32 s54, v254, 11
	s_addc_u32 s39, s54, s39
	s_or_b32 s33, s33, 1
	s_mul_hi_i32 s37, s33, 36
	s_mul_i32 s33, s33, 36
	s_sub_i32 s50, s51, s5
	v_and_b32_e32 v1, 15, v200
	s_add_u32 s50, s33, s50
	v_ashrrev_i32_e32 v198, 6, v200
	s_addc_u32 s51, s37, 0
	v_lshlrev_b32_e32 v2, 7, v1
	s_lshl_b64 s[50:51], s[50:51], 15
	v_lshl_or_b32 v100, v198, 11, v2
	s_add_u32 s50, s52, s50
	v_ashrrev_i32_e32 v101, 31, v100
	v_bfe_u32 v199, v200, 4, 2
	s_addc_u32 s51, s54, s51
	v_lshlrev_b64 v[100:101], 1, v[100:101]
	v_lshl_add_u64 v[102:103], s[38:39], 0, v[100:101]
	v_lshlrev_b32_e32 v2, 4, v199
	v_lshl_add_u64 v[100:101], s[50:51], 0, v[100:101]
	v_lshl_add_u64 v[102:103], v[102:103], 0, v[2:3]
	v_lshl_add_u64 v[100:101], v[100:101], 0, v[2:3]
	global_load_dwordx4 v[120:123], v[102:103], off
	global_load_dwordx4 v[116:119], v[102:103], off offset:64
	global_load_dwordx4 v[128:131], v[100:101], off
	global_load_dwordx4 v[124:127], v[100:101], off offset:64
	global_load_dwordx4 v[108:111], v[102:103], off offset:128
	global_load_dwordx4 v[104:107], v[102:103], off offset:192
	global_load_dwordx4 v[112:115], v[100:101], off offset:128
	s_nop 0
	global_load_dwordx4 v[100:103], v[100:101], off offset:192
	s_cmp_lt_i32 s5, 4
	v_lshlrev_b32_e32 v164, 16, v160
	v_and_b32_e32 v165, 0xffff0000, v160
	v_lshlrev_b32_e32 v166, 16, v161
	v_and_b32_e32 v167, 0xffff0000, v161
	v_lshlrev_b32_e32 v168, 16, v162
	v_and_b32_e32 v169, 0xffff0000, v162
	v_lshlrev_b32_e32 v170, 16, v163
	v_and_b32_e32 v171, 0xffff0000, v163
	v_lshlrev_b32_e32 v160, 16, v156
	v_and_b32_e32 v161, 0xffff0000, v156
	v_lshlrev_b32_e32 v156, 16, v157
	v_and_b32_e32 v157, 0xffff0000, v157
	v_lshlrev_b32_e32 v162, 16, v158
	v_and_b32_e32 v163, 0xffff0000, v158
	v_lshlrev_b32_e32 v158, 16, v159
	v_and_b32_e32 v159, 0xffff0000, v159
	s_cbranch_scc1 .LBB0_765
	v_pk_mul_f32 v[174:175], v[152:153], v[164:165] op_sel:[1,1] op_sel_hi:[0,1]
	v_pk_mul_f32 v[178:179], v[154:155], v[166:167] op_sel:[1,1] op_sel_hi:[0,1]
	v_pk_mul_f32 v[182:183], v[148:149], v[168:169] op_sel:[1,1] op_sel_hi:[0,1]
	v_pk_mul_f32 v[186:187], v[150:151], v[170:171] op_sel:[1,1] op_sel_hi:[0,1]
	v_pk_mul_f32 v[190:191], v[136:137], v[160:161] op_sel:[1,1] op_sel_hi:[0,1]
	v_pk_mul_f32 v[194:195], v[138:139], v[156:157] op_sel:[1,1] op_sel_hi:[0,1]
	v_pk_mul_f32 v[204:205], v[132:133], v[162:163] op_sel:[1,1] op_sel_hi:[0,1]
	v_pk_mul_f32 v[208:209], v[134:135], v[158:159] op_sel:[1,1] op_sel_hi:[0,1]
	v_pk_mul_f32 v[172:173], v[152:153], v[164:165]
	v_pk_fma_f32 v[164:165], v[152:153], v[164:165], v[174:175] op_sel_hi:[1,0,1]
	v_pk_mul_f32 v[176:177], v[154:155], v[166:167]
	v_pk_fma_f32 v[166:167], v[154:155], v[166:167], v[178:179] op_sel_hi:[1,0,1]
	v_pk_mul_f32 v[180:181], v[148:149], v[168:169]
	v_pk_fma_f32 v[168:169], v[148:149], v[168:169], v[182:183] op_sel_hi:[1,0,1]
	v_pk_mul_f32 v[184:185], v[150:151], v[170:171]
	v_pk_fma_f32 v[170:171], v[150:151], v[170:171], v[186:187] op_sel_hi:[1,0,1]
	v_pk_mul_f32 v[188:189], v[136:137], v[160:161]
	v_pk_fma_f32 v[160:161], v[136:137], v[160:161], v[190:191] op_sel_hi:[1,0,1]
	v_pk_mul_f32 v[192:193], v[138:139], v[156:157]
	v_pk_fma_f32 v[156:157], v[138:139], v[156:157], v[194:195] op_sel_hi:[1,0,1]
	v_pk_mul_f32 v[202:203], v[132:133], v[162:163]
	v_pk_fma_f32 v[162:163], v[132:133], v[162:163], v[204:205] op_sel_hi:[1,0,1]
	v_pk_mul_f32 v[206:207], v[134:135], v[158:159]
	v_pk_fma_f32 v[158:159], v[134:135], v[158:159], v[208:209] op_sel_hi:[1,0,1]
	v_sub_f32_e32 v170, v184, v186
	v_sub_f32_e32 v158, v206, v208
	v_sub_f32_e32 v162, v202, v204
	v_sub_f32_e32 v168, v180, v182
	v_sub_f32_e32 v156, v192, v194
	v_sub_f32_e32 v166, v176, v178
	v_sub_f32_e32 v160, v188, v190
	v_sub_f32_e32 v164, v172, v174
; DEVI void ret_rot(const bf16x8 r0, const bf16x8 r1, const RetIn& in, bool lat, float scale, float (&o)[16]) {
;     float a[8], c[8]; unpack8(r0, a); unpack8(r1, c);
; #pragma unroll
;     for (int i = 0; i < 8; ++i) { o[i] = a[i]; o[8 + i] = c[i]; }
;     if (lat) {
; #pragma unroll
;         for (int q = 0; q < 4; ++q) { const f32x4 cs = (q == 0) ? in.cs0 : (q == 1) ? in.cs1 : (q == 2) ? in.cs2 : in.cs3;
;             const float x1 = o[4 * q], x2 = o[4 * q + 1], y1 = o[4 * q + 2], y2 = o[4 * q + 3];
;             o[4 * q] = x1 * cs[0] - x2 * cs[1]; o[4 * q + 1] = x1 * cs[1] + x2 * cs[0];
;             o[4 * q + 2] = y1 * cs[2] - y2 * cs[3]; o[4 * q + 3] = y1 * cs[3] + y2 * cs[2]; }
;     }
.LBB0_765:
	v_lshlrev_b32_e32 v195, 16, v141
	v_lshlrev_b32_e32 v192, 16, v140
	v_lshlrev_b32_e32 v191, 16, v143
	v_lshlrev_b32_e32 v188, 16, v142
	v_lshlrev_b32_e32 v187, 16, v145
	v_lshlrev_b32_e32 v184, 16, v144
	v_lshlrev_b32_e32 v183, 16, v147
	v_lshlrev_b32_e32 v180, 16, v146
	v_readlane_b32 s37, v254, 55
	v_pk_mov_b32 v[172:173], v[182:183], v[180:181] op_sel:[1,0]
	v_pk_mov_b32 v[174:175], v[186:187], v[184:185] op_sel:[1,0]
	v_pk_mov_b32 v[176:177], v[190:191], v[188:189] op_sel:[1,0]
	s_andn2_b64 vcc, exec, s[16:17]
	v_pk_mov_b32 v[178:179], v[194:195], v[192:193] op_sel:[1,0]
	s_cbranch_vccnz .LBB0_767
	v_and_b32_e32 v209, 0xffff0000, v141
	v_and_b32_e32 v208, 16, v140
	v_and_b32_e32 v141, 16, v141
	v_and_b32_e32 v140, 0xffff0000, v140
	v_mov_b32_e32 v194, v140
	v_mov_b32_e32 v212, v155
	v_mov_b32_e32 v213, v153
	v_pk_mov_b32 v[140:141], v[208:209], v[140:141] op_sel:[1,0]
	v_mov_b32_e32 v210, v154
	v_mov_b32_e32 v211, v152
	v_pk_mul_f32 v[140:141], v[212:213], v[140:141]
	v_and_b32_e32 v205, 0xffff0000, v143
	v_and_b32_e32 v204, 16, v142
	v_and_b32_e32 v143, 16, v143
	v_and_b32_e32 v142, 0xffff0000, v142
	v_pk_fma_f32 v[178:179], v[210:211], v[178:179], v[140:141] neg_lo:[0,0,1] neg_hi:[0,0,1]
	v_mov_b32_e32 v140, v152
	v_mov_b32_e32 v141, v155
	v_mov_b32_e32 v190, v142
	v_mov_b32_e32 v193, v209
	v_pk_mul_f32 v[140:141], v[140:141], v[194:195]
	v_mov_b32_e32 v152, v153
	v_mov_b32_e32 v153, v154
	v_mov_b32_e32 v154, v151
	v_mov_b32_e32 v155, v149
	v_pk_mov_b32 v[142:143], v[204:205], v[142:143] op_sel:[1,0]
	v_pk_fma_f32 v[140:141], v[152:153], v[192:193], v[140:141]
	v_mov_b32_e32 v152, v150
	v_mov_b32_e32 v153, v148
	v_pk_mul_f32 v[142:143], v[154:155], v[142:143]
	v_and_b32_e32 v207, 0xffff0000, v145
	v_and_b32_e32 v206, 16, v144
	v_and_b32_e32 v145, 16, v145
	v_and_b32_e32 v144, 0xffff0000, v144
	v_pk_fma_f32 v[176:177], v[152:153], v[176:177], v[142:143] neg_lo:[0,0,1] neg_hi:[0,0,1]
	v_mov_b32_e32 v142, v148
	v_mov_b32_e32 v143, v151
	v_mov_b32_e32 v189, v205
	v_mov_b32_e32 v186, v144
	v_pk_mul_f32 v[142:143], v[142:143], v[190:191]
	v_mov_b32_e32 v148, v149
	v_mov_b32_e32 v149, v150
	v_mov_b32_e32 v150, v139
	v_mov_b32_e32 v151, v137
	v_pk_mov_b32 v[144:145], v[206:207], v[144:145] op_sel:[1,0]
	v_pk_fma_f32 v[142:143], v[148:149], v[188:189], v[142:143]
	v_mov_b32_e32 v148, v138
	v_mov_b32_e32 v149, v136
	v_pk_mul_f32 v[144:145], v[150:151], v[144:145]
	v_and_b32_e32 v203, 0xffff0000, v147
	v_pk_fma_f32 v[174:175], v[148:149], v[174:175], v[144:145] neg_lo:[0,0,1] neg_hi:[0,0,1]
	v_mov_b32_e32 v144, v136
	v_mov_b32_e32 v145, v139
	v_and_b32_e32 v202, 16, v146
	v_and_b32_e32 v147, 16, v147
	v_and_b32_e32 v146, 0xffff0000, v146
	v_mov_b32_e32 v185, v207
	v_pk_mul_f32 v[144:145], v[144:145], v[186:187]
	v_mov_b32_e32 v136, v137
	v_mov_b32_e32 v137, v138
	v_mov_b32_e32 v182, v146
	v_pk_fma_f32 v[136:137], v[136:137], v[184:185], v[144:145]
	v_mov_b32_e32 v144, v135
	v_mov_b32_e32 v145, v133
	v_pk_mov_b32 v[146:147], v[202:203], v[146:147] op_sel:[1,0]
	v_mov_b32_e32 v138, v134
	v_mov_b32_e32 v139, v132
	v_pk_mul_f32 v[144:145], v[144:145], v[146:147]
	v_mov_b32_e32 v181, v203
	v_pk_fma_f32 v[172:173], v[138:139], v[172:173], v[144:145] neg_lo:[0,0,1] neg_hi:[0,0,1]
	v_mov_b32_e32 v138, v132
	v_mov_b32_e32 v139, v135
	v_pk_mul_f32 v[138:139], v[138:139], v[182:183]
	v_mov_b32_e32 v132, v133
	v_mov_b32_e32 v133, v134
	v_pk_fma_f32 v[132:133], v[132:133], v[180:181], v[138:139]
	s_branch .LBB0_768

; DEVI int chunk_row0(int b, int c) { return (c < 4) ? (NLAT + b * CL + c * 64) : (b * SEQ + (c - 4) * 64); }
; DEVI void ret_decays(int h, float& ldf, float& ldb) { ldf = log1pf(-exp2f(-(5.f + 2.f * h))); ldb = log1pf(-exp2f(-(6.f + 2.f * h))); }
; DEVI void scan_c_ret(const Params& p, int l, int b, int h, int c, const RetIn& in, char* smem) {
;     ...
;     const int row0 = chunk_row0(b, c); const bool lat = c >= 4;
;     const int tk = tid >> 3, kk16 = (tid & 7) * 16;
;     float ldf, ldb; ret_decays(h, ldf, ldb);
;     const bf16x8 gt0 = in.g0, gt1 = in.g1;
.LBB0_768:
	s_add_i32 s5, s4, 6
	v_cvt_f32_ubyte0_e32 v134, s5
	s_mov_b32 s33, 0x42fc0000
	v_cmp_lt_f32_e32 vcc, s33, v134
	s_and_b64 s[16:17], vcc, exec
	s_cselect_b32 s5, 0xffffffc0, 0
	v_cndmask_b32_e32 v135, 0, v226, vcc
	v_sub_f32_e32 v134, v135, v134
	v_exp_f32_e32 v134, v134
	s_mov_b32 s17, 0x3f2aaaab
	s_mov_b32 s50, 0x3f317218
	s_add_i32 s4, s4, 5
	v_ldexp_f32 v180, v134, s5
	v_sub_f32_e32 v138, 1.0, v180
	v_cvt_f64_f32_e32 v[134:135], v138
	v_frexp_exp_i32_f64_e32 v134, v[134:135]
	v_frexp_mant_f32_e32 v135, v138
	v_cmp_gt_f32_e32 vcc, s17, v135
	v_add_f32_e32 v144, -1.0, v138
	v_sub_f32_e64 v145, -v180, v144
	v_subbrev_co_u32_e32 v135, vcc, 0, v134, vcc
	v_cvt_f32_i32_e32 v134, v135
	v_sub_u32_e32 v135, 0, v135
	v_ldexp_f32 v139, v138, v135
	v_sub_f32_e32 v138, v144, v138
	v_add_f32_e32 v138, 1.0, v138
	v_add_f32_e32 v147, -1.0, v139
	v_add_f32_e32 v138, v145, v138
	v_ldexp_f32 v135, v138, v135
	v_add_f32_e32 v138, 1.0, v147
	v_sub_f32_e32 v138, v139, v138
	v_add_f32_e32 v148, v135, v138
	v_add_f32_e32 v138, 1.0, v139
	v_add_f32_e32 v144, -1.0, v138
	v_sub_f32_e32 v139, v139, v144
	v_add_f32_e32 v135, v135, v139
	v_add_f32_e32 v150, v138, v135
	v_rcp_f32_e32 v151, v150
	v_add_f32_e32 v139, v147, v148
	v_sub_f32_e32 v138, v150, v138
	v_sub_f32_e32 v135, v135, v138
	v_mul_f32_e32 v152, v139, v151
	v_mul_f32_e32 v144, v150, v152
	v_fma_f32 v146, v152, v150, -v144
	v_fmac_f32_e32 v146, v152, v135
	v_add_f32_e32 v138, v144, v146
	v_sub_f32_e32 v145, v139, v138
	v_sub_f32_e32 v147, v139, v147
	v_sub_f32_e32 v153, v148, v147
	v_pk_add_f32 v[148:149], v[138:139], v[144:145] neg_lo:[0,1] neg_hi:[0,1]
	v_mov_b32_e32 v147, v138
	v_pk_add_f32 v[138:139], v[148:149], v[146:147] neg_lo:[0,1] neg_hi:[0,1]
	v_cmp_nlt_f32_e32 vcc, 1.0, v180
	v_add_f32_e32 v139, v153, v139
	v_add_f32_e32 v148, v138, v139
	v_add_f32_e32 v139, v145, v148
	v_mul_f32_e32 v138, v151, v139
	v_add_f32_e32 v153, v152, v138
	v_sub_f32_e32 v144, v153, v152
	v_mul_f32_e32 v146, v150, v138
	v_sub_f32_e32 v152, v138, v144
	v_fma_f32 v144, v138, v150, -v146
	v_fmac_f32_e32 v144, v138, v135
	v_add_f32_e32 v138, v146, v144
	v_sub_f32_e32 v147, v139, v138
	v_sub_f32_e32 v135, v145, v139
	v_add_f32_e32 v135, v148, v135
	v_pk_add_f32 v[148:149], v[138:139], v[146:147] neg_lo:[0,1] neg_hi:[0,1]
	v_mov_b32_e32 v145, v138
	v_pk_add_f32 v[138:139], v[148:149], v[144:145] neg_lo:[0,1] neg_hi:[0,1]
	s_mov_b32 s16, 0x33800000
	v_add_f32_e32 v135, v135, v139
	v_add_f32_e32 v135, v138, v135
	v_add_f32_e32 v135, v147, v135
	v_mul_f32_e32 v135, v151, v135
	v_add_f32_e32 v138, v152, v135
	v_add_f32_e32 v144, v153, v138
	v_mul_f32_e32 v145, v144, v144
	v_fmamk_f32 v146, v145, 0x3e9b6dac, v224
	v_ldexp_f32 v139, v144, 1
	v_mul_f32_e32 v135, v144, v145
	v_fmaak_f32 v197, v145, v146, 0x3f2aaada
	v_sub_f32_e32 v144, v144, v153
	v_sub_f32_e32 v138, v138, v144
	v_pk_mul_f32 v[144:145], v[134:135], v[196:197]
	v_ldexp_f32 v146, v138, 1
	v_fma_f32 v138, v134, s50, -v144
	v_fmac_f32_e32 v138, 0xb102e308, v134
	v_pk_add_f32 v[134:135], v[144:145], v[138:139]
	v_cmp_gt_f32_e64 s[38:39], s16, v180
	v_sub_f32_e32 v139, v135, v139
	v_sub_f32_e32 v139, v145, v139
	v_add_f32_e32 v147, v146, v139
	v_mov_b32_e32 v146, v144
	v_pk_add_f32 v[144:145], v[134:135], v[144:145] neg_lo:[0,1] neg_hi:[0,1]
	v_pk_add_f32 v[148:149], v[134:135], v[146:147]
	v_mov_b32_e32 v139, v134
	v_mov_b32_e32 v145, v149
	v_pk_add_f32 v[150:151], v[138:139], v[144:145] neg_lo:[0,1] neg_hi:[0,1]
	v_pk_add_f32 v[138:139], v[138:139], v[144:145]
	v_mov_b32_e32 v154, v135
	v_pk_add_f32 v[144:145], v[138:139], v[134:135] op_sel:[1,0] op_sel_hi:[0,1] neg_lo:[0,1] neg_hi:[0,1]
	v_pk_add_f32 v[152:153], v[148:149], v[144:145] op_sel_hi:[1,0] neg_lo:[0,1] neg_hi:[0,1]
	v_mov_b32_e32 v148, v149
	v_mov_b32_e32 v149, v139
	v_mov_b32_e32 v155, v144
	v_pk_add_f32 v[144:145], v[148:149], v[154:155] neg_lo:[0,1] neg_hi:[0,1]
	v_mov_b32_e32 v146, v147
	v_mov_b32_e32 v147, v134
	v_pk_add_f32 v[134:135], v[146:147], v[144:145] neg_lo:[0,1] neg_hi:[0,1]
	v_mov_b32_e32 v152, v150
	v_pk_add_f32 v[144:145], v[152:153], v[134:135]
	v_mov_b32_e32 v151, v139
	v_pk_add_f32 v[146:147], v[144:145], v[144:145] op_sel:[0,1] op_sel_hi:[1,0]
	v_lshlrev_b32_e32 v182, 3, v199
	v_pk_add_f32 v[138:139], v[138:139], v[146:147] op_sel:[1,0] op_sel_hi:[0,1]
	v_mov_b32_e32 v145, v138
	v_pk_add_f32 v[148:149], v[144:145], v[150:151] neg_lo:[0,1] neg_hi:[0,1]
	v_mov_b32_e32 v135, v146
	v_sub_f32_e32 v139, v144, v148
	v_pk_add_f32 v[134:135], v[134:135], v[148:149] neg_lo:[0,1] neg_hi:[0,1]
	v_sub_f32_e32 v139, v150, v139
	v_add_f32_e32 v134, v134, v139
	v_add_f32_e32 v134, v134, v135
	v_add_f32_e32 v134, v138, v134
	v_cndmask_b32_e32 v134, v231, v134, vcc
	v_cmp_neq_f32_e32 vcc, 1.0, v180
	v_cvt_f32_ubyte0_e32 v135, s4
	s_nop 0
	v_cndmask_b32_e32 v134, v234, v134, vcc
	v_cmp_lt_f32_e32 vcc, s33, v135
	s_and_b64 s[4:5], vcc, exec
	s_cselect_b32 s4, 0xffffffc0, 0
	v_cndmask_b32_e32 v138, 0, v226, vcc
	v_sub_f32_e32 v135, v138, v135
	v_exp_f32_e32 v138, v135
	v_cndmask_b32_e64 v135, v134, -v180, s[38:39]
	v_readlane_b32 s33, v254, 48
	s_lshl_b32 s52, s29, 8
	v_ldexp_f32 v183, v138, s4
	v_sub_f32_e32 v134, 1.0, v183
	v_cvt_f64_f32_e32 v[138:139], v134
	v_frexp_exp_i32_f64_e32 v138, v[138:139]
	v_frexp_mant_f32_e32 v139, v134
	v_cmp_gt_f32_e32 vcc, s17, v139
	v_add_f32_e32 v145, -1.0, v134
	v_sub_f32_e64 v146, -v183, v145
	v_subbrev_co_u32_e32 v139, vcc, 0, v138, vcc
	v_cvt_f32_i32_e32 v138, v139
	v_sub_u32_e32 v139, 0, v139
	v_ldexp_f32 v144, v134, v139
	v_sub_f32_e32 v134, v145, v134
	v_add_f32_e32 v134, 1.0, v134
	v_add_f32_e32 v149, -1.0, v144
	v_add_f32_e32 v134, v146, v134
; DEVI void scan_c_ret(const Params& p, int l, int b, int h, int c, const RetIn& in, char* smem) {
;     ...
;     {   float qf[16], kf[16];
;         ret_rot(in.q0, in.q1, in, lat, 1.f, qf);
;         ret_rot(in.k0, in.k1, in, lat, 0.08838834764831845f, kf);
;         float t0[8], t1[8];
; #pragma unroll
;         for (int e = 0; e < 8; ++e) { t0[e] = qf[e]; t1[e] = qf[8 + e]; }
;         *(bf16x8*)(qs + tk * 136 + kk16) = pack8(t0); *(bf16x8*)(qs + tk * 136 + kk16 + 8) = pack8(t1);
; #pragma unroll
;         for (int e = 0; e < 8; ++e) { t0[e] = kf[e]; t1[e] = kf[8 + e]; }
;         *(bf16x8*)(ks + tk * 136 + kk16) = pack8(t0); *(bf16x8*)(ks + tk * 136 + kk16 + 8) = pack8(t1);
;         const bf16x8 v0 = in.v0, v1 = in.v1;
; #pragma unroll
;         for (int e = 0; e < 8; ++e) { vT[(kk16 + e) * 72 + tk] = (bf16_t)v0[e]; vT[(kk16 + 8 + e) * 72 + tk] = (bf16_t)v1[e]; }
;     }
;     __syncthreads();
	v_add_f32_e32 v145, 1.0, v144
	v_ldexp_f32 v134, v134, v139
	v_add_f32_e32 v139, 1.0, v149
	v_add_f32_e32 v146, -1.0, v145
	v_sub_f32_e32 v139, v144, v139
	v_sub_f32_e32 v144, v144, v146
	v_add_f32_e32 v139, v134, v139
	v_add_f32_e32 v134, v134, v144
	v_add_f32_e32 v152, v145, v134
	v_rcp_f32_e32 v153, v152
	v_sub_f32_e32 v144, v152, v145
	v_add_f32_e32 v145, v149, v139
	v_sub_f32_e32 v134, v134, v144
	v_mul_f32_e32 v154, v145, v153
	v_mul_f32_e32 v146, v152, v154
	v_fma_f32 v148, v154, v152, -v146
	v_fmac_f32_e32 v148, v154, v134
	v_add_f32_e32 v144, v146, v148
	v_sub_f32_e32 v147, v145, v144
	v_sub_f32_e32 v149, v145, v149
	v_sub_f32_e32 v139, v139, v149
	v_pk_add_f32 v[150:151], v[144:145], v[146:147] neg_lo:[0,1] neg_hi:[0,1]
	v_mov_b32_e32 v149, v144
	v_pk_add_f32 v[144:145], v[150:151], v[148:149] neg_lo:[0,1] neg_hi:[0,1]
	v_cmp_nlt_f32_e32 vcc, 1.0, v183
	v_add_f32_e32 v139, v139, v145
	v_add_f32_e32 v139, v144, v139
	v_add_f32_e32 v145, v147, v139
	v_mul_f32_e32 v144, v153, v145
	v_add_f32_e32 v155, v154, v144
	v_sub_f32_e32 v146, v155, v154
	v_mul_f32_e32 v148, v152, v144
	v_sub_f32_e32 v154, v144, v146
	v_fma_f32 v146, v144, v152, -v148
	v_fmac_f32_e32 v146, v144, v134
	v_add_f32_e32 v144, v148, v146
	v_sub_f32_e32 v149, v145, v144
	v_sub_f32_e32 v134, v147, v145
	v_pk_add_f32 v[150:151], v[144:145], v[148:149] neg_lo:[0,1] neg_hi:[0,1]
	v_mov_b32_e32 v147, v144
	v_add_f32_e32 v134, v139, v134
	v_pk_add_f32 v[144:145], v[150:151], v[146:147] neg_lo:[0,1] neg_hi:[0,1]
	s_mov_b32 s4, 0x3db504f3
	v_add_f32_e32 v134, v134, v145
	v_add_f32_e32 v134, v144, v134
	v_add_f32_e32 v134, v149, v134
	v_mul_f32_e32 v134, v153, v134
	v_add_f32_e32 v134, v154, v134
	v_add_f32_e32 v144, v155, v134
	v_mul_f32_e32 v146, v144, v144
	v_fmamk_f32 v147, v146, 0x3e9b6dac, v224
	v_mul_f32_e32 v139, v144, v146
	v_fmaak_f32 v197, v146, v147, 0x3f2aaada
	v_ldexp_f32 v145, v144, 1
	v_sub_f32_e32 v144, v144, v155
	v_pk_mul_f32 v[146:147], v[138:139], v[196:197]
	v_sub_f32_e32 v134, v134, v144
	v_fma_f32 v144, v138, s50, -v146
	v_fmac_f32_e32 v144, 0xb102e308, v138
	v_pk_add_f32 v[138:139], v[146:147], v[144:145]
	v_ldexp_f32 v134, v134, 1
	v_sub_f32_e32 v145, v139, v145
	v_sub_f32_e32 v145, v147, v145
	v_add_f32_e32 v149, v134, v145
	v_mov_b32_e32 v148, v146
	v_pk_add_f32 v[146:147], v[138:139], v[146:147] neg_lo:[0,1] neg_hi:[0,1]
	v_pk_add_f32 v[150:151], v[138:139], v[148:149]
	v_mov_b32_e32 v145, v138
	v_mov_b32_e32 v147, v151
	v_pk_add_f32 v[152:153], v[144:145], v[146:147] neg_lo:[0,1] neg_hi:[0,1]
	v_pk_add_f32 v[144:145], v[144:145], v[146:147]
	v_mov_b32_e32 v180, v139
	v_pk_add_f32 v[146:147], v[144:145], v[138:139] op_sel:[1,0] op_sel_hi:[0,1] neg_lo:[0,1] neg_hi:[0,1]
	v_pk_add_f32 v[154:155], v[150:151], v[146:147] op_sel_hi:[1,0] neg_lo:[0,1] neg_hi:[0,1]
	v_mov_b32_e32 v150, v151
	v_mov_b32_e32 v151, v145
	v_mov_b32_e32 v181, v146
	v_pk_add_f32 v[146:147], v[150:151], v[180:181] neg_lo:[0,1] neg_hi:[0,1]
	v_mov_b32_e32 v148, v149
	v_mov_b32_e32 v149, v138
	v_pk_add_f32 v[138:139], v[148:149], v[146:147] neg_lo:[0,1] neg_hi:[0,1]
	v_mov_b32_e32 v154, v152
	v_pk_add_f32 v[146:147], v[154:155], v[138:139]
	v_mov_b32_e32 v153, v145
	v_pk_add_f32 v[148:149], v[146:147], v[146:147] op_sel:[0,1] op_sel_hi:[1,0]
	s_movk_i32 s17, 0x110
	v_pk_add_f32 v[144:145], v[144:145], v[148:149] op_sel:[1,0] op_sel_hi:[0,1]
	v_mov_b32_e32 v147, v144
	v_pk_add_f32 v[150:151], v[146:147], v[152:153] neg_lo:[0,1] neg_hi:[0,1]
	v_mov_b32_e32 v139, v148
	v_sub_f32_e32 v134, v146, v150
	v_pk_add_f32 v[138:139], v[138:139], v[150:151] neg_lo:[0,1] neg_hi:[0,1]
	v_sub_f32_e32 v134, v152, v134
	v_add_f32_e32 v134, v138, v134
	v_add_f32_e32 v134, v134, v139
	v_add_f32_e32 v134, v144, v134
	v_cndmask_b32_e32 v134, v231, v134, vcc
	v_cmp_neq_f32_e32 vcc, 1.0, v183
	v_pk_mov_b32 v[144:145], v[178:179], v[140:141] op_sel:[1,0]
	v_mov_b32_e32 v179, v141
	v_cndmask_b32_e32 v139, v234, v134, vcc
	v_lshlrev_b32_e32 v134, 4, v200
	v_pk_mov_b32 v[140:141], v[176:177], v[142:143] op_sel:[1,0]
	v_and_b32_e32 v138, 0x70, v134
	v_ashrrev_i32_e32 v134, 3, v200
	v_pk_mul_f32 v[148:149], v[140:141], s[4:5] op_sel_hi:[1,0]
	v_pk_mov_b32 v[140:141], v[174:175], v[136:137] op_sel:[1,0]
	v_mov_b32_e32 v177, v143
	v_pk_mul_f32 v[152:153], v[140:141], s[4:5] op_sel_hi:[1,0]
	v_pk_mov_b32 v[140:141], v[172:173], v[132:133] op_sel:[1,0]
	v_mov_b32_e32 v173, v133
	v_mul_lo_u32 v133, v134, s17
	v_lshlrev_b32_e32 v132, 1, v138
	v_pk_mul_f32 v[154:155], v[140:141], s[4:5] op_sel_hi:[1,0]
	v_cvt_pk_bf16_f32 v140, v164, v165
	v_cvt_pk_bf16_f32 v141, v166, v167
	v_cvt_pk_bf16_f32 v142, v168, v169
	v_cvt_pk_bf16_f32 v143, v170, v171
	v_add3_u32 v133, 0, v133, v132
	v_pk_mul_f32 v[144:145], v[144:145], s[4:5] op_sel_hi:[1,0]
	v_pk_mul_f32 v[146:147], v[178:179], s[4:5] op_sel_hi:[1,0]
	v_pk_mul_f32 v[150:151], v[176:177], s[4:5] op_sel_hi:[1,0]
	v_mov_b32_e32 v175, v137
	ds_write_b128 v133, v[140:143] offset:32768
	v_cvt_pk_bf16_f32 v140, v160, v161
	v_cvt_pk_bf16_f32 v141, v156, v157
	v_cvt_pk_bf16_f32 v142, v162, v163
	v_cvt_pk_bf16_f32 v143, v158, v159
	v_pk_mul_f32 v[136:137], v[174:175], s[4:5] op_sel_hi:[1,0]
	v_pk_mul_f32 v[172:173], v[172:173], s[4:5] op_sel_hi:[1,0]
	ds_write_b128 v133, v[140:143] offset:32784
	v_cvt_pk_bf16_f32 v140, v144, v145
	v_cvt_pk_bf16_f32 v141, v146, v147
	v_cvt_pk_bf16_f32 v142, v148, v149
	v_cvt_pk_bf16_f32 v143, v150, v151
	ds_write_b128 v133, v[140:143] offset:50176
	v_cvt_pk_bf16_f32 v140, v152, v153
	v_cvt_pk_bf16_f32 v141, v136, v137
	v_cvt_pk_bf16_f32 v142, v154, v155
	v_cvt_pk_bf16_f32 v143, v172, v173
	v_mul_u32_u24_e32 v136, 0x48, v138
	ds_write_b128 v133, v[140:143] offset:50192
	v_lshlrev_b32_e32 v133, 1, v134
	v_lshlrev_b32_e32 v136, 1, v136
	v_add3_u32 v137, s33, v133, v136
	v_add3_u32 v133, s33, v136, v133
	ds_write_b16 v137, v92
	ds_write_b16 v133, v96 offset:1152
	ds_write_b16_d16_hi v137, v92 offset:144
	ds_write_b16_d16_hi v137, v96 offset:1296
	ds_write_b16 v137, v93 offset:288
	ds_write_b16 v133, v97 offset:1440
	ds_write_b16_d16_hi v137, v93 offset:432
	ds_write_b16_d16_hi v133, v97 offset:1584
	ds_write_b16 v137, v94 offset:576
	ds_write_b16 v133, v98 offset:1728
	ds_write_b16_d16_hi v137, v94 offset:720
	ds_write_b16_d16_hi v133, v98 offset:1872
	ds_write_b16 v137, v95 offset:864
	ds_write_b16 v133, v99 offset:2016
	ds_write_b16_d16_hi v137, v95 offset:1008
	ds_write_b16_d16_hi v133, v99 offset:2160
	v_lshlrev_b32_e32 v133, 4, v198
	v_and_b32_e32 v137, 48, v133
	v_lshlrev_b32_e32 v156, 1, v182
	v_or_b32_e32 v92, v137, v1
	v_add_u32_e32 v136, 0, v156
	v_mad_u32_u24 v154, v92, s17, v136
	s_waitcnt lgkmcnt(0)
	s_barrier
; DEVI unsigned cvt_pk(float lo, float hi) { f32x2 v = {lo, hi}; bf16x2_t b = __builtin_convertvector(v, bf16x2_t); return __builtin_bit_cast(unsigned, b); }
; DEVI void scan_c_ret(const Params& p, int l, int b, int h, int c, const RetIn& in, char* smem) {
;     ...
;     {   const int jf = wid & 3;
; #pragma unroll
;         for (int q = 0; q < 2; ++q) { const int iff = (wid >> 2) * 2 + q;
;             f32x4 a = {0.f, 0.f, 0.f, 0.f};
; #pragma unroll
;             for (int ksx = 0; ksx < 4; ++ksx) a = __builtin_amdgcn_mfma_f32_16x16x32_bf16(ldfrag(ks, 136, jf * 16, ksx * 32, fr, fq), ldfrag(qs, 136, iff * 16, ksx * 32, fr, fq), a, 0, 0, 0);
;             const int i = iff * 16 + fr, j0 = jf * 16 + fq * 4;
;             float r[4];
; #pragma unroll
;             for (int e = 0; e < 4; ++e) { const int j = j0 + e; r[e] = a[e] * ((j <= i) ? __expf(ldf * (float)(i - j)) : __expf(ldb * (float)(j - i))); }
;             *(u32x2*)(att + i * 72 + j0) = (u32x2){cvt_pk(r[0], r[1]), cvt_pk(r[2], r[3])};
;         }
;     }
;     __syncthreads();
	ds_read_b128 v[92:95], v154 offset:50176
	s_movk_i32 s4, 0xffe0
	v_and_or_b32 v155, v134, s4, v1
	v_mad_u64_u32 v[152:153], s[4:5], v155, s17, v[136:137]
	ds_read_b128 v[96:99], v152 offset:32768
	ds_read_b128 v[140:143], v154 offset:50240
	ds_read_b128 v[144:147], v152 offset:32832
	s_waitcnt lgkmcnt(2)
	v_mfma_f32_16x16x32_bf16 v[92:95], v[92:95], v[96:99], 0
	ds_read_b128 v[96:99], v154 offset:50304
	v_lshl_or_b32 v137, v199, 2, v137
	v_sub_u32_e32 v157, v137, v155
	v_sub_u32_e32 v158, 0, v157
	s_waitcnt lgkmcnt(1)
	v_mfma_f32_16x16x32_bf16 v[92:95], v[140:143], v[144:147], v[92:95]
	ds_read_b128 v[140:143], v154 offset:50368
	ds_read_b128 v[144:147], v152 offset:32896
	ds_read_b128 v[148:151], v152 offset:32960
	v_max_i32_e32 v157, v157, v158
	v_cvt_f32_u32_e32 v157, v157
	v_cmp_gt_f32_e32 vcc, s16, v183
	s_waitcnt lgkmcnt(1)
	v_mfma_f32_16x16x32_bf16 v[92:95], v[96:99], v[144:147], v[92:95]
	v_or_b32_e32 v158, 2, v137
	v_cndmask_b32_e64 v139, v139, -v183, vcc
	v_cmp_gt_i32_e32 vcc, v137, v155
	v_or_b32_e32 v159, 3, v137
	s_waitcnt lgkmcnt(0)
	v_mfma_f32_16x16x32_bf16 v[92:95], v[140:143], v[148:151], v[92:95]
	v_cndmask_b32_e32 v96, v139, v135, vcc
	v_mul_f32_e32 v96, v96, v157
	v_or_b32_e32 v157, 1, v137
	v_sub_u32_e32 v97, v157, v155
	v_sub_u32_e32 v98, v155, v157
	v_cmp_lt_i32_e32 vcc, v137, v155
	v_mul_f32_e32 v96, 0x3fb8aa3b, v96
	v_exp_f32_e32 v96, v96
	v_cndmask_b32_e32 v97, v97, v98, vcc
	v_cvt_f32_i32_e32 v97, v97
	v_cndmask_b32_e32 v98, v135, v139, vcc
	v_cmp_gt_i32_e32 vcc, v158, v155
	s_add_i32 s4, 0, 0x15000
	v_mul_f32_e32 v97, v98, v97
	v_sub_u32_e32 v98, v158, v155
	v_sub_u32_e32 v99, 0, v98
	v_max_i32_e32 v98, v98, v99
	v_cvt_f32_u32_e32 v98, v98
	v_cndmask_b32_e32 v99, v139, v135, vcc
	v_cmp_gt_i32_e32 vcc, v159, v155
	v_mul_f32_e32 v97, 0x3fb8aa3b, v97
	v_mul_f32_e32 v98, v99, v98
	v_sub_u32_e32 v99, v159, v155
	v_sub_u32_e32 v144, 0, v99
	v_max_i32_e32 v99, v99, v144
	v_cvt_f32_u32_e32 v99, v99
	v_cndmask_b32_e32 v144, v139, v135, vcc
	v_mul_f32_e32 v98, 0x3fb8aa3b, v98
	v_exp_f32_e32 v97, v97
	v_mul_f32_e32 v99, v144, v99
	v_mul_f32_e32 v99, 0x3fb8aa3b, v99
	v_exp_f32_e32 v98, v98
	v_exp_f32_e32 v99, v99
	v_pk_mul_f32 v[92:93], v[96:97], v[92:93]
	v_lshlrev_b32_e32 v153, 1, v137
	v_cvt_pk_bf16_f32 v92, v92, v93
	v_pk_mul_f32 v[94:95], v[98:99], v[94:95]
	v_or_b32_e32 v133, v133, v1
	v_cvt_pk_bf16_f32 v93, v94, v95
	v_mul_lo_u32 v94, v155, s91
	v_add3_u32 v153, s4, v153, v94
	ds_write_b64 v153, v[92:93]
	ds_read_b128 v[92:95], v154 offset:50176
	ds_read_b128 v[96:99], v154 offset:50240
	ds_read_b128 v[140:143], v152 offset:37120
	ds_read_b128 v[144:147], v152 offset:37184
	s_waitcnt lgkmcnt(1)
	v_mfma_f32_16x16x32_bf16 v[92:95], v[92:95], v[140:143], 0
	ds_read_b128 v[140:143], v154 offset:50304
	v_or_b32_e32 v155, 16, v155
	v_cmp_gt_i32_e32 vcc, v137, v155
	s_waitcnt lgkmcnt(1)
	v_mfma_f32_16x16x32_bf16 v[92:95], v[96:99], v[144:147], v[92:95]
	ds_read_b128 v[96:99], v154 offset:50368
	ds_read_b128 v[144:147], v152 offset:37248
	ds_read_b128 v[148:151], v152 offset:37312
	v_sub_u32_e32 v152, v137, v155
	v_sub_u32_e32 v154, 0, v152
	s_waitcnt lgkmcnt(1)
	v_mfma_f32_16x16x32_bf16 v[92:95], v[140:143], v[144:147], v[92:95]
	v_cndmask_b32_e32 v140, v139, v135, vcc
	v_sub_u32_e32 v141, v157, v155
	v_sub_u32_e32 v142, v155, v157
	v_cmp_lt_i32_e32 vcc, v137, v155
	v_max_i32_e32 v152, v152, v154
	v_cvt_f32_u32_e32 v152, v152
	v_cndmask_b32_e32 v137, v141, v142, vcc
	v_cvt_f32_i32_e32 v137, v137
	v_cndmask_b32_e32 v141, v135, v139, vcc
	v_cmp_gt_i32_e32 vcc, v158, v155
	v_mul_f32_e32 v140, v140, v152
	v_mul_f32_e32 v137, v141, v137
	v_sub_u32_e32 v141, v158, v155
	v_sub_u32_e32 v142, 0, v141
	v_max_i32_e32 v141, v141, v142
	v_cvt_f32_u32_e32 v142, v141
	v_mul_f32_e32 v137, 0x3fb8aa3b, v137
	v_exp_f32_e32 v141, v137
	v_cndmask_b32_e32 v137, v139, v135, vcc
	v_mul_f32_e32 v137, v137, v142
	v_sub_u32_e32 v142, v159, v155
	v_sub_u32_e32 v143, 0, v142
	v_max_i32_e32 v142, v142, v143
	v_cvt_f32_u32_e32 v143, v142
	v_mul_f32_e32 v137, 0x3fb8aa3b, v137
	v_cmp_gt_i32_e32 vcc, v159, v155
	v_exp_f32_e32 v142, v137
	v_mul_f32_e32 v140, 0x3fb8aa3b, v140
	v_cndmask_b32_e32 v137, v139, v135, vcc
	v_mul_f32_e32 v137, v137, v143
	v_mul_f32_e32 v137, 0x3fb8aa3b, v137
	v_exp_f32_e32 v140, v140
	v_exp_f32_e32 v143, v137
	s_waitcnt lgkmcnt(0)
	v_mfma_f32_16x16x32_bf16 v[92:95], v[96:99], v[148:151], v[92:95]
	v_mad_u32_u24 v137, v1, s17, v136
	v_mul_lo_u32 v133, v133, s91
	v_add3_u32 v133, s33, v133, v156
	v_sub_u32_e32 v136, 64, v1
	v_cvt_f32_ubyte0_e32 v136, v136
	s_nop 2
	v_pk_mul_f32 v[92:93], v[140:141], v[92:93]
	v_pk_mul_f32 v[94:95], v[142:143], v[94:95]
	v_cvt_pk_bf16_f32 v92, v92, v93
	v_cvt_pk_bf16_f32 v93, v94, v95
	ds_write_b64 v153, v[92:93] offset:2304
	s_waitcnt lgkmcnt(0)
	s_barrier
; DEVI void scan_c_ret(const Params& p, int l, int b, int h, int c, const RetIn& in, char* smem) {
;     ...
;     {   const int vf = wid;
;         const bf16x8 vt0 = ldfrag(vT, 72, vf * 16, 0, fr, fq), vt1 = ldfrag(vT, 72, vf * 16, 32, fr, fq);
; #pragma unroll
;         for (int iff = 0; iff < 4; ++iff) {
;             const int i = iff * 16 + fr;
;             const float sf = __expf(ldf * (float)(i + 1)), sb = __expf(ldb * (float)(64 - i));
;             f32x4 acc = {0.f, 0.f, 0.f, 0.f}, accf = {0.f, 0.f, 0.f, 0.f}, accb = {0.f, 0.f, 0.f, 0.f};
;             acc = __builtin_amdgcn_mfma_f32_16x16x32_bf16(vt0, ldfrag(att, 72, iff * 16, 0, fr, fq), acc, 0, 0, 0);
;             acc = __builtin_amdgcn_mfma_f32_16x16x32_bf16(vt1, ldfrag(att, 72, iff * 16, 32, fr, fq), acc, 0, 0, 0);
; #pragma unroll
;             for (int ksx = 0; ksx < 4; ++ksx) { const bf16x8 qv = ldfrag(qs, 136, iff * 16, ksx * 32, fr, fq);
;                 accf = __builtin_amdgcn_mfma_f32_16x16x32_bf16(sff[ksx], qv, accf, 0, 0, 0);
;                 accb = __builtin_amdgcn_mfma_f32_16x16x32_bf16(sbf[ksx], qv, accb, 0, 0, 0); }
;             *(f32x4*)(obuf + i * 128 + vf * 16 + fq * 4) = acc + sf * accf + sb * accb;
;         }
;     }
	ds_read_b128 v[92:95], v137 offset:32768
	ds_read_b128 v[96:99], v137 offset:32832
	s_waitcnt vmcnt(7) lgkmcnt(1)
	v_mfma_f32_16x16x32_bf16 v[140:143], v[120:123], v[92:95], 0
	v_mul_f32_e32 v136, v135, v136
	v_mul_f32_e32 v136, 0x3fb8aa3b, v136
	v_exp_f32_e32 v136, v136
	s_waitcnt vmcnt(5)
	v_mfma_f32_16x16x32_bf16 v[92:95], v[128:131], v[92:95], 0
	v_or_b32_e32 v157, 16, v1
	s_waitcnt lgkmcnt(0)
	v_mfma_f32_16x16x32_bf16 v[140:143], v[116:119], v[96:99], v[140:143]
	s_waitcnt vmcnt(4)
	v_mfma_f32_16x16x32_bf16 v[92:95], v[124:127], v[96:99], v[92:95]
	ds_read_b128 v[96:99], v137 offset:32896
	ds_read_b128 v[144:147], v133
	ds_read_b128 v[148:151], v133 offset:64
	ds_read_b128 v[152:155], v137 offset:32960
	v_lshlrev_b32_e32 v133, 6, v198
	s_waitcnt vmcnt(3) lgkmcnt(3)
	v_mfma_f32_16x16x32_bf16 v[140:143], v[108:111], v[96:99], v[140:143]
	v_add3_u32 v133, 0, v133, v2
	v_add_u32_e32 v2, 1, v1
	v_cvt_f32_ubyte0_e32 v2, v2
	s_waitcnt vmcnt(1)
	v_mfma_f32_16x16x32_bf16 v[92:95], v[112:115], v[96:99], v[92:95]
	v_mul_f32_e32 v2, v139, v2
	v_mul_f32_e32 v2, 0x3fb8aa3b, v2
	v_exp_f32_e32 v2, v2
	s_waitcnt lgkmcnt(0)
	v_mfma_f32_16x16x32_bf16 v[96:99], v[104:107], v[152:155], v[140:143]
	s_nop 2
	v_mul_u32_u24_e32 v140, 0x90, v1
	v_add3_u32 v156, s4, v140, v156
	ds_read_b128 v[140:143], v156
	s_waitcnt vmcnt(0)
	v_mfma_f32_16x16x32_bf16 v[92:95], v[100:103], v[152:155], v[92:95]
	ds_read_b128 v[152:155], v156 offset:64
	s_mov_b64 s[4:5], 0x43caec00
	s_waitcnt lgkmcnt(1)
	v_mfma_f32_16x16x32_bf16 v[140:143], v[144:147], v[140:143], 0
	s_waitcnt lgkmcnt(0)
	v_mfma_f32_16x16x32_bf16 v[140:143], v[148:151], v[152:155], v[140:143]
	s_nop 7
	v_pk_fma_f32 v[98:99], v[2:3], v[98:99], v[142:143] op_sel_hi:[0,1,1]
	v_pk_fma_f32 v[96:97], v[2:3], v[96:97], v[140:141] op_sel_hi:[0,1,1]
	v_pk_fma_f32 v[92:93], v[136:137], v[92:93], v[96:97] op_sel_hi:[0,1,1]
	v_pk_fma_f32 v[94:95], v[136:137], v[94:95], v[98:99] op_sel_hi:[0,1,1]
	v_lshl_add_u32 v2, v1, 9, v133
	ds_write_b128 v2, v[92:95]
	ds_read_b128 v[92:95], v137 offset:37120
	ds_read_b128 v[96:99], v137 offset:37184
	s_waitcnt lgkmcnt(1)
	v_mfma_f32_16x16x32_bf16 v[140:143], v[120:123], v[92:95], 0
	v_add_u32_e32 v2, 17, v1
	v_cvt_f32_ubyte0_e32 v2, v2
	v_sub_u32_e32 v136, 64, v157
	v_mfma_f32_16x16x32_bf16 v[92:95], v[128:131], v[92:95], 0
	v_mul_f32_e32 v2, v139, v2
	v_cvt_f32_ubyte0_e32 v136, v136
	v_mul_f32_e32 v2, 0x3fb8aa3b, v2
	s_waitcnt lgkmcnt(0)
	v_mfma_f32_16x16x32_bf16 v[140:143], v[116:119], v[96:99], v[140:143]
	v_mul_f32_e32 v136, v135, v136
	v_mul_f32_e32 v136, 0x3fb8aa3b, v136
	v_exp_f32_e32 v2, v2
	v_mfma_f32_16x16x32_bf16 v[92:95], v[124:127], v[96:99], v[92:95]
	ds_read_b128 v[96:99], v137 offset:37248
	ds_read_b128 v[152:155], v137 offset:37312
	v_exp_f32_e32 v136, v136
	s_waitcnt lgkmcnt(1)
	v_mfma_f32_16x16x32_bf16 v[140:143], v[108:111], v[96:99], v[140:143]
	v_mfma_f32_16x16x32_bf16 v[92:95], v[112:115], v[96:99], v[92:95]
	s_waitcnt lgkmcnt(0)
	v_mfma_f32_16x16x32_bf16 v[96:99], v[104:107], v[152:155], v[140:143]
	s_nop 4
	ds_read_b128 v[140:143], v156 offset:2304
	v_mfma_f32_16x16x32_bf16 v[92:95], v[100:103], v[152:155], v[92:95]
	ds_read_b128 v[152:155], v156 offset:2368
	s_waitcnt lgkmcnt(1)
	v_mfma_f32_16x16x32_bf16 v[140:143], v[144:147], v[140:143], 0
	s_waitcnt lgkmcnt(0)
	v_mfma_f32_16x16x32_bf16 v[140:143], v[148:151], v[152:155], v[140:143]
	s_nop 7
	v_pk_fma_f32 v[98:99], v[2:3], v[98:99], v[142:143] op_sel_hi:[0,1,1]
	v_pk_fma_f32 v[96:97], v[2:3], v[96:97], v[140:141] op_sel_hi:[0,1,1]
	v_pk_fma_f32 v[92:93], v[136:137], v[92:93], v[96:97] op_sel_hi:[0,1,1]
	v_pk_fma_f32 v[94:95], v[136:137], v[94:95], v[98:99] op_sel_hi:[0,1,1]
	v_lshl_add_u32 v2, v157, 9, v133
	ds_write_b128 v2, v[92:95]
	ds_read_b128 v[92:95], v137 offset:41472
	ds_read_b128 v[96:99], v137 offset:41536
	s_waitcnt lgkmcnt(1)
	v_mfma_f32_16x16x32_bf16 v[140:143], v[120:123], v[92:95], 0
	v_or_b32_e32 v157, 32, v1
	v_add_u32_e32 v2, 33, v1
	v_cvt_f32_ubyte0_e32 v2, v2
	v_mfma_f32_16x16x32_bf16 v[92:95], v[128:131], v[92:95], 0
	v_sub_u32_e32 v136, 64, v157
	v_mul_f32_e32 v2, v139, v2
	v_cvt_f32_ubyte0_e32 v136, v136
	s_waitcnt lgkmcnt(0)
	v_mfma_f32_16x16x32_bf16 v[140:143], v[116:119], v[96:99], v[140:143]
	v_mul_f32_e32 v2, 0x3fb8aa3b, v2
	v_mul_f32_e32 v136, v135, v136
	v_mul_f32_e32 v136, 0x3fb8aa3b, v136
	v_mfma_f32_16x16x32_bf16 v[92:95], v[124:127], v[96:99], v[92:95]
	ds_read_b128 v[96:99], v137 offset:41600
	ds_read_b128 v[152:155], v137 offset:41664
	v_exp_f32_e32 v2, v2
	v_exp_f32_e32 v136, v136
	s_waitcnt lgkmcnt(1)
	v_mfma_f32_16x16x32_bf16 v[140:143], v[108:111], v[96:99], v[140:143]
	v_mfma_f32_16x16x32_bf16 v[92:95], v[112:115], v[96:99], v[92:95]
	s_waitcnt lgkmcnt(0)
	v_mfma_f32_16x16x32_bf16 v[96:99], v[104:107], v[152:155], v[140:143]
	s_nop 4
	ds_read_b128 v[140:143], v156 offset:4608
	v_mfma_f32_16x16x32_bf16 v[92:95], v[100:103], v[152:155], v[92:95]
	ds_read_b128 v[152:155], v156 offset:4672
	s_waitcnt lgkmcnt(1)
	v_mfma_f32_16x16x32_bf16 v[140:143], v[144:147], v[140:143], 0
	s_waitcnt lgkmcnt(0)
	v_mfma_f32_16x16x32_bf16 v[140:143], v[148:151], v[152:155], v[140:143]
	s_nop 7
	v_pk_fma_f32 v[98:99], v[2:3], v[98:99], v[142:143] op_sel_hi:[0,1,1]
	v_pk_fma_f32 v[96:97], v[2:3], v[96:97], v[140:141] op_sel_hi:[0,1,1]
	v_pk_fma_f32 v[92:93], v[136:137], v[92:93], v[96:97] op_sel_hi:[0,1,1]
	v_pk_fma_f32 v[94:95], v[136:137], v[94:95], v[98:99] op_sel_hi:[0,1,1]
	v_lshl_add_u32 v2, v157, 9, v133
	ds_write_b128 v2, v[92:95]
	ds_read_b128 v[92:95], v137 offset:45824
	ds_read_b128 v[96:99], v137 offset:45888
	s_waitcnt lgkmcnt(1)
; DEVI float silu_f(float x) { return x * __builtin_amdgcn_rcpf(1.f + __expf(-x)); }
; DEVI void scan_c_tail(const float* o, int tid, const bf16x8 g0, const bf16x8 g1, int row0, bf16_t* ymix, int ycol) {
;     ...
;     for (int i = 0; i < 8; ++i) { y0[i] = ov[i] * rstd * silu_f(ga[i]); y1[i] = ov[8 + i] * rstd * silu_f(gb[i]); }
; DEVI void scan_c_ret(const Params& p, int l, int b, int h, int c, const RetIn& in, char* smem) {
;     ...
;         for (int iff = 0; iff < 4; ++iff) {
;             const int i = iff * 16 + fr;
;             const float sf = __expf(ldf * (float)(i + 1)), sb = __expf(ldb * (float)(64 - i));
;             f32x4 acc = {0.f, 0.f, 0.f, 0.f}, accf = {0.f, 0.f, 0.f, 0.f}, accb = {0.f, 0.f, 0.f, 0.f};
;             acc = __builtin_amdgcn_mfma_f32_16x16x32_bf16(vt0, ldfrag(att, 72, iff * 16, 0, fr, fq), acc, 0, 0, 0);
;             acc = __builtin_amdgcn_mfma_f32_16x16x32_bf16(vt1, ldfrag(att, 72, iff * 16, 32, fr, fq), acc, 0, 0, 0);
; #pragma unroll
;             for (int ksx = 0; ksx < 4; ++ksx) { const bf16x8 qv = ldfrag(qs, 136, iff * 16, ksx * 32, fr, fq);
;                 accf = __builtin_amdgcn_mfma_f32_16x16x32_bf16(sff[ksx], qv, accf, 0, 0, 0);
;                 accb = __builtin_amdgcn_mfma_f32_16x16x32_bf16(sbf[ksx], qv, accb, 0, 0, 0); }
;             *(f32x4*)(obuf + i * 128 + vf * 16 + fq * 4) = acc + sf * accf + sb * accb;
;         }
;     }
;     __syncthreads();
	v_mfma_f32_16x16x32_bf16 v[120:123], v[120:123], v[92:95], 0
	v_mfma_f32_16x16x32_bf16 v[92:95], v[128:131], v[92:95], 0
	s_waitcnt lgkmcnt(0)
	v_mfma_f32_16x16x32_bf16 v[116:119], v[116:119], v[96:99], v[120:123]
	v_mfma_f32_16x16x32_bf16 v[92:95], v[124:127], v[96:99], v[92:95]
	ds_read_b128 v[96:99], v137 offset:45952
	s_nop 2
	ds_read_b128 v[120:123], v137 offset:46016
	s_waitcnt lgkmcnt(1)
	v_mfma_f32_16x16x32_bf16 v[108:111], v[108:111], v[96:99], v[116:119]
	s_nop 2
	v_or_b32_e32 v116, 48, v1
	v_mfma_f32_16x16x32_bf16 v[92:95], v[112:115], v[96:99], v[92:95]
	v_add_u32_e32 v1, 49, v1
	v_cvt_f32_ubyte0_e32 v1, v1
	v_sub_u32_e32 v2, 64, v116
	s_waitcnt lgkmcnt(0)
	v_mfma_f32_16x16x32_bf16 v[96:99], v[104:107], v[120:123], v[108:111]
	ds_read_b128 v[104:107], v156 offset:6912
	v_mul_f32_e32 v1, v139, v1
	v_cvt_f32_ubyte0_e32 v2, v2
	v_mfma_f32_16x16x32_bf16 v[92:95], v[100:103], v[120:123], v[92:95]
	ds_read_b128 v[100:103], v156 offset:6976
	v_mul_f32_e32 v1, 0x3fb8aa3b, v1
	v_mul_f32_e32 v2, v135, v2
	s_waitcnt lgkmcnt(1)
	v_mfma_f32_16x16x32_bf16 v[104:107], v[144:147], v[104:107], 0
	v_mul_f32_e32 v108, 0x3fb8aa3b, v2
	v_exp_f32_e32 v2, v1
	v_exp_f32_e32 v108, v108
	s_waitcnt lgkmcnt(0)
	v_mfma_f32_16x16x32_bf16 v[100:103], v[148:151], v[100:103], v[104:107]
	v_lshl_add_u32 v1, v116, 9, v133
	v_lshlrev_b32_e32 v112, 16, v52
	v_and_b32_e32 v113, 0xffff0000, v52
	v_mul_f32_e32 v52, 0xbfb8aa3b, v112
	v_exp_f32_e32 v52, v52
	s_nop 2
	v_pk_fma_f32 v[98:99], v[2:3], v[98:99], v[102:103] op_sel_hi:[0,1,1]
	v_pk_fma_f32 v[96:97], v[2:3], v[96:97], v[100:101] op_sel_hi:[0,1,1]
	v_pk_fma_f32 v[92:93], v[108:109], v[92:93], v[96:97] op_sel_hi:[0,1,1]
	v_pk_fma_f32 v[94:95], v[108:109], v[94:95], v[98:99] op_sel_hi:[0,1,1]
	ds_write_b128 v1, v[92:95]
	v_lshlrev_b32_e32 v1, 9, v134
	v_lshlrev_b32_e32 v2, 2, v138
	v_add3_u32 v1, 0, v1, v2
	s_waitcnt lgkmcnt(0)
	s_barrier
; DEVI float silu_f(float x) { return x * __builtin_amdgcn_rcpf(1.f + __expf(-x)); }
; DEVI void scan_c_tail(const float* o, int tid, const bf16x8 g0, const bf16x8 g1, int row0, bf16_t* ymix, int ycol) {
;     const int tk = tid >> 3, v16 = (tid & 7) * 16;
;     float ov[16]; float ss = 0.f;
; #pragma unroll
;     for (int q = 0; q < 4; ++q) { const f32x4 t = *(const f32x4*)(o + tk * 128 + v16 + q * 4); ov[q * 4] = t[0]; ov[q * 4 + 1] = t[1]; ov[q * 4 + 2] = t[2]; ov[q * 4 + 3] = t[3]; }
; #pragma unroll
;     for (int i = 0; i < 16; ++i) ss += ov[i] * ov[i];
;     ss += __shfl_xor(ss, 1); ss += __shfl_xor(ss, 2); ss += __shfl_xor(ss, 4);
;     const float rstd = rsqrtf(ss * (1.f / 128.f) + EPS);
;     float ga[8], gb[8]; unpack8(g0, ga); unpack8(g1, gb);
;     float y0[8], y1[8];
; #pragma unroll
;     for (int i = 0; i < 8; ++i) { y0[i] = ov[i] * rstd * silu_f(ga[i]); y1[i] = ov[8 + i] * rstd * silu_f(gb[i]); }
;     *(bf16x8*)(ymix + (size_t)(row0 + tk) * DM + ycol + v16) = pack8(y0);
;     *(bf16x8*)(ymix + (size_t)(row0 + tk) * DM + ycol + v16 + 8) = pack8(y1);
; }
	ds_read_b128 v[92:95], v1
	ds_read_b128 v[96:99], v1 offset:16
	ds_read_b128 v[100:103], v1 offset:32
	ds_read_b128 v[104:107], v1 offset:48
	v_xor_b32_e32 v2, 1, v227
	s_waitcnt lgkmcnt(3)
	v_mul_f32_e32 v1, v93, v93
	v_fmac_f32_e32 v1, v92, v92
	v_fmac_f32_e32 v1, v94, v94
	v_fmac_f32_e32 v1, v95, v95
	s_waitcnt lgkmcnt(2)
	v_fmac_f32_e32 v1, v96, v96
	v_fmac_f32_e32 v1, v97, v97
	v_fmac_f32_e32 v1, v98, v98
	v_fmac_f32_e32 v1, v99, v99
	s_waitcnt lgkmcnt(1)
	v_pk_mul_f32 v[110:111], v[100:101], v[100:101]
	v_pk_mul_f32 v[108:109], v[102:103], v[102:103]
	v_add_f32_e32 v1, v110, v1
	v_add_f32_e32 v1, v111, v1
	v_add_f32_e32 v1, v108, v1
	v_add_f32_e32 v1, v109, v1
	s_waitcnt lgkmcnt(0)
	v_pk_mul_f32 v[110:111], v[104:105], v[104:105]
	v_pk_mul_f32 v[108:109], v[106:107], v[106:107]
	v_add_f32_e32 v1, v110, v1
	v_add_f32_e32 v1, v111, v1
	v_add_f32_e32 v1, v108, v1
	v_and_b32_e32 v108, 64, v227
	v_add_u32_e32 v108, 64, v108
	v_cmp_lt_i32_e32 vcc, v2, v108
	v_add_f32_e32 v1, v109, v1
	v_and_b32_e32 v109, 0xffff0000, v56
	v_cndmask_b32_e32 v2, v227, v2, vcc
	v_lshlrev_b32_e32 v2, 2, v2
	ds_bpermute_b32 v2, v2, v1
	v_mov_b32_e32 v133, v3
	s_waitcnt lgkmcnt(0)
	v_add_f32_e32 v1, v1, v2
	v_xor_b32_e32 v2, 2, v227
	v_cmp_lt_i32_e32 vcc, v2, v108
	s_nop 1
	v_cndmask_b32_e32 v2, v227, v2, vcc
	v_lshlrev_b32_e32 v2, 2, v2
	ds_bpermute_b32 v2, v2, v1
	s_waitcnt lgkmcnt(0)
	v_add_f32_e32 v1, v1, v2
	v_xor_b32_e32 v2, 4, v227
	v_cmp_lt_i32_e32 vcc, v2, v108
	v_lshlrev_b32_e32 v108, 16, v56
	v_mul_f32_e32 v56, 0xbfb8aa3b, v109
	v_cndmask_b32_e32 v2, v227, v2, vcc
	v_lshlrev_b32_e32 v2, 2, v2
	ds_bpermute_b32 v2, v2, v1
	v_exp_f32_e32 v56, v56
	s_waitcnt lgkmcnt(0)
	v_add_f32_e32 v1, v1, v2
	v_fmamk_f32 v1, v1, 0x3c000000, v223
	v_mul_f32_e32 v2, 0x4b800000, v1
	v_cmp_gt_f32_e32 vcc, s97, v1
	s_nop 1
	v_cndmask_b32_e32 v1, v1, v2, vcc
	v_rsq_f32_e32 v1, v1
	s_nop 0
	v_mul_f32_e32 v2, 0x45800000, v1
	v_cndmask_b32_e32 v2, v1, v2, vcc
	v_mul_f32_e32 v1, 0xbfb8aa3b, v108
	v_exp_f32_e32 v1, v1
	v_pk_mul_f32 v[92:93], v[92:93], v[2:3] op_sel_hi:[1,0]
	v_pk_mul_f32 v[100:101], v[100:101], v[2:3] op_sel_hi:[1,0]
	v_pk_mul_f32 v[94:95], v[94:95], v[2:3] op_sel_hi:[1,0]
	v_add_f32_e32 v1, 1.0, v1
	v_rcp_f32_e32 v110, v1
	v_add_f32_e32 v1, 1.0, v56
	v_mul_f32_e32 v56, 0xbfb8aa3b, v113
	v_exp_f32_e32 v56, v56
	v_rcp_f32_e32 v111, v1
	v_add_f32_e32 v1, 1.0, v52
	v_rcp_f32_e32 v114, v1
	v_add_f32_e32 v1, 1.0, v56
	v_rcp_f32_e32 v115, v1
	v_lshlrev_b32_e32 v56, 16, v57
	v_pk_mul_f32 v[108:109], v[110:111], v[108:109]
	v_mul_f32_e32 v1, 0xbfb8aa3b, v56
	v_and_b32_e32 v57, 0xffff0000, v57
	v_pk_mul_f32 v[92:93], v[108:109], v[92:93]
	v_pk_mul_f32 v[108:109], v[114:115], v[112:113]
	v_exp_f32_e32 v1, v1
	v_mul_f32_e32 v52, 0xbfb8aa3b, v57
	v_pk_mul_f32 v[100:101], v[108:109], v[100:101]
	v_exp_f32_e32 v108, v52
	v_add_f32_e32 v1, 1.0, v1
	v_rcp_f32_e32 v52, v1
	v_and_b32_e32 v109, 0xffff0000, v53
	v_add_f32_e32 v1, 1.0, v108
	v_lshlrev_b32_e32 v108, 16, v53
	v_mul_f32_e32 v53, 0xbfb8aa3b, v108
	v_exp_f32_e32 v110, v53
	v_mul_f32_e32 v53, 0xbfb8aa3b, v109
	v_exp_f32_e32 v111, v53
	v_rcp_f32_e32 v53, v1
	v_add_f32_e32 v1, 1.0, v110
	v_rcp_f32_e32 v110, v1
	v_add_f32_e32 v1, 1.0, v111
	v_rcp_f32_e32 v111, v1
	v_pk_mul_f32 v[52:53], v[52:53], v[56:57]
	v_pk_mul_f32 v[96:97], v[96:97], v[2:3] op_sel_hi:[1,0]
	v_pk_mul_f32 v[56:57], v[52:53], v[94:95]
	v_pk_mul_f32 v[52:53], v[102:103], v[2:3] op_sel_hi:[1,0]
	v_pk_mul_f32 v[94:95], v[110:111], v[108:109]
	v_lshlrev_b32_e32 v108, 16, v54
	v_pk_mul_f32 v[94:95], v[94:95], v[52:53]
	v_lshlrev_b32_e32 v52, 16, v58
	v_mul_f32_e32 v1, 0xbfb8aa3b, v52
	v_and_b32_e32 v53, 0xffff0000, v58
	v_exp_f32_e32 v1, v1
	v_mul_f32_e32 v58, 0xbfb8aa3b, v53
	v_exp_f32_e32 v58, v58
	v_and_b32_e32 v109, 0xffff0000, v54
	v_add_f32_e32 v1, 1.0, v1
	v_mul_f32_e32 v54, 0xbfb8aa3b, v108
	v_rcp_f32_e32 v102, v1
	v_add_f32_e32 v1, 1.0, v58
	v_exp_f32_e32 v54, v54
	v_mul_f32_e32 v58, 0xbfb8aa3b, v109
	v_exp_f32_e32 v58, v58
	v_rcp_f32_e32 v103, v1
	v_add_f32_e32 v1, 1.0, v54
	v_rcp_f32_e32 v110, v1
	v_add_f32_e32 v1, 1.0, v58
	v_rcp_f32_e32 v111, v1
	v_pk_mul_f32 v[52:53], v[102:103], v[52:53]
	v_pk_mul_f32 v[102:103], v[110:111], v[108:109]
	v_pk_mul_f32 v[96:97], v[52:53], v[96:97]
	v_pk_mul_f32 v[52:53], v[104:105], v[2:3] op_sel_hi:[1,0]
	s_nop 0
	v_pk_mul_f32 v[102:103], v[102:103], v[52:53]
	v_lshlrev_b32_e32 v52, 16, v59
	v_mul_f32_e32 v1, 0xbfb8aa3b, v52
	v_and_b32_e32 v53, 0xffff0000, v59
	v_exp_f32_e32 v1, v1
	v_mul_f32_e32 v54, 0xbfb8aa3b, v53
	v_exp_f32_e32 v104, v54
	v_pk_mul_f32 v[58:59], v[98:99], v[2:3] op_sel_hi:[1,0]
	v_lshlrev_b32_e32 v98, 16, v55
	v_add_f32_e32 v1, 1.0, v1
	v_and_b32_e32 v99, 0xffff0000, v55
	v_mul_f32_e32 v55, 0xbfb8aa3b, v98
	v_rcp_f32_e32 v54, v1
	v_add_f32_e32 v1, 1.0, v104
	v_exp_f32_e32 v104, v55
	v_mul_f32_e32 v55, 0xbfb8aa3b, v99
	v_exp_f32_e32 v105, v55
	v_rcp_f32_e32 v55, v1
	v_add_f32_e32 v1, 1.0, v104
	v_rcp_f32_e32 v104, v1
	v_add_f32_e32 v1, 1.0, v105
	v_rcp_f32_e32 v105, v1
	v_pk_mul_f32 v[52:53], v[54:55], v[52:53]
	v_pk_mul_f32 v[54:55], v[104:105], v[98:99]
	v_pk_mul_f32 v[58:59], v[52:53], v[58:59]
	v_pk_mul_f32 v[52:53], v[106:107], v[2:3] op_sel_hi:[1,0]
	s_nop 0
	v_pk_mul_f32 v[98:99], v[54:55], v[52:53]
	v_cvt_pk_bf16_f32 v53, v56, v57
	v_add_u32_e32 v56, s28, v134
	v_ashrrev_i32_e32 v57, 31, v56
	v_lshlrev_b64 v[56:57], 12, v[56:57]
	v_lshl_add_u64 v[56:57], s[82:83], 0, v[56:57]
	v_lshl_add_u64 v[56:57], v[56:57], 0, s[52:53]
	v_lshl_add_u64 v[56:57], v[56:57], 0, v[132:133]
	v_cvt_pk_bf16_f32 v55, v58, v59
	v_lshl_add_u64 v[58:59], v[56:57], 0, s[4:5]
	s_mov_b32 s4, 0x43cae000
	v_add_co_u32_e32 v56, vcc, s4, v56
	v_cvt_pk_bf16_f32 v52, v92, v93
	v_cvt_pk_bf16_f32 v54, v96, v97
	v_addc_co_u32_e32 v57, vcc, 0, v57, vcc
	global_store_dwordx4 v[56:57], v[52:55], off offset:3072
	s_mov_b64 s[28:29], -1
	s_and_b64 vcc, s[44:45], exec
	v_cvt_pk_bf16_f32 v52, v100, v101
	v_cvt_pk_bf16_f32 v53, v94, v95
	v_cvt_pk_bf16_f32 v54, v102, v103
	v_cvt_pk_bf16_f32 v55, v98, v99
	global_store_dwordx4 v[58:59], v[52:55], off offset:16
	s_barrier
	s_cbranch_vccz .LBB0_770
	s_ashr_i32 s16, s25, 12
	s_lshl_b64 s[4:5], s[42:43], 23
	s_add_u32 s17, s37, s4
	s_addc_u32 s25, s78, s5
	s_lshl_b32 s4, s7, 8
	s_lshl_b32 s5, s16, 7
	s_add_i32 s4, s4, s5
	s_ashr_i32 s5, s4, 31
	s_lshl_b64 s[4:5], s[4:5], 11
	s_add_u32 s16, s17, s4
	s_addc_u32 s17, s25, s5
	s_mov_b64 s[28:29], 0
